# v30 + ssd_states publishes (dt,acs) per position and ssd_out loads them instead of recomputing; ssd_states dt inputs fetched at item top
# speedup vs baseline: 1.0062x; 1.0062x over previous
.LBB0_427:
	s_ashr_i32 s24, s47, 3
	s_and_b32 s10, s47, 7
	s_lshl_b32 s25, s24, 6
	s_lshl_b32 s0, s10, 3
	s_add_i32 s0, s0, s34
	s_mov_b32 s1, 0
	s_lshl_b64 s[0:1], s[0:1], 2
	v_or_b32_e32 v166, s25, v120
	v_mov_b32_e32 v167, 0
	v_lshlrev_b64 v[166:167], 10, v[166:167]
	s_add_u32 s2, s28, s0
	s_addc_u32 s3, s29, s1
	v_lshl_add_u64 v[166:167], s[14:15], 0, v[166:167]
	v_lshl_add_u64 v[166:167], v[166:167], 0, s[0:1]
	s_add_u32 s0, s30, s0
	s_addc_u32 s1, s31, s1
	global_load_dword v162, v[166:167], off
	global_load_dword v163, v33, s[2:3]
	global_load_dword v164, v33, s[0:1]
	v_lshl_or_b32 v10, s10, 7, v121
	v_add_u32_e32 v98, s25, v131
	v_add_u32_e32 v0, -3, v98
	v_mov_b64_e32 v[82:83], s[12:13]
	v_lshlrev_b32_e32 v32, 1, v10
	v_lshlrev_b32_e32 v10, 2, v10
	v_mov_b32_e32 v11, v33
	s_and_b32 s48, s25, 0xfc0
	v_mad_i64_i32 v[0:1], s[0:1], v0, s96, v[82:83]
	v_lshl_add_u64 v[84:85], s[20:21], 0, v[10:11]
	s_movk_i32 s8, 0x7000
	v_lshl_add_u64 v[4:5], v[0:1], 0, v[32:33]
	v_add_u32_e32 v99, s48, v131
	s_mov_b32 s50, 0x1d000
	v_add_co_u32_e64 v96, s[8:9], s8, v84
	s_mov_b64 s[54:55], 0x2000
	v_add_co_u32_e64 v8, s[2:3], s50, v4
	v_cmp_gt_i32_e64 s[4:5], 2, v99
	v_addc_co_u32_e64 v97, s[8:9], 0, v85, s[8:9]
	v_lshl_add_u64 v[6:7], v[4:5], 0, s[54:55]
	v_cmp_gt_i32_e64 s[0:1], 3, v99
	v_addc_co_u32_e64 v9, s[2:3], 0, v5, s[2:3]
	v_cndmask_b32_e64 v4, v232, v231, s[4:5]
	v_mov_b32_e32 v5, v33
	v_cmp_gt_i32_e64 s[6:7], 1, v99
	s_mov_b32 s8, 0xd000
	v_cndmask_b32_e64 v0, 0, v231, s[0:1]
	v_mov_b32_e32 v1, v33
	v_lshl_add_u64 v[14:15], v[6:7], 0, v[4:5]
	v_cndmask_b32_e64 v4, v233, v231, s[6:7]
	v_add_co_u32_e64 v92, s[8:9], s8, v84
	v_lshl_add_u64 v[12:13], v[6:7], 0, v[0:1]
	v_lshl_add_u64 v[100:101], v[6:7], 0, v[4:5]
	v_cmp_gt_i32_e64 s[2:3], -1, v99
	v_mov_b32_e32 v4, 0x24000
	v_addc_co_u32_e64 v93, s[8:9], 0, v85, s[8:9]
	global_load_dwordx4 v[0:3], v[12:13], off
	global_load_dwordx4 v[66:69], v[8:9], off
	global_load_dwordx4 v[70:73], v[14:15], off
	v_cndmask_b32_e64 v4, v4, v231, s[2:3]
	s_mov_b32 s8, 0x13000
	global_load_dwordx4 v[74:77], v[100:101], off
	v_lshl_add_u64 v[94:95], v[6:7], 0, v[4:5]
	v_add_co_u32_e64 v90, s[8:9], s8, v84
	global_load_dwordx4 v[78:81], v[94:95], off
	global_load_dwordx4 v[38:41], v10, s[22:23]
	global_load_dwordx4 v[42:45], v10, s[20:21]
	global_load_dwordx4 v[28:31], v10, s[20:21] offset:16
	global_load_dwordx4 v[46:49], v10, s[22:23] offset:16
	v_lshl_add_u64 v[4:5], v[84:85], 0, s[84:85]
	s_mov_b64 s[52:53], 0xc000
	v_addc_co_u32_e64 v91, s[8:9], 0, v85, s[8:9]
	global_load_dwordx4 v[50:53], v[96:97], off offset:-4096
	global_load_dwordx4 v[54:57], v[4:5], off offset:16
	global_load_dwordx4 v[24:27], v[90:91], off offset:-4096
	v_lshl_add_u64 v[4:5], v[84:85], 0, s[52:53]
	global_load_dwordx4 v[58:61], v[92:93], off offset:-4096
	global_load_dwordx4 v[62:65], v[4:5], off offset:16
	s_mov_b64 s[56:57], 0x12000
	v_lshl_add_u64 v[4:5], v[84:85], 0, s[56:57]
	global_load_dwordx4 v[4:7], v[4:5], off offset:16
	v_cmp_gt_i32_e64 s[8:9], 0, v99
	v_lshl_add_u64 v[88:89], s[22:23], 0, v[10:11]
	global_load_dwordx4 v[8:11], v[8:9], off offset:2048
	s_nop 0
	global_load_dwordx4 v[20:23], v[12:13], off offset:2048
	global_load_dwordx4 v[16:19], v[14:15], off offset:2048
	s_nop 0
	global_load_dwordx4 v[12:15], v[100:101], off offset:2048
	s_lshl_b32 s49, s10, 3
	global_load_dwordx4 v[100:103], v[94:95], off offset:2048
	s_mov_b64 s[58:59], 0x1000
	s_waitcnt vmcnt(18)
	v_cndmask_b32_e64 v99, v69, 0, s[8:9]
	v_cndmask_b32_e64 v145, v68, 0, s[8:9]
	v_cndmask_b32_e64 v69, v3, 0, s[0:1]
	v_cndmask_b32_e64 v68, v2, 0, s[0:1]
	v_cndmask_b32_e64 v3, v1, 0, s[0:1]
	v_cndmask_b32_e64 v1, v0, 0, s[0:1]
	s_waitcnt vmcnt(17)
	v_cndmask_b32_e64 v107, v72, 0, s[4:5]
	v_cndmask_b32_e64 v105, v71, 0, s[4:5]
	v_cndmask_b32_e64 v104, v70, 0, s[4:5]
	s_waitcnt vmcnt(16)
	v_cndmask_b32_e64 v76, v76, 0, s[6:7]
	v_cndmask_b32_e64 v75, v75, 0, s[6:7]
	v_cndmask_b32_e64 v74, v74, 0, s[6:7]
	v_cndmask_b32_e64 v143, v67, 0, s[8:9]
	v_cndmask_b32_e64 v141, v66, 0, s[8:9]
	v_lshlrev_b32_e32 v0, 16, v1
	v_and_b32_e32 v1, 0xffff0000, v1
	v_lshlrev_b32_e32 v2, 16, v3
	v_and_b32_e32 v3, 0xffff0000, v3
	v_lshlrev_b32_e32 v66, 16, v68
	v_and_b32_e32 v67, 0xffff0000, v68
	v_lshlrev_b32_e32 v68, 16, v69
	v_and_b32_e32 v69, 0xffff0000, v69
	v_lshlrev_b32_e32 v94, 16, v104
	v_and_b32_e32 v95, 0xffff0000, v104
	v_lshlrev_b32_e32 v104, 16, v105
	v_and_b32_e32 v105, 0xffff0000, v105
	v_lshlrev_b32_e32 v106, 16, v107
	v_and_b32_e32 v107, 0xffff0000, v107
	v_cndmask_b32_e64 v109, v73, 0, s[4:5]
	s_waitcnt vmcnt(13)
	v_pk_fma_f32 v[0:1], v[42:43], v[0:1], v[38:39]
	v_pk_fma_f32 v[2:3], v[44:45], v[2:3], v[40:41]
	s_waitcnt vmcnt(11)
	v_pk_fma_f32 v[70:71], v[28:29], v[66:67], v[46:47]
	v_pk_fma_f32 v[72:73], v[30:31], v[68:69], v[48:49]
	global_load_dwordx4 v[66:69], v[96:97], off
	v_lshlrev_b32_e32 v96, 16, v74
	v_and_b32_e32 v97, 0xffff0000, v74
	v_lshlrev_b32_e32 v110, 16, v75
	v_and_b32_e32 v111, 0xffff0000, v75
	v_lshlrev_b32_e32 v112, 16, v76
	v_and_b32_e32 v113, 0xffff0000, v76
	v_pk_fma_f32 v[38:39], v[42:43], v[94:95], v[38:39]
	v_pk_fma_f32 v[40:41], v[44:45], v[104:105], v[40:41]
	v_pk_fma_f32 v[28:29], v[28:29], v[106:107], v[46:47]
	v_cndmask_b32_e64 v156, v79, 0, s[2:3]
	v_lshlrev_b32_e32 v108, 16, v109
	v_and_b32_e32 v109, 0xffff0000, v109
	v_lshlrev_b32_e32 v140, 16, v141
	v_and_b32_e32 v141, 0xffff0000, v141
	v_lshlrev_b32_e32 v142, 16, v143
	v_and_b32_e32 v143, 0xffff0000, v143
	v_lshlrev_b32_e32 v144, 16, v145
	v_and_b32_e32 v145, 0xffff0000, v145
	s_waitcnt vmcnt(11)
	v_pk_fma_f32 v[40:41], v[52:53], v[110:111], v[40:41]
	v_pk_fma_f32 v[38:39], v[50:51], v[96:97], v[38:39]
	s_waitcnt vmcnt(10)
	v_pk_fma_f32 v[28:29], v[54:55], v[112:113], v[28:29]
	v_cndmask_b32_e64 v157, v78, 0, s[2:3]
	v_pk_fma_f32 v[0:1], v[50:51], v[94:95], v[0:1]
	v_pk_fma_f32 v[30:31], v[30:31], v[108:109], v[48:49]
	s_waitcnt vmcnt(8)
	v_pk_fma_f32 v[46:47], v[58:59], v[140:141], v[38:39]
	v_pk_fma_f32 v[38:39], v[60:61], v[142:143], v[40:41]
	s_waitcnt vmcnt(7)
	v_pk_fma_f32 v[48:49], v[62:63], v[144:145], v[28:29]
	v_lshlrev_b32_e32 v28, 16, v156
	v_and_b32_e32 v29, 0xffff0000, v156
	v_pk_fma_f32 v[0:1], v[58:59], v[96:97], v[0:1]
	v_lshlrev_b32_e32 v50, 16, v157
	v_and_b32_e32 v51, 0xffff0000, v157
	v_pk_fma_f32 v[58:59], v[26:27], v[28:29], v[38:39]
	v_pk_fma_f32 v[0:1], v[24:25], v[140:141], v[0:1]
	v_pk_fma_f32 v[24:25], v[24:25], v[50:51], v[46:47]
	v_mul_f32_e32 v50, 0xbfb8aa3b, v58
	v_exp_f32_e32 v50, v50
	v_cndmask_b32_e64 v77, v77, 0, s[6:7]
	v_cndmask_b32_e64 v155, v80, 0, s[2:3]
	v_pk_fma_f32 v[70:71], v[54:55], v[106:107], v[70:71]
	v_pk_fma_f32 v[2:3], v[52:53], v[104:105], v[2:3]
	v_lshlrev_b32_e32 v114, 16, v77
	v_and_b32_e32 v115, 0xffff0000, v77
	global_load_dwordx4 v[74:77], v[92:93], off
	v_pk_fma_f32 v[92:93], v[62:63], v[112:113], v[70:71]
	v_lshlrev_b32_e32 v52, 16, v155
	v_and_b32_e32 v53, 0xffff0000, v155
	v_cndmask_b32_e64 v154, v81, 0, s[2:3]
	v_pk_fma_f32 v[72:73], v[56:57], v[108:109], v[72:73]
	v_lshlrev_b32_e32 v146, 16, v99
	v_and_b32_e32 v147, 0xffff0000, v99
	s_waitcnt vmcnt(7)
	v_pk_fma_f32 v[92:93], v[4:5], v[144:145], v[92:93]
	v_pk_fma_f32 v[30:31], v[56:57], v[114:115], v[30:31]
	v_pk_fma_f32 v[4:5], v[4:5], v[52:53], v[48:49]
	v_mul_f32_e32 v51, 0xbfb8aa3b, v59
	v_add_f32_e32 v50, 1.0, v50
	v_pk_fma_f32 v[2:3], v[60:61], v[110:111], v[2:3]
	v_pk_fma_f32 v[116:117], v[64:65], v[114:115], v[72:73]
	v_pk_fma_f32 v[30:31], v[64:65], v[146:147], v[30:31]
	v_lshlrev_b32_e32 v54, 16, v154
	v_and_b32_e32 v55, 0xffff0000, v154
	v_exp_f32_e32 v51, v51
	v_rcp_f32_e32 v60, v50
	v_mul_f32_e32 v50, 0xbfb8aa3b, v4
	global_load_dwordx4 v[70:73], v[90:91], off
	v_pk_fma_f32 v[2:3], v[26:27], v[142:143], v[2:3]
	v_pk_fma_f32 v[90:91], v[6:7], v[146:147], v[116:117]
	v_add_co_u32_e64 v26, s[10:11], s76, v84
	v_pk_fma_f32 v[6:7], v[6:7], v[54:55], v[30:31]
	v_exp_f32_e32 v55, v50
	v_addc_co_u32_e64 v27, s[10:11], 0, v85, s[10:11]
	v_add_co_u32_e64 v38, s[10:11], s76, v88
	v_add_f32_e32 v54, 1.0, v51
	s_nop 0
	v_addc_co_u32_e64 v39, s[10:11], 0, v89, s[10:11]
	v_mul_f32_e32 v56, 0xbfb8aa3b, v5
	v_lshl_add_u64 v[78:79], v[84:85], 0, s[58:59]
	v_lshl_add_u64 v[42:43], v[88:89], 0, s[58:59]
	s_mov_b64 s[10:11], 0x7000
	v_exp_f32_e32 v56, v56
	v_rcp_f32_e32 v61, v54
	v_add_f32_e32 v54, 1.0, v55
	global_load_dwordx4 v[78:81], v[78:79], off offset:16
	v_lshl_add_u64 v[46:47], v[84:85], 0, s[10:11]
	global_load_dwordx4 v[26:29], v[26:27], off
	s_mov_b64 s[10:11], 0xd000
	global_load_dwordx4 v[38:41], v[38:39], off
	v_rcp_f32_e32 v62, v54
	global_load_dwordx4 v[42:45], v[42:43], off offset:16
	v_mul_f32_e32 v54, 0xbfb8aa3b, v6
	global_load_dwordx4 v[46:49], v[46:47], off offset:16
	v_lshl_add_u64 v[50:51], v[84:85], 0, s[10:11]
	v_exp_f32_e32 v64, v54
	v_mul_f32_e32 v54, 0xbfb8aa3b, v7
	s_mov_b64 s[10:11], 0x13000
	global_load_dwordx4 v[50:53], v[50:51], off offset:16
	v_exp_f32_e32 v65, v54
	v_lshl_add_u64 v[54:55], v[84:85], 0, s[10:11]
	v_add_f32_e32 v63, 1.0, v56
	global_load_dwordx4 v[54:57], v[54:55], off offset:16
	v_mul_f32_e32 v99, 0xbfb8aa3b, v0
	v_exp_f32_e32 v99, v99
	v_mul_f32_e32 v116, 0xbfb8aa3b, v1
	v_exp_f32_e32 v117, v116
	v_mul_f32_e32 v30, 0xbfb8aa3b, v24
	v_add_f32_e32 v99, 1.0, v99
	v_rcp_f32_e32 v116, v99
	v_add_f32_e32 v99, 1.0, v117
	v_mul_f32_e32 v117, 0xbfb8aa3b, v2
	v_exp_f32_e32 v148, v117
	v_mul_f32_e32 v117, 0xbfb8aa3b, v3
	v_exp_f32_e32 v149, v117
	v_rcp_f32_e32 v117, v99
	v_add_f32_e32 v99, 1.0, v148
	v_rcp_f32_e32 v148, v99
	v_add_f32_e32 v99, 1.0, v149
	v_mul_f32_e32 v149, 0xbfb8aa3b, v92
	v_exp_f32_e32 v150, v149
	v_mul_f32_e32 v149, 0xbfb8aa3b, v93
	v_exp_f32_e32 v151, v149
	v_mul_f32_e32 v31, 0xbfb8aa3b, v25
	v_exp_f32_e32 v30, v30
	v_exp_f32_e32 v31, v31
	v_rcp_f32_e32 v149, v99
	v_add_f32_e32 v99, 1.0, v150
	v_rcp_f32_e32 v150, v99
	v_add_f32_e32 v99, 1.0, v151
	v_mul_f32_e32 v151, 0xbfb8aa3b, v90
	v_exp_f32_e32 v152, v151
	v_mul_f32_e32 v151, 0xbfb8aa3b, v91
	v_add_f32_e32 v30, 1.0, v30
	v_add_f32_e32 v31, 1.0, v31
	v_add_f32_e32 v64, 1.0, v64
	v_add_f32_e32 v65, 1.0, v65
	v_exp_f32_e32 v153, v151
	v_rcp_f32_e32 v30, v30
	v_rcp_f32_e32 v31, v31
	v_rcp_f32_e32 v63, v63
	v_rcp_f32_e32 v64, v64
	v_rcp_f32_e32 v65, v65
	v_rcp_f32_e32 v151, v99
	v_add_f32_e32 v99, 1.0, v152
	v_rcp_f32_e32 v152, v99
	v_add_f32_e32 v99, 1.0, v153
	v_pk_mul_f32 v[24:25], v[24:25], v[30:31]
	v_pk_mul_f32 v[30:31], v[58:59], v[60:61]
	v_pk_mul_f32 v[58:59], v[4:5], v[62:63]
	v_pk_mul_f32 v[60:61], v[6:7], v[64:65]
	s_waitcnt vmcnt(13)
	v_cndmask_b32_e64 v23, v23, 0, s[0:1]
	v_cndmask_b32_e64 v21, v21, 0, s[0:1]
	v_cndmask_b32_e64 v20, v20, 0, s[0:1]
	v_rcp_f32_e32 v153, v99
	v_cvt_pk_bf16_f32 v4, v24, v25
	v_cvt_pk_bf16_f32 v6, v58, v59
	v_cvt_pk_bf16_f32 v7, v60, v61
	v_cndmask_b32_e64 v22, v22, 0, s[0:1]
	s_waitcnt vmcnt(12)
	v_cndmask_b32_e64 v24, v19, 0, s[4:5]
	v_cndmask_b32_e64 v19, v17, 0, s[4:5]
	v_cndmask_b32_e64 v17, v16, 0, s[4:5]
	s_waitcnt vmcnt(11)
	v_cndmask_b32_e64 v61, v15, 0, s[6:7]
	v_cndmask_b32_e64 v59, v14, 0, s[6:7]
	v_cndmask_b32_e64 v89, v11, 0, s[8:9]
	v_cndmask_b32_e64 v85, v10, 0, s[8:9]
	v_cndmask_b32_e64 v65, v9, 0, s[8:9]
	v_cndmask_b32_e64 v63, v8, 0, s[8:9]
	v_lshlrev_b32_e32 v8, 16, v20
	v_and_b32_e32 v9, 0xffff0000, v20
	v_lshlrev_b32_e32 v10, 16, v21
	v_and_b32_e32 v11, 0xffff0000, v21
	v_lshlrev_b32_e32 v14, 16, v23
	v_and_b32_e32 v15, 0xffff0000, v23
	v_cvt_pk_bf16_f32 v5, v30, v31
	v_cndmask_b32_e64 v25, v18, 0, s[4:5]
	v_cndmask_b32_e64 v31, v13, 0, s[6:7]
	v_cndmask_b32_e64 v30, v12, 0, s[6:7]
	v_lshlrev_b32_e32 v12, 16, v22
	v_and_b32_e32 v13, 0xffff0000, v22
	s_waitcnt vmcnt(4)
	v_pk_fma_f32 v[10:11], v[28:29], v[10:11], v[40:41]
	v_pk_fma_f32 v[8:9], v[26:27], v[8:9], v[38:39]
	s_waitcnt vmcnt(3)
	v_pk_fma_f32 v[14:15], v[80:81], v[14:15], v[44:45]
	v_lshlrev_b32_e32 v16, 16, v17
	v_and_b32_e32 v17, 0xffff0000, v17
	v_lshlrev_b32_e32 v18, 16, v19
	v_and_b32_e32 v19, 0xffff0000, v19
	v_lshlrev_b32_e32 v22, 16, v24
	v_and_b32_e32 v23, 0xffff0000, v24
	v_pk_fma_f32 v[12:13], v[78:79], v[12:13], v[42:43]
	v_lshlrev_b32_e32 v20, 16, v25
	v_and_b32_e32 v21, 0xffff0000, v25
	v_pk_fma_f32 v[10:11], v[68:69], v[18:19], v[10:11]
	v_pk_fma_f32 v[8:9], v[66:67], v[16:17], v[8:9]
	s_waitcnt vmcnt(2)
	v_pk_fma_f32 v[14:15], v[48:49], v[22:23], v[14:15]
	v_lshlrev_b32_e32 v24, 16, v30
	v_and_b32_e32 v25, 0xffff0000, v30
	v_lshlrev_b32_e32 v30, 16, v31
	v_and_b32_e32 v31, 0xffff0000, v31
	v_lshlrev_b32_e32 v60, 16, v61
	v_and_b32_e32 v61, 0xffff0000, v61
	v_pk_fma_f32 v[12:13], v[46:47], v[20:21], v[12:13]
	v_lshlrev_b32_e32 v58, 16, v59
	v_and_b32_e32 v59, 0xffff0000, v59
	v_pk_fma_f32 v[10:11], v[76:77], v[30:31], v[10:11]
	v_pk_fma_f32 v[8:9], v[74:75], v[24:25], v[8:9]
	s_waitcnt vmcnt(1)
	v_pk_fma_f32 v[14:15], v[52:53], v[60:61], v[14:15]
	v_lshlrev_b32_e32 v62, 16, v63
	v_and_b32_e32 v63, 0xffff0000, v63
	v_lshlrev_b32_e32 v64, 16, v65
	v_and_b32_e32 v65, 0xffff0000, v65
	v_lshlrev_b32_e32 v88, 16, v89
	v_and_b32_e32 v89, 0xffff0000, v89
	v_pk_mul_f32 v[0:1], v[0:1], v[116:117]
	v_pk_mul_f32 v[2:3], v[2:3], v[148:149]
	v_pk_mul_f32 v[92:93], v[92:93], v[150:151]
	v_pk_mul_f32 v[90:91], v[90:91], v[152:153]
	v_pk_fma_f32 v[12:13], v[50:51], v[58:59], v[12:13]
	v_lshlrev_b32_e32 v84, 16, v85
	v_and_b32_e32 v85, 0xffff0000, v85
	v_pk_fma_f32 v[10:11], v[72:73], v[64:65], v[10:11]
	v_pk_fma_f32 v[8:9], v[70:71], v[62:63], v[8:9]
	s_waitcnt vmcnt(0)
	v_pk_fma_f32 v[14:15], v[56:57], v[88:89], v[14:15]
	v_cvt_pk_bf16_f32 v0, v0, v1
	v_cvt_pk_bf16_f32 v1, v2, v3
	v_cvt_pk_bf16_f32 v2, v92, v93
	v_cvt_pk_bf16_f32 v3, v90, v91
	v_mul_f32_e32 v90, 0xbfb8aa3b, v8
	v_mul_f32_e32 v91, 0xbfb8aa3b, v9
	v_pk_fma_f32 v[12:13], v[54:55], v[84:85], v[12:13]
	v_mul_f32_e32 v92, 0xbfb8aa3b, v10
	v_mul_f32_e32 v93, 0xbfb8aa3b, v11
	v_mul_f32_e32 v96, 0xbfb8aa3b, v14
	v_mul_f32_e32 v97, 0xbfb8aa3b, v15
	v_exp_f32_e32 v90, v90
	v_exp_f32_e32 v91, v91
	v_exp_f32_e32 v92, v92
	v_exp_f32_e32 v93, v93
	v_mul_f32_e32 v94, 0xbfb8aa3b, v12
	v_mul_f32_e32 v95, 0xbfb8aa3b, v13
	v_exp_f32_e32 v96, v96
	v_exp_f32_e32 v97, v97
	v_exp_f32_e32 v94, v94
	v_exp_f32_e32 v95, v95
	v_add_f32_e32 v90, 1.0, v90
	v_add_f32_e32 v91, 1.0, v91
	v_add_f32_e32 v92, 1.0, v92
	v_add_f32_e32 v93, 1.0, v93
	v_add_f32_e32 v96, 1.0, v96
	v_add_f32_e32 v97, 1.0, v97
	v_rcp_f32_e32 v90, v90
	v_rcp_f32_e32 v91, v91
	v_rcp_f32_e32 v92, v92
	v_rcp_f32_e32 v93, v93
	v_add_f32_e32 v94, 1.0, v94
	v_add_f32_e32 v95, 1.0, v95
	v_rcp_f32_e32 v96, v96
	v_rcp_f32_e32 v97, v97
	v_rcp_f32_e32 v94, v94
	v_rcp_f32_e32 v95, v95
	v_pk_mul_f32 v[8:9], v[8:9], v[90:91]
	v_pk_mul_f32 v[10:11], v[10:11], v[92:93]
	v_pk_mul_f32 v[14:15], v[14:15], v[96:97]
	v_pk_mul_f32 v[12:13], v[12:13], v[94:95]
	v_cvt_pk_bf16_f32 v8, v8, v9
	v_cvt_pk_bf16_f32 v9, v10, v11
	v_cvt_pk_bf16_f32 v11, v14, v15
	v_pk_fma_f32 v[14:15], v[26:27], v[16:17], v[38:39]
	v_pk_fma_f32 v[16:17], v[78:79], v[20:21], v[42:43]
	v_cndmask_b32_e64 v102, v102, 0, s[2:3]
	v_cndmask_b32_e64 v100, v100, 0, s[2:3]
	v_cvt_pk_bf16_f32 v10, v12, v13
	v_pk_fma_f32 v[12:13], v[28:29], v[18:19], v[40:41]
	v_pk_fma_f32 v[18:19], v[80:81], v[22:23], v[44:45]
	v_pk_fma_f32 v[14:15], v[66:67], v[24:25], v[14:15]
	v_pk_fma_f32 v[16:17], v[46:47], v[58:59], v[16:17]
	v_cndmask_b32_e64 v99, v103, 0, s[2:3]
	v_cndmask_b32_e64 v101, v101, 0, s[2:3]
	v_pk_fma_f32 v[12:13], v[68:69], v[30:31], v[12:13]
	v_pk_fma_f32 v[18:19], v[48:49], v[60:61], v[18:19]
	v_pk_fma_f32 v[14:15], v[74:75], v[62:63], v[14:15]
	v_pk_fma_f32 v[16:17], v[50:51], v[84:85], v[16:17]
	v_lshlrev_b32_e32 v20, 16, v100
	v_and_b32_e32 v21, 0xffff0000, v100
	v_lshlrev_b32_e32 v24, 16, v102
	v_and_b32_e32 v25, 0xffff0000, v102
	v_pk_fma_f32 v[12:13], v[76:77], v[64:65], v[12:13]
	v_pk_fma_f32 v[18:19], v[52:53], v[88:89], v[18:19]
	v_lshlrev_b32_e32 v22, 16, v101
	v_and_b32_e32 v23, 0xffff0000, v101
	v_lshlrev_b32_e32 v26, 16, v99
	v_and_b32_e32 v27, 0xffff0000, v99
	v_pk_fma_f32 v[14:15], v[70:71], v[20:21], v[14:15]
	v_pk_fma_f32 v[16:17], v[54:55], v[24:25], v[16:17]
	v_pk_fma_f32 v[12:13], v[72:73], v[22:23], v[12:13]
	v_pk_fma_f32 v[18:19], v[56:57], v[26:27], v[18:19]
	v_mul_f32_e32 v20, 0xbfb8aa3b, v14
	v_mul_f32_e32 v21, 0xbfb8aa3b, v15
	v_mul_f32_e32 v24, 0xbfb8aa3b, v16
	v_mul_f32_e32 v25, 0xbfb8aa3b, v17
	v_exp_f32_e32 v20, v20
	v_exp_f32_e32 v21, v21
	v_mul_f32_e32 v22, 0xbfb8aa3b, v12
	v_mul_f32_e32 v23, 0xbfb8aa3b, v13
	v_exp_f32_e32 v24, v24
	v_exp_f32_e32 v25, v25
	v_mul_f32_e32 v26, 0xbfb8aa3b, v18
	v_mul_f32_e32 v27, 0xbfb8aa3b, v19
	v_exp_f32_e32 v22, v22
	v_exp_f32_e32 v23, v23
	v_exp_f32_e32 v26, v26
	v_exp_f32_e32 v27, v27
	v_add_f32_e32 v20, 1.0, v20
	v_add_f32_e32 v21, 1.0, v21
	v_add_f32_e32 v24, 1.0, v24
	v_add_f32_e32 v25, 1.0, v25
	v_rcp_f32_e32 v20, v20
	v_rcp_f32_e32 v21, v21
	v_add_f32_e32 v22, 1.0, v22
	v_add_f32_e32 v23, 1.0, v23
	v_rcp_f32_e32 v24, v24
	v_rcp_f32_e32 v25, v25
	v_add_f32_e32 v26, 1.0, v26
	v_add_f32_e32 v27, 1.0, v27
	v_rcp_f32_e32 v22, v22
	v_rcp_f32_e32 v23, v23
	v_rcp_f32_e32 v26, v26
	v_rcp_f32_e32 v27, v27
	v_pk_mul_f32 v[14:15], v[14:15], v[20:21]
	v_pk_mul_f32 v[16:17], v[16:17], v[24:25]
	v_pk_mul_f32 v[20:21], v[12:13], v[22:23]
	v_pk_mul_f32 v[18:19], v[18:19], v[26:27]
	v_cvt_pk_bf16_f32 v12, v14, v15
	v_cvt_pk_bf16_f32 v14, v16, v17
	v_lshl_add_u64 v[16:17], s[18:19], 0, v[32:33]
	v_cvt_pk_bf16_f32 v15, v18, v19
	v_mad_i64_i32 v[18:19], s[0:1], v98, s77, v[16:17]
	global_store_dwordx4 v[18:19], v[0:3], off
	global_store_dwordx4 v[18:19], v[8:11], off offset:2048
	s_add_i32 s4, s49, s34
	v_or_b32_e32 v140, s25, v123
	v_or_b32_e32 v8, 1, v98
	v_mad_i64_i32 v[8:9], s[0:1], v8, s77, v[16:17]
	v_lshl_or_b32 v16, s4, 6, v124
	v_cvt_pk_bf16_f32 v13, v20, v21
	global_store_dwordx4 v[8:9], v[4:7], off
	global_store_dwordx4 v[8:9], v[12:15], off offset:2048
	v_add_u32_e32 v8, -3, v140
	v_ashrrev_i32_e32 v17, 31, v16
	v_mad_i64_i32 v[8:9], s[0:1], v8, s96, v[82:83]
	v_lshlrev_b64 v[88:89], 1, v[16:17]
	v_lshl_add_u64 v[66:67], v[8:9], 0, v[88:89]
	v_or_b32_e32 v8, s48, v123
	v_cmp_eq_u32_e64 s[0:1], 0, v8
	v_lshl_add_u64 v[18:19], v[66:67], 0, s[54:55]
	v_lshlrev_b64 v[16:17], 2, v[16:17]
	v_cndmask_b32_e64 v32, 0, v231, s[0:1]
	v_lshl_add_u64 v[8:9], v[18:19], 0, v[32:33]
	global_load_dwordx4 v[8:11], v[8:9], off
	v_cndmask_b32_e64 v32, v232, v231, s[0:1]
	v_lshl_add_u64 v[12:13], v[18:19], 0, v[32:33]
	v_cndmask_b32_e64 v32, v233, v231, s[0:1]
	global_load_dwordx4 v[12:15], v[12:13], off
	v_lshl_add_u64 v[18:19], v[18:19], 0, v[32:33]
	global_load_dwordx4 v[28:31], v[18:19], off
	v_lshl_add_u64 v[42:43], s[20:21], 0, v[16:17]
	s_movk_i32 s2, 0x6000
	v_lshl_add_u64 v[38:39], s[22:23], 0, v[16:17]
	global_load_dwordx4 v[16:19], v[42:43], off offset:16
	global_load_dwordx4 v[20:23], v[42:43], off
	global_load_dwordx4 v[24:27], v[38:39], off offset:16
	s_nop 0
	global_load_dwordx4 v[38:41], v[38:39], off
	s_mul_i32 s6, s33, 0x4800
	s_add_i32 s7, s6, 0
	s_ashr_i32 s5, s4, 31
	s_add_i32 s7, s7, 0x14000
	s_waitcnt vmcnt(6)
	v_cndmask_b32_e64 v95, v10, 0, s[0:1]
	v_add_co_u32_e64 v10, s[2:3], s2, v42
	v_cndmask_b32_e64 v32, v11, 0, s[0:1]
	v_cndmask_b32_e64 v93, v9, 0, s[0:1]
	v_cndmask_b32_e64 v91, v8, 0, s[0:1]
	v_lshl_add_u64 v[8:9], v[42:43], 0, s[84:85]
	v_addc_co_u32_e64 v11, s[2:3], 0, v43, s[2:3]
	global_load_dwordx4 v[50:53], v[10:11], off
	global_load_dwordx4 v[46:49], v[8:9], off offset:16
	v_add_co_u32_e64 v8, s[2:3], s50, v66
	s_waitcnt vmcnt(7)
	v_cndmask_b32_e64 v99, v12, 0, s[0:1]
	v_addc_co_u32_e64 v9, s[2:3], 0, v67, s[2:3]
	s_mov_b32 s2, 0xc000
	s_nop 0
	v_add_co_u32_e64 v12, s[2:3], s2, v42
	v_cndmask_b32_e64 v105, v15, 0, s[0:1]
	v_cndmask_b32_e64 v103, v14, 0, s[0:1]
	v_cndmask_b32_e64 v101, v13, 0, s[0:1]
	s_waitcnt vmcnt(6)
	v_cndmask_b32_e64 v110, v31, 0, s[0:1]
	v_addc_co_u32_e64 v13, s[2:3], 0, v43, s[2:3]
	v_cndmask_b32_e64 v111, v30, 0, s[0:1]
	v_cndmask_b32_e64 v109, v29, 0, s[0:1]
	v_cndmask_b32_e64 v107, v28, 0, s[0:1]
	s_mov_b32 s0, 0x12000
	global_load_dwordx4 v[8:11], v[8:9], off
	v_add_co_u32_e64 v14, s[0:1], s0, v42
	global_load_dwordx4 v[58:61], v[12:13], off
	v_lshl_add_u64 v[12:13], v[42:43], 0, s[52:53]
	global_load_dwordx4 v[62:65], v[12:13], off offset:16
	v_addc_co_u32_e64 v15, s[0:1], 0, v43, s[0:1]
	v_lshl_add_u64 v[12:13], v[42:43], 0, s[56:57]
	global_load_dwordx4 v[54:57], v[14:15], off
	global_load_dwordx4 v[28:31], v[12:13], off offset:16
	s_mov_b32 s0, 0x26000
	v_add_co_u32_e64 v12, s[0:1], s0, v66
	v_lshlrev_b32_e32 v90, 16, v91
	s_nop 0
	v_addc_co_u32_e64 v13, s[0:1], 0, v67, s[0:1]
	s_mov_b32 s0, 0x2f000
	s_nop 0
	v_add_co_u32_e64 v42, s[0:1], s0, v66
	v_and_b32_e32 v91, 0xffff0000, v91
	s_nop 0
	v_addc_co_u32_e64 v43, s[0:1], 0, v67, s[0:1]
	global_load_dwordx4 v[12:15], v[12:13], off
	s_nop 0
	global_load_dwordx4 v[42:45], v[42:43], off
	v_lshlrev_b32_e32 v94, 16, v95
	v_and_b32_e32 v95, 0xffff0000, v95
	v_lshlrev_b32_e32 v96, 16, v32
	v_and_b32_e32 v97, 0xffff0000, v32
	s_waitcnt vmcnt(9)
	v_pk_fma_f32 v[90:91], v[20:21], v[90:91], v[38:39]
	v_lshlrev_b32_e32 v98, 16, v99
	v_and_b32_e32 v99, 0xffff0000, v99
	v_lshlrev_b32_e32 v92, 16, v93
	v_and_b32_e32 v93, 0xffff0000, v93
	v_pk_fma_f32 v[96:97], v[18:19], v[96:97], v[26:27]
	v_pk_fma_f32 v[94:95], v[16:17], v[94:95], v[24:25]
	v_lshlrev_b32_e32 v102, 16, v103
	v_and_b32_e32 v103, 0xffff0000, v103
	v_lshlrev_b32_e32 v104, 16, v105
	v_and_b32_e32 v105, 0xffff0000, v105
	v_lshlrev_b32_e32 v106, 16, v107
	v_and_b32_e32 v107, 0xffff0000, v107
	v_pk_fma_f32 v[92:93], v[22:23], v[92:93], v[40:41]
	v_lshlrev_b32_e32 v100, 16, v101
	v_and_b32_e32 v101, 0xffff0000, v101
	v_lshlrev_b32_e32 v112, 16, v111
	v_and_b32_e32 v113, 0xffff0000, v111
	v_lshlrev_b32_e32 v114, 16, v110
	v_and_b32_e32 v115, 0xffff0000, v110
	v_lshlrev_b32_e32 v108, 16, v109
	v_and_b32_e32 v109, 0xffff0000, v109
	s_mov_b32 s0, 0x38000
	v_add_co_u32_e64 v68, s[0:1], s0, v66
	s_waitcnt vmcnt(8)
	v_pk_fma_f32 v[90:91], v[50:51], v[98:99], v[90:91]
	s_waitcnt vmcnt(7)
	v_pk_fma_f32 v[96:97], v[48:49], v[104:105], v[96:97]
	v_pk_fma_f32 v[94:95], v[46:47], v[102:103], v[94:95]
	v_pk_fma_f32 v[92:93], v[52:53], v[100:101], v[92:93]
	v_addc_co_u32_e64 v69, s[0:1], 0, v67, s[0:1]
	s_mov_b32 s0, 0x41000
	s_nop 0
	v_add_co_u32_e64 v74, s[0:1], s0, v66
	v_pk_fma_f32 v[100:101], v[22:23], v[100:101], v[40:41]
	s_nop 0
	v_addc_co_u32_e64 v75, s[0:1], 0, v67, s[0:1]
	global_load_dwordx4 v[70:73], v[68:69], off
	global_load_dwordx4 v[78:81], v[74:75], off
	v_pk_fma_f32 v[98:99], v[20:21], v[98:99], v[38:39]
	v_pk_fma_f32 v[100:101], v[52:53], v[108:109], v[100:101]
	v_pk_fma_f32 v[98:99], v[50:51], v[106:107], v[98:99]
	v_pk_fma_f32 v[104:105], v[18:19], v[104:105], v[26:27]
	v_pk_fma_f32 v[102:103], v[16:17], v[102:103], v[24:25]
	v_pk_fma_f32 v[104:105], v[48:49], v[114:115], v[104:105]
	v_pk_fma_f32 v[102:103], v[46:47], v[112:113], v[102:103]
	s_mov_b32 s0, 0x4a000
	v_add_co_u32_e64 v68, s[0:1], s0, v66
	s_waitcnt vmcnt(7)
	v_pk_fma_f32 v[110:111], v[58:59], v[106:107], v[90:91]
	v_lshlrev_b32_e32 v90, 16, v8
	v_and_b32_e32 v91, 0xffff0000, v8
	s_waitcnt vmcnt(6)
	v_pk_fma_f32 v[142:143], v[64:65], v[114:115], v[96:97]
	v_pk_fma_f32 v[144:145], v[62:63], v[112:113], v[94:95]
	v_lshlrev_b32_e32 v94, 16, v10
	v_and_b32_e32 v95, 0xffff0000, v10
	v_lshlrev_b32_e32 v96, 16, v11
	v_and_b32_e32 v97, 0xffff0000, v11
	s_waitcnt vmcnt(5)
	v_pk_fma_f32 v[10:11], v[54:55], v[90:91], v[110:111]
	v_pk_fma_f32 v[116:117], v[60:61], v[108:109], v[92:93]
	v_lshlrev_b32_e32 v92, 16, v9
	v_and_b32_e32 v93, 0xffff0000, v9
	v_mul_f32_e32 v32, 0xbfb8aa3b, v10
	v_pk_fma_f32 v[8:9], v[56:57], v[92:93], v[116:117]
	v_exp_f32_e32 v32, v32
	v_mul_f32_e32 v116, 0xbfb8aa3b, v11
	v_exp_f32_e32 v141, v116
	s_waitcnt vmcnt(4)
	v_pk_fma_f32 v[110:111], v[30:31], v[96:97], v[142:143]
	v_add_f32_e32 v32, 1.0, v32
	v_rcp_f32_e32 v142, v32
	v_add_f32_e32 v32, 1.0, v141
	v_mul_f32_e32 v141, 0xbfb8aa3b, v8
	v_exp_f32_e32 v141, v141
	v_mul_f32_e32 v143, 0xbfb8aa3b, v9
	v_pk_fma_f32 v[116:117], v[28:29], v[94:95], v[144:145]
	v_exp_f32_e32 v145, v143
	v_rcp_f32_e32 v143, v32
	v_add_f32_e32 v32, 1.0, v141
	v_mul_f32_e32 v141, 0xbfb8aa3b, v116
	v_rcp_f32_e32 v144, v32
	v_add_f32_e32 v32, 1.0, v145
	v_exp_f32_e32 v141, v141
	v_mul_f32_e32 v145, 0xbfb8aa3b, v117
	v_exp_f32_e32 v147, v145
	v_rcp_f32_e32 v145, v32
	v_add_f32_e32 v32, 1.0, v141
	v_mul_f32_e32 v141, 0xbfb8aa3b, v110
	v_rcp_f32_e32 v146, v32
	v_add_f32_e32 v32, 1.0, v147
	v_exp_f32_e32 v141, v141
	v_mul_f32_e32 v147, 0xbfb8aa3b, v111
	v_exp_f32_e32 v149, v147
	v_rcp_f32_e32 v147, v32
	v_add_f32_e32 v32, 1.0, v141
	v_rcp_f32_e32 v148, v32
	v_add_f32_e32 v32, 1.0, v149
	v_rcp_f32_e32 v149, v32
	v_pk_mul_f32 v[10:11], v[10:11], v[142:143]
	v_pk_mul_f32 v[142:143], v[8:9], v[144:145]
	v_pk_mul_f32 v[116:117], v[116:117], v[146:147]
	v_pk_mul_f32 v[110:111], v[110:111], v[148:149]
	v_cvt_pk_bf16_f32 v9, v142, v143
	v_pk_fma_f32 v[98:99], v[58:59], v[90:91], v[98:99]
	v_pk_fma_f32 v[142:143], v[60:61], v[92:93], v[100:101]
	s_waitcnt vmcnt(3)
	v_lshlrev_b32_e32 v100, 16, v12
	v_and_b32_e32 v101, 0xffff0000, v12
	v_cvt_pk_bf16_f32 v8, v10, v11
	v_cvt_pk_bf16_f32 v10, v116, v117
	v_cvt_pk_bf16_f32 v11, v110, v111
	v_lshlrev_b32_e32 v110, 16, v14
	v_and_b32_e32 v111, 0xffff0000, v14
	v_lshlrev_b32_e32 v116, 16, v15
	v_and_b32_e32 v117, 0xffff0000, v15
	v_pk_fma_f32 v[14:15], v[54:55], v[100:101], v[98:99]
	v_pk_fma_f32 v[144:145], v[64:65], v[96:97], v[104:105]
	v_mul_f32_e32 v32, 0xbfb8aa3b, v14
	v_exp_f32_e32 v32, v32
	v_mul_f32_e32 v141, 0xbfb8aa3b, v15
	v_exp_f32_e32 v141, v141
	v_lshlrev_b32_e32 v104, 16, v13
	v_and_b32_e32 v105, 0xffff0000, v13
	v_pk_fma_f32 v[12:13], v[56:57], v[104:105], v[142:143]
	v_add_f32_e32 v32, 1.0, v32
	v_rcp_f32_e32 v142, v32
	v_add_f32_e32 v32, 1.0, v141
	v_mul_f32_e32 v141, 0xbfb8aa3b, v12
	v_exp_f32_e32 v141, v141
	v_mul_f32_e32 v143, 0xbfb8aa3b, v13
	v_pk_fma_f32 v[98:99], v[30:31], v[116:117], v[144:145]
	v_exp_f32_e32 v145, v143
	v_pk_fma_f32 v[102:103], v[62:63], v[94:95], v[102:103]
	v_rcp_f32_e32 v143, v32
	v_pk_fma_f32 v[102:103], v[28:29], v[110:111], v[102:103]
	v_add_f32_e32 v32, 1.0, v141
	v_mul_f32_e32 v141, 0xbfb8aa3b, v102
	v_rcp_f32_e32 v144, v32
	v_add_f32_e32 v32, 1.0, v145
	v_exp_f32_e32 v141, v141
	v_mul_f32_e32 v145, 0xbfb8aa3b, v103
	v_exp_f32_e32 v147, v145
	v_rcp_f32_e32 v145, v32
	v_add_f32_e32 v32, 1.0, v141
	v_mul_f32_e32 v141, 0xbfb8aa3b, v98
	v_rcp_f32_e32 v146, v32
	v_add_f32_e32 v32, 1.0, v147
	v_exp_f32_e32 v141, v141
	v_mul_f32_e32 v147, 0xbfb8aa3b, v99
	v_exp_f32_e32 v149, v147
	v_rcp_f32_e32 v147, v32
	v_add_f32_e32 v32, 1.0, v141
	v_rcp_f32_e32 v148, v32
	v_add_f32_e32 v32, 1.0, v149
	v_rcp_f32_e32 v149, v32
	v_pk_mul_f32 v[14:15], v[14:15], v[142:143]
	v_pk_mul_f32 v[102:103], v[102:103], v[146:147]
	v_pk_mul_f32 v[142:143], v[12:13], v[144:145]
	v_pk_mul_f32 v[98:99], v[98:99], v[148:149]
	v_cvt_pk_bf16_f32 v12, v14, v15
	v_cvt_pk_bf16_f32 v14, v102, v103
	v_cvt_pk_bf16_f32 v15, v98, v99
	v_pk_fma_f32 v[98:99], v[22:23], v[108:109], v[40:41]
	v_pk_fma_f32 v[102:103], v[20:21], v[106:107], v[38:39]
	v_pk_fma_f32 v[108:109], v[16:17], v[112:113], v[24:25]
	v_pk_fma_f32 v[98:99], v[52:53], v[92:93], v[98:99]
	v_pk_fma_f32 v[102:103], v[50:51], v[90:91], v[102:103]
	v_cvt_pk_bf16_f32 v13, v142, v143
	v_pk_fma_f32 v[108:109], v[46:47], v[94:95], v[108:109]
	v_pk_fma_f32 v[112:113], v[58:59], v[100:101], v[102:103]
	v_pk_fma_f32 v[142:143], v[60:61], v[104:105], v[98:99]
	s_waitcnt vmcnt(2)
	v_lshlrev_b32_e32 v98, 16, v42
	v_and_b32_e32 v99, 0xffff0000, v42
	v_pk_fma_f32 v[106:107], v[18:19], v[114:115], v[26:27]
	v_pk_fma_f32 v[144:145], v[62:63], v[110:111], v[108:109]
	v_lshlrev_b32_e32 v108, 16, v44
	v_and_b32_e32 v109, 0xffff0000, v44
	v_lshlrev_b32_e32 v114, 16, v45
	v_and_b32_e32 v115, 0xffff0000, v45
	v_pk_fma_f32 v[44:45], v[54:55], v[98:99], v[112:113]
	v_lshlrev_b32_e32 v102, 16, v43
	v_mul_f32_e32 v32, 0xbfb8aa3b, v44
	v_exp_f32_e32 v32, v32
	v_mul_f32_e32 v112, 0xbfb8aa3b, v45
	v_exp_f32_e32 v141, v112
	v_and_b32_e32 v103, 0xffff0000, v43
	v_pk_fma_f32 v[42:43], v[56:57], v[102:103], v[142:143]
	v_add_f32_e32 v32, 1.0, v32
	v_addc_co_u32_e64 v69, s[0:1], 0, v67, s[0:1]
	v_rcp_f32_e32 v142, v32
	v_add_f32_e32 v32, 1.0, v141
	v_mul_f32_e32 v141, 0xbfb8aa3b, v42
	s_mov_b32 s0, 0x53000
	v_exp_f32_e32 v141, v141
	v_mul_f32_e32 v143, 0xbfb8aa3b, v43
	v_add_co_u32_e64 v74, s[0:1], s0, v66
	v_pk_fma_f32 v[112:113], v[28:29], v[108:109], v[144:145]
	v_exp_f32_e32 v145, v143
	v_addc_co_u32_e64 v75, s[0:1], 0, v67, s[0:1]
	global_load_dwordx4 v[82:85], v[68:69], off
	s_nop 0
	global_load_dwordx4 v[74:77], v[74:75], off
	v_rcp_f32_e32 v143, v32
	v_add_f32_e32 v32, 1.0, v141
	v_mul_f32_e32 v141, 0xbfb8aa3b, v112
	v_rcp_f32_e32 v144, v32
	v_add_f32_e32 v32, 1.0, v145
	v_exp_f32_e32 v141, v141
	v_mul_f32_e32 v145, 0xbfb8aa3b, v113
	v_pk_fma_f32 v[106:107], v[48:49], v[96:97], v[106:107]
	v_exp_f32_e32 v147, v145
	v_pk_fma_f32 v[106:107], v[64:65], v[116:117], v[106:107]
	v_rcp_f32_e32 v145, v32
	v_pk_fma_f32 v[106:107], v[30:31], v[114:115], v[106:107]
	v_add_f32_e32 v32, 1.0, v141
	v_mul_f32_e32 v141, 0xbfb8aa3b, v106
	v_rcp_f32_e32 v146, v32
	v_add_f32_e32 v32, 1.0, v147
	v_exp_f32_e32 v141, v141
	v_mul_f32_e32 v147, 0xbfb8aa3b, v107
	v_exp_f32_e32 v149, v147
	v_rcp_f32_e32 v147, v32
	v_add_f32_e32 v32, 1.0, v141
	v_rcp_f32_e32 v148, v32
	v_add_f32_e32 v32, 1.0, v149
	v_rcp_f32_e32 v149, v32
	v_pk_fma_f32 v[90:91], v[20:21], v[90:91], v[38:39]
	v_pk_fma_f32 v[92:93], v[22:23], v[92:93], v[40:41]
	v_pk_mul_f32 v[44:45], v[44:45], v[142:143]
	v_pk_mul_f32 v[142:143], v[42:43], v[144:145]
	v_pk_fma_f32 v[92:93], v[52:53], v[104:105], v[92:93]
	v_pk_fma_f32 v[90:91], v[50:51], v[100:101], v[90:91]
	v_pk_mul_f32 v[112:113], v[112:113], v[146:147]
	v_pk_mul_f32 v[106:107], v[106:107], v[148:149]
	v_cvt_pk_bf16_f32 v43, v142, v143
	v_pk_fma_f32 v[142:143], v[60:61], v[102:103], v[92:93]
	v_pk_fma_f32 v[90:91], v[58:59], v[98:99], v[90:91]
	s_waitcnt vmcnt(3)
	v_lshlrev_b32_e32 v92, 16, v70
	v_and_b32_e32 v93, 0xffff0000, v70
	v_cvt_pk_bf16_f32 v42, v44, v45
	v_cvt_pk_bf16_f32 v44, v112, v113
	v_cvt_pk_bf16_f32 v45, v106, v107
	v_lshlrev_b32_e32 v106, 16, v72
	v_and_b32_e32 v107, 0xffff0000, v72
	v_lshlrev_b32_e32 v112, 16, v73
	v_and_b32_e32 v113, 0xffff0000, v73
	v_pk_fma_f32 v[72:73], v[54:55], v[92:93], v[90:91]
	v_pk_fma_f32 v[96:97], v[18:19], v[96:97], v[26:27]
	v_mul_f32_e32 v32, 0xbfb8aa3b, v72
	v_exp_f32_e32 v32, v32
	v_mul_f32_e32 v141, 0xbfb8aa3b, v73
	v_exp_f32_e32 v141, v141
	v_pk_fma_f32 v[96:97], v[48:49], v[116:117], v[96:97]
	v_add_f32_e32 v32, 1.0, v32
	v_pk_fma_f32 v[144:145], v[64:65], v[114:115], v[96:97]
	v_lshlrev_b32_e32 v96, 16, v71
	v_and_b32_e32 v97, 0xffff0000, v71
	v_pk_fma_f32 v[70:71], v[56:57], v[96:97], v[142:143]
	v_rcp_f32_e32 v142, v32
	v_add_f32_e32 v32, 1.0, v141
	v_mul_f32_e32 v141, 0xbfb8aa3b, v70
	v_pk_fma_f32 v[94:95], v[16:17], v[94:95], v[24:25]
	v_exp_f32_e32 v141, v141
	v_mul_f32_e32 v143, 0xbfb8aa3b, v71
	v_pk_fma_f32 v[94:95], v[46:47], v[110:111], v[94:95]
	v_pk_fma_f32 v[90:91], v[30:31], v[112:113], v[144:145]
	v_exp_f32_e32 v145, v143
	v_pk_fma_f32 v[94:95], v[62:63], v[108:109], v[94:95]
	s_mov_b32 s0, 0x5c000
	v_pk_fma_f32 v[94:95], v[28:29], v[106:107], v[94:95]
	v_rcp_f32_e32 v143, v32
	v_add_f32_e32 v32, 1.0, v141
	v_mul_f32_e32 v141, 0xbfb8aa3b, v94
	v_add_co_u32_e64 v66, s[0:1], s0, v66
	v_rcp_f32_e32 v144, v32
	v_add_f32_e32 v32, 1.0, v145
	v_exp_f32_e32 v141, v141
	v_mul_f32_e32 v145, 0xbfb8aa3b, v95
	v_addc_co_u32_e64 v67, s[0:1], 0, v67, s[0:1]
	v_exp_f32_e32 v147, v145
	global_load_dwordx4 v[66:69], v[66:67], off
	v_rcp_f32_e32 v145, v32
	v_add_f32_e32 v32, 1.0, v141
	v_mul_f32_e32 v141, 0xbfb8aa3b, v90
	v_rcp_f32_e32 v146, v32
	v_add_f32_e32 v32, 1.0, v147
	v_exp_f32_e32 v141, v141
	v_mul_f32_e32 v147, 0xbfb8aa3b, v91
	v_exp_f32_e32 v149, v147
	v_rcp_f32_e32 v147, v32
	v_add_f32_e32 v32, 1.0, v141
	v_rcp_f32_e32 v148, v32
	v_add_f32_e32 v32, 1.0, v149
	v_rcp_f32_e32 v149, v32
	v_pk_mul_f32 v[72:73], v[72:73], v[142:143]
	v_pk_mul_f32 v[142:143], v[70:71], v[144:145]
	v_pk_mul_f32 v[94:95], v[94:95], v[146:147]
	v_pk_mul_f32 v[90:91], v[90:91], v[148:149]
	v_cvt_pk_bf16_f32 v70, v72, v73
	v_cvt_pk_bf16_f32 v73, v90, v91
	v_pk_fma_f32 v[90:91], v[20:21], v[100:101], v[38:39]
	v_cvt_pk_bf16_f32 v72, v94, v95
	v_pk_fma_f32 v[94:95], v[22:23], v[104:105], v[40:41]
	v_pk_fma_f32 v[100:101], v[16:17], v[110:111], v[24:25]
	v_pk_fma_f32 v[104:105], v[18:19], v[116:117], v[26:27]
	v_pk_fma_f32 v[90:91], v[50:51], v[98:99], v[90:91]
	v_pk_fma_f32 v[104:105], v[48:49], v[114:115], v[104:105]
	v_pk_fma_f32 v[100:101], v[46:47], v[108:109], v[100:101]
	v_pk_fma_f32 v[116:117], v[58:59], v[92:93], v[90:91]
	s_waitcnt vmcnt(3)
	v_lshlrev_b32_e32 v90, 16, v78
	v_and_b32_e32 v91, 0xffff0000, v78
	v_cvt_pk_bf16_f32 v71, v142, v143
	v_pk_fma_f32 v[142:143], v[62:63], v[106:107], v[100:101]
	v_pk_fma_f32 v[144:145], v[64:65], v[112:113], v[104:105]
	v_lshlrev_b32_e32 v100, 16, v80
	v_and_b32_e32 v101, 0xffff0000, v80
	v_lshlrev_b32_e32 v104, 16, v81
	v_and_b32_e32 v105, 0xffff0000, v81
	v_pk_fma_f32 v[80:81], v[54:55], v[90:91], v[116:117]
	v_pk_fma_f32 v[94:95], v[52:53], v[102:103], v[94:95]
	v_mul_f32_e32 v32, 0xbfb8aa3b, v80
	v_exp_f32_e32 v32, v32
	v_mul_f32_e32 v116, 0xbfb8aa3b, v81
	v_exp_f32_e32 v141, v116
	v_pk_fma_f32 v[110:111], v[60:61], v[96:97], v[94:95]
	v_lshlrev_b32_e32 v94, 16, v79
	v_and_b32_e32 v95, 0xffff0000, v79
	v_pk_fma_f32 v[78:79], v[56:57], v[94:95], v[110:111]
	v_add_f32_e32 v32, 1.0, v32
	v_pk_fma_f32 v[116:117], v[28:29], v[100:101], v[142:143]
	v_rcp_f32_e32 v142, v32
	v_add_f32_e32 v32, 1.0, v141
	v_mul_f32_e32 v141, 0xbfb8aa3b, v78
	v_exp_f32_e32 v141, v141
	v_mul_f32_e32 v143, 0xbfb8aa3b, v79
	v_pk_fma_f32 v[110:111], v[30:31], v[104:105], v[144:145]
	v_exp_f32_e32 v145, v143
	v_rcp_f32_e32 v143, v32
	v_add_f32_e32 v32, 1.0, v141
	v_mul_f32_e32 v141, 0xbfb8aa3b, v116
	v_rcp_f32_e32 v144, v32
	v_add_f32_e32 v32, 1.0, v145
	v_exp_f32_e32 v141, v141
	v_mul_f32_e32 v145, 0xbfb8aa3b, v117
	v_exp_f32_e32 v147, v145
	v_rcp_f32_e32 v145, v32
	v_add_f32_e32 v32, 1.0, v141
	v_mul_f32_e32 v141, 0xbfb8aa3b, v110
	v_rcp_f32_e32 v146, v32
	v_add_f32_e32 v32, 1.0, v147
	v_exp_f32_e32 v141, v141
	v_mul_f32_e32 v147, 0xbfb8aa3b, v111
	v_exp_f32_e32 v149, v147
	v_rcp_f32_e32 v147, v32
	v_add_f32_e32 v32, 1.0, v141
	v_rcp_f32_e32 v148, v32
	v_add_f32_e32 v32, 1.0, v149
	v_rcp_f32_e32 v149, v32
	v_pk_fma_f32 v[98:99], v[20:21], v[98:99], v[38:39]
	v_pk_mul_f32 v[80:81], v[80:81], v[142:143]
	v_pk_fma_f32 v[98:99], v[50:51], v[92:93], v[98:99]
	v_pk_mul_f32 v[110:111], v[110:111], v[148:149]
	v_pk_mul_f32 v[142:143], v[78:79], v[144:145]
	v_cvt_pk_bf16_f32 v78, v80, v81
	v_cvt_pk_bf16_f32 v81, v110, v111
	v_pk_fma_f32 v[102:103], v[22:23], v[102:103], v[40:41]
	v_pk_fma_f32 v[110:111], v[18:19], v[114:115], v[26:27]
	v_pk_fma_f32 v[98:99], v[58:59], v[90:91], v[98:99]
	s_waitcnt vmcnt(2)
	v_lshlrev_b32_e32 v114, 16, v82
	v_and_b32_e32 v115, 0xffff0000, v82
	v_pk_mul_f32 v[116:117], v[116:117], v[146:147]
	v_cvt_pk_bf16_f32 v79, v142, v143
	v_pk_fma_f32 v[102:103], v[52:53], v[96:97], v[102:103]
	v_lshlrev_b32_e32 v142, 16, v84
	v_and_b32_e32 v143, 0xffff0000, v84
	v_lshlrev_b32_e32 v144, 16, v85
	v_and_b32_e32 v145, 0xffff0000, v85
	v_pk_fma_f32 v[84:85], v[54:55], v[114:115], v[98:99]
	v_cvt_pk_bf16_f32 v80, v116, v117
	v_pk_fma_f32 v[110:111], v[48:49], v[112:113], v[110:111]
	v_pk_fma_f32 v[102:103], v[60:61], v[94:95], v[102:103]
	v_lshlrev_b32_e32 v116, 16, v83
	v_and_b32_e32 v117, 0xffff0000, v83
	v_mul_f32_e32 v32, 0xbfb8aa3b, v84
	v_pk_fma_f32 v[110:111], v[64:65], v[104:105], v[110:111]
	v_pk_fma_f32 v[82:83], v[56:57], v[116:117], v[102:103]
	v_exp_f32_e32 v32, v32
	v_mul_f32_e32 v102, 0xbfb8aa3b, v85
	v_pk_fma_f32 v[108:109], v[16:17], v[108:109], v[24:25]
	v_pk_fma_f32 v[98:99], v[30:31], v[144:145], v[110:111]
	v_exp_f32_e32 v110, v102
	v_pk_fma_f32 v[108:109], v[46:47], v[106:107], v[108:109]
	v_add_f32_e32 v32, 1.0, v32
	v_pk_fma_f32 v[108:109], v[62:63], v[100:101], v[108:109]
	v_pk_fma_f32 v[92:93], v[20:21], v[92:93], v[38:39]
	v_pk_fma_f32 v[102:103], v[28:29], v[142:143], v[108:109]
	v_mul_f32_e32 v109, 0xbfb8aa3b, v82
	v_rcp_f32_e32 v108, v32
	v_add_f32_e32 v32, 1.0, v110
	v_exp_f32_e32 v110, v109
	v_mul_f32_e32 v109, 0xbfb8aa3b, v83
	v_exp_f32_e32 v111, v109
	v_rcp_f32_e32 v109, v32
	v_add_f32_e32 v32, 1.0, v110
	v_rcp_f32_e32 v110, v32
	v_add_f32_e32 v32, 1.0, v111
	v_mul_f32_e32 v111, 0xbfb8aa3b, v102
	v_exp_f32_e32 v141, v111
	v_mul_f32_e32 v111, 0xbfb8aa3b, v103
	v_exp_f32_e32 v147, v111
	v_rcp_f32_e32 v111, v32
	v_add_f32_e32 v32, 1.0, v141
	v_mul_f32_e32 v141, 0xbfb8aa3b, v98
	v_rcp_f32_e32 v146, v32
	v_add_f32_e32 v32, 1.0, v147
	v_exp_f32_e32 v141, v141
	v_mul_f32_e32 v147, 0xbfb8aa3b, v99
	v_exp_f32_e32 v149, v147
	v_rcp_f32_e32 v147, v32
	v_add_f32_e32 v32, 1.0, v141
	v_rcp_f32_e32 v148, v32
	v_add_f32_e32 v32, 1.0, v149
	v_rcp_f32_e32 v149, v32
	v_pk_mul_f32 v[84:85], v[84:85], v[108:109]
	v_pk_fma_f32 v[92:93], v[50:51], v[90:91], v[92:93]
	v_pk_mul_f32 v[108:109], v[82:83], v[110:111]
	v_pk_mul_f32 v[98:99], v[98:99], v[148:149]
	v_pk_mul_f32 v[102:103], v[102:103], v[146:147]
	v_cvt_pk_bf16_f32 v82, v84, v85
	v_cvt_pk_bf16_f32 v85, v98, v99
	v_pk_fma_f32 v[96:97], v[22:23], v[96:97], v[40:41]
	v_pk_fma_f32 v[98:99], v[16:17], v[106:107], v[24:25]
	v_pk_fma_f32 v[92:93], v[58:59], v[114:115], v[92:93]
	s_waitcnt vmcnt(1)
	v_lshlrev_b32_e32 v106, 16, v74
	v_and_b32_e32 v107, 0xffff0000, v74
	v_cvt_pk_bf16_f32 v84, v102, v103
	v_pk_fma_f32 v[102:103], v[18:19], v[112:113], v[26:27]
	v_pk_fma_f32 v[96:97], v[52:53], v[94:95], v[96:97]
	v_lshlrev_b32_e32 v110, 16, v76
	v_and_b32_e32 v111, 0xffff0000, v76
	v_lshlrev_b32_e32 v112, 16, v77
	v_and_b32_e32 v113, 0xffff0000, v77
	v_pk_fma_f32 v[76:77], v[54:55], v[106:107], v[92:93]
	v_cvt_pk_bf16_f32 v83, v108, v109
	v_pk_fma_f32 v[102:103], v[48:49], v[104:105], v[102:103]
	v_pk_fma_f32 v[96:97], v[60:61], v[116:117], v[96:97]
	v_lshlrev_b32_e32 v108, 16, v75
	v_and_b32_e32 v109, 0xffff0000, v75
	v_mul_f32_e32 v32, 0xbfb8aa3b, v76
	v_pk_fma_f32 v[20:21], v[20:21], v[90:91], v[38:39]
	v_pk_fma_f32 v[102:103], v[64:65], v[144:145], v[102:103]
	v_pk_fma_f32 v[74:75], v[56:57], v[108:109], v[96:97]
	v_exp_f32_e32 v32, v32
	v_mul_f32_e32 v96, 0xbfb8aa3b, v77
	v_pk_fma_f32 v[22:23], v[22:23], v[94:95], v[40:41]
	v_pk_fma_f32 v[16:17], v[16:17], v[100:101], v[24:25]
	v_pk_fma_f32 v[20:21], v[50:51], v[114:115], v[20:21]
	v_pk_fma_f32 v[92:93], v[30:31], v[112:113], v[102:103]
	v_exp_f32_e32 v102, v96
	v_pk_fma_f32 v[22:23], v[52:53], v[116:117], v[22:23]
	v_pk_fma_f32 v[16:17], v[46:47], v[142:143], v[16:17]
	v_pk_fma_f32 v[20:21], v[58:59], v[106:107], v[20:21]
	s_waitcnt vmcnt(0)
	v_lshlrev_b32_e32 v24, 16, v66
	v_and_b32_e32 v25, 0xffff0000, v66
	v_pk_fma_f32 v[98:99], v[46:47], v[100:101], v[98:99]
	v_pk_fma_f32 v[18:19], v[18:19], v[104:105], v[26:27]
	v_pk_fma_f32 v[22:23], v[60:61], v[108:109], v[22:23]
	v_pk_fma_f32 v[16:17], v[62:63], v[110:111], v[16:17]
	v_lshlrev_b32_e32 v26, 16, v67
	v_and_b32_e32 v27, 0xffff0000, v67
	v_lshlrev_b32_e32 v38, 16, v68
	v_and_b32_e32 v39, 0xffff0000, v68
	v_pk_fma_f32 v[20:21], v[54:55], v[24:25], v[20:21]
	v_pk_fma_f32 v[98:99], v[62:63], v[142:143], v[98:99]
	v_pk_fma_f32 v[22:23], v[56:57], v[26:27], v[22:23]
	v_mul_f32_e32 v24, 0xbfb8aa3b, v20
	v_mul_f32_e32 v25, 0xbfb8aa3b, v21
	v_pk_fma_f32 v[16:17], v[28:29], v[38:39], v[16:17]
	v_pk_fma_f32 v[96:97], v[28:29], v[110:111], v[98:99]
	v_add_f32_e32 v32, 1.0, v32
	v_mul_f32_e32 v99, 0xbfb8aa3b, v74
	v_exp_f32_e32 v24, v24
	v_exp_f32_e32 v25, v25
	v_mul_f32_e32 v26, 0xbfb8aa3b, v22
	v_mul_f32_e32 v27, 0xbfb8aa3b, v23
	v_mul_f32_e32 v28, 0xbfb8aa3b, v16
	v_mul_f32_e32 v29, 0xbfb8aa3b, v17
	v_rcp_f32_e32 v98, v32
	v_add_f32_e32 v32, 1.0, v102
	v_exp_f32_e32 v102, v99
	v_mul_f32_e32 v99, 0xbfb8aa3b, v75
	v_exp_f32_e32 v26, v26
	v_exp_f32_e32 v27, v27
	v_exp_f32_e32 v28, v28
	v_exp_f32_e32 v29, v29
	v_exp_f32_e32 v103, v99
	v_add_f32_e32 v24, 1.0, v24
	v_add_f32_e32 v25, 1.0, v25
	v_rcp_f32_e32 v99, v32
	v_add_f32_e32 v32, 1.0, v102
	v_rcp_f32_e32 v24, v24
	v_rcp_f32_e32 v25, v25
	v_add_f32_e32 v26, 1.0, v26
	v_add_f32_e32 v27, 1.0, v27
	v_add_f32_e32 v28, 1.0, v28
	v_add_f32_e32 v29, 1.0, v29
	v_rcp_f32_e32 v102, v32
	v_add_f32_e32 v32, 1.0, v103
	v_mul_f32_e32 v103, 0xbfb8aa3b, v96
	v_rcp_f32_e32 v26, v26
	v_rcp_f32_e32 v27, v27
	v_rcp_f32_e32 v28, v28
	v_rcp_f32_e32 v29, v29
	v_exp_f32_e32 v141, v103
	v_mul_f32_e32 v103, 0xbfb8aa3b, v97
	v_exp_f32_e32 v147, v103
	v_pk_mul_f32 v[20:21], v[20:21], v[24:25]
	v_pk_mul_f32 v[22:23], v[22:23], v[26:27]
	v_pk_mul_f32 v[24:25], v[16:17], v[28:29]
	v_cvt_pk_bf16_f32 v16, v20, v21
	v_lshl_add_u64 v[20:21], s[18:19], 0, v[88:89]
	v_rcp_f32_e32 v103, v32
	v_add_f32_e32 v32, 1.0, v141
	v_mul_f32_e32 v141, 0xbfb8aa3b, v92
	v_pk_fma_f32 v[18:19], v[48:49], v[144:145], v[18:19]
	v_cvt_pk_bf16_f32 v17, v22, v23
	v_mad_i64_i32 v[22:23], s[0:1], v140, s77, v[20:21]
	v_rcp_f32_e32 v146, v32
	v_add_f32_e32 v32, 1.0, v147
	v_exp_f32_e32 v141, v141
	v_mul_f32_e32 v147, 0xbfb8aa3b, v93
	v_pk_fma_f32 v[18:19], v[64:65], v[112:113], v[18:19]
	v_lshlrev_b32_e32 v40, 16, v69
	v_and_b32_e32 v41, 0xffff0000, v69
	global_store_dwordx4 v[22:23], v[8:11], off
	v_or_b32_e32 v22, 1, v140
	v_exp_f32_e32 v149, v147
	v_pk_fma_f32 v[18:19], v[30:31], v[40:41], v[18:19]
	v_mad_i64_i32 v[22:23], s[0:1], v22, s77, v[20:21]
	v_mul_f32_e32 v30, 0xbfb8aa3b, v18
	v_mul_f32_e32 v31, 0xbfb8aa3b, v19
	global_store_dwordx4 v[22:23], v[12:15], off
	v_or_b32_e32 v22, 2, v140
	v_exp_f32_e32 v30, v30
	v_exp_f32_e32 v31, v31
	v_mad_i64_i32 v[22:23], s[0:1], v22, s77, v[20:21]
	v_rcp_f32_e32 v147, v32
	v_add_f32_e32 v32, 1.0, v141
	global_store_dwordx4 v[22:23], v[42:45], off
	v_or_b32_e32 v22, 3, v140
	v_rcp_f32_e32 v148, v32
	v_add_f32_e32 v32, 1.0, v149
	v_mad_i64_i32 v[22:23], s[0:1], v22, s77, v[20:21]
	v_rcp_f32_e32 v149, v32
	global_store_dwordx4 v[22:23], v[70:73], off
	v_or_b32_e32 v22, 4, v140
	v_add_f32_e32 v30, 1.0, v30
	v_add_f32_e32 v31, 1.0, v31
	v_mad_i64_i32 v[22:23], s[0:1], v22, s77, v[20:21]
	v_rcp_f32_e32 v30, v30
	v_rcp_f32_e32 v31, v31
	global_store_dwordx4 v[22:23], v[78:81], off
	v_or_b32_e32 v22, 5, v140
	v_mad_i64_i32 v[22:23], s[0:1], v22, s77, v[20:21]
	v_pk_mul_f32 v[76:77], v[76:77], v[98:99]
	v_pk_mul_f32 v[98:99], v[74:75], v[102:103]
	v_pk_mul_f32 v[96:97], v[96:97], v[146:147]
	v_pk_mul_f32 v[92:93], v[92:93], v[148:149]
	global_store_dwordx4 v[22:23], v[82:85], off
	v_or_b32_e32 v22, 6, v140
	v_cvt_pk_bf16_f32 v74, v76, v77
	v_cvt_pk_bf16_f32 v75, v98, v99
	v_cvt_pk_bf16_f32 v76, v96, v97
	v_cvt_pk_bf16_f32 v77, v92, v93
	v_mad_i64_i32 v[22:23], s[0:1], v22, s77, v[20:21]
	v_pk_mul_f32 v[26:27], v[18:19], v[30:31]
	global_store_dwordx4 v[22:23], v[74:77], off
	v_or_b32_e32 v22, 7, v140
	v_cvt_pk_bf16_f32 v18, v24, v25
	v_cvt_pk_bf16_f32 v19, v26, v27
	v_mad_i64_i32 v[20:21], s[0:1], v22, s77, v[20:21]
	global_store_dwordx4 v[20:21], v[16:19], off
	v_mov_b32_e32 v20, v162
	v_mov_b32_e32 v21, v163
	v_mov_b32_e32 v22, v164
	s_mov_b32 s0, 0xbfb8aa3b
	v_add_f32_e32 v20, v20, v21
	v_mul_f32_e64 v21, |v20|, s0
	v_exp_f32_e32 v23, v21
	v_max_f32_e32 v24, 0, v20
	s_mov_b32 s0, 0x3f2aaaab
	v_add_f32_e32 v25, 1.0, v23
	v_add_f32_e32 v20, -1.0, v25
	v_sub_f32_e32 v21, v20, v25
	v_add_f32_e32 v21, 1.0, v21
	v_sub_f32_e32 v20, v23, v20
	v_add_f32_e32 v26, v20, v21
	v_frexp_mant_f32_e32 v27, v25
	v_cvt_f64_f32_e32 v[20:21], v25
	v_frexp_exp_i32_f64_e32 v20, v[20:21]
	v_cmp_gt_f32_e64 s[0:1], s0, v27
	s_nop 1
	v_subbrev_co_u32_e64 v20, s[0:1], 0, v20, s[0:1]
	v_sub_u32_e32 v21, 0, v20
	v_ldexp_f32 v25, v25, v21
	v_ldexp_f32 v21, v26, v21
	v_add_f32_e32 v26, -1.0, v25
	v_add_f32_e32 v29, 1.0, v25
	v_add_f32_e32 v27, 1.0, v26
	v_add_f32_e32 v30, -1.0, v29
	v_sub_f32_e32 v27, v25, v27
	v_sub_f32_e32 v25, v25, v30
	v_add_f32_e32 v27, v21, v27
	v_add_f32_e32 v21, v21, v25
	v_add_f32_e32 v25, v29, v21
	v_rcp_f32_e32 v30, v25
	v_add_f32_e32 v28, v26, v27
	v_sub_f32_e32 v26, v28, v26
	v_sub_f32_e32 v26, v27, v26
	v_sub_f32_e32 v27, v25, v29
	v_sub_f32_e32 v21, v21, v27
	v_mul_f32_e32 v27, v28, v30
	v_mul_f32_e32 v29, v25, v27
	v_fma_f32 v31, v27, v25, -v29
	v_fmac_f32_e32 v31, v27, v21
	v_add_f32_e32 v32, v29, v31
	v_sub_f32_e32 v38, v28, v32
	v_sub_f32_e32 v28, v28, v38
	v_sub_f32_e32 v29, v32, v29
	v_sub_f32_e32 v28, v28, v32
	v_add_f32_e32 v26, v26, v28
	v_sub_f32_e32 v28, v29, v31
	v_add_f32_e32 v26, v28, v26
	v_add_f32_e32 v28, v38, v26
	v_mul_f32_e32 v29, v30, v28
	v_mul_f32_e32 v31, v25, v29
	v_fma_f32 v25, v29, v25, -v31
	v_fmac_f32_e32 v25, v29, v21
	v_sub_f32_e32 v21, v38, v28
	v_add_f32_e32 v21, v26, v21
	v_add_f32_e32 v26, v31, v25
	v_sub_f32_e32 v32, v28, v26
	v_sub_f32_e32 v28, v28, v32
	v_sub_f32_e32 v31, v26, v31
	v_sub_f32_e32 v26, v28, v26
	v_add_f32_e32 v21, v21, v26
	v_sub_f32_e32 v25, v31, v25
	v_cvt_f32_i32_e32 v20, v20
	v_add_f32_e32 v21, v25, v21
	v_add_f32_e32 v25, v27, v29
	v_add_f32_e32 v21, v32, v21
	v_sub_f32_e32 v26, v25, v27
	v_mul_f32_e32 v21, v30, v21
	v_sub_f32_e32 v26, v29, v26
	v_add_f32_e32 v21, v26, v21
	v_mul_f32_e32 v29, 0x3f317218, v20
	s_mov_b32 s0, 0x3f317218
	v_add_f32_e32 v26, v25, v21
	v_fma_f32 v30, v20, s0, -v29
	v_mul_f32_e32 v27, v26, v26
	v_fmac_f32_e32 v30, 0xb102e308, v20
	v_sub_f32_e32 v20, v26, v25
	v_fmamk_f32 v28, v27, 0x3e9b6dac, v229
	v_sub_f32_e32 v20, v21, v20
	v_add_f32_e32 v21, v29, v30
	v_fmaak_f32 v28, v27, v28, 0x3f2aaada
	v_sub_f32_e32 v25, v21, v29
	v_ldexp_f32 v29, v26, 1
	v_mul_f32_e32 v26, v26, v27
	v_mul_f32_e32 v26, v26, v28
	v_add_f32_e32 v27, v29, v26
	v_sub_f32_e32 v28, v27, v29
	v_ldexp_f32 v20, v20, 1
	v_sub_f32_e32 v26, v26, v28
	v_add_f32_e32 v20, v20, v26
	v_add_f32_e32 v26, v27, v20
	v_sub_f32_e32 v27, v26, v27
	v_sub_f32_e32 v20, v20, v27
	v_add_f32_e32 v27, v21, v26
	v_sub_f32_e32 v28, v27, v21
	v_sub_f32_e32 v29, v27, v28
	v_sub_f32_e32 v25, v30, v25
	v_sub_f32_e32 v21, v21, v29
	v_sub_f32_e32 v26, v26, v28
	v_add_f32_e32 v21, v26, v21
	v_add_f32_e32 v26, v25, v20
	v_sub_f32_e32 v28, v26, v25
	v_sub_f32_e32 v29, v26, v28
	v_sub_f32_e32 v25, v25, v29
	v_sub_f32_e32 v20, v20, v28
	v_add_f32_e32 v21, v26, v21
	v_add_f32_e32 v20, v20, v25
	v_add_f32_e32 v25, v27, v21
	v_sub_f32_e32 v26, v25, v27
	v_sub_f32_e32 v21, v21, v26
	v_add_f32_e32 v20, v20, v21
	s_mov_b32 s0, 0x7f800000
	v_add_f32_e32 v20, v25, v20
	v_cmp_neq_f32_e64 s[0:1], s0, v23
	v_mul_f32_e32 v21, 0x3fb8aa3b, v22
	v_exp_f32_e32 v21, v21
	v_cndmask_b32_e64 v20, v234, v20, s[0:1]
	v_cmp_ngt_f32_e64 s[0:1], -1.0, v23
	s_nop 1
	v_cndmask_b32_e64 v20, v235, v20, s[0:1]
	v_cmp_neq_f32_e64 s[0:1], -1.0, v23
	s_nop 1
	v_cndmask_b32_e64 v20, v236, v20, s[0:1]
	s_mov_b32 s0, 0x33800000
	v_cmp_lt_f32_e64 s[0:1], |v23|, s0
	s_nop 1
	v_cndmask_b32_e64 v20, v20, v23, s[0:1]
	v_add_f32_e32 v20, v24, v20
	v_mul_f32_e64 v22, v20, -v21
	ds_bpermute_b32 v23, v125, v22
	s_waitcnt lgkmcnt(0)
	v_fma_f32 v21, v20, -v21, v23
	v_cndmask_b32_e32 v21, v21, v22, vcc
	ds_bpermute_b32 v22, v126, v21
	v_add3_u32 v23, s7, v122, v134
	ds_write_b128 v23, v[0:3]
	ds_write_b128 v23, v[4:7] offset:288
	ds_write_b128 v138, v[8:11]
	ds_write_b128 v138, v[12:15] offset:160
	ds_write_b128 v138, v[42:45] offset:320
	ds_write_b128 v138, v[70:73] offset:480
	ds_write_b128 v138, v[78:81] offset:640
	ds_write_b128 v138, v[82:85] offset:800
	ds_write_b128 v138, v[74:77] offset:960
	ds_write_b128 v138, v[16:19] offset:1120
	s_waitcnt lgkmcnt(10)
	v_add_f32_e32 v22, v21, v22
	v_cndmask_b32_e64 v21, v22, v21, s[36:37]
	ds_bpermute_b32 v22, v127, v21
	s_waitcnt lgkmcnt(0)
	v_add_f32_e32 v22, v21, v22
	v_cndmask_b32_e64 v21, v22, v21, s[38:39]
	ds_bpermute_b32 v22, v128, v21
	s_waitcnt lgkmcnt(0)
	v_add_f32_e32 v0, v21, v22
	v_cndmask_b32_e64 v0, v0, v21, s[40:41]
	ds_bpermute_b32 v1, v129, v0
	s_waitcnt lgkmcnt(0)
	v_add_f32_e32 v1, v0, v1
	v_cndmask_b32_e64 v0, v1, v0, s[42:43]
	ds_bpermute_b32 v1, v130, v0
	s_waitcnt lgkmcnt(0)
	v_add_f32_e32 v1, v0, v1
	v_cndmask_b32_e64 v0, v1, v0, s[44:45]
	ds_write_b32 v132, v20
	ds_write_b32 v133, v0
	s_add_i32 s2, s4, s25
	s_lshl_b32 s2, s2, 9
	v_lshl_add_u32 v158, v120, 3, s2
	v_mov_b32_e32 v159, 0
	v_lshl_add_u64 v[158:159], s[16:17], 0, v[158:159]
	s_mov_b64 s[2:3], 0x5d600000
	v_mov_b32_e32 v160, v20
	v_mov_b32_e32 v161, v0
	v_lshl_add_u64 v[158:159], v[158:159], 0, s[2:3]
	global_store_dwordx2 v[158:159], v[160:161], off
	v_mov_b32_e32 v0, s35
	s_waitcnt lgkmcnt(0)
	s_waitcnt lgkmcnt(0)
	s_barrier
	ds_read_b32 v22, v0 offset:252
	s_and_saveexec_b64 s[0:1], vcc
	s_cbranch_execz .LBB0_429
	s_waitcnt lgkmcnt(0)
	v_mul_f32_e32 v0, 0x3fb8aa3b, v22
	s_add_i32 s2, s4, s25
	v_exp_f32_e32 v0, v0
	s_ashr_i32 s3, s2, 31
	s_lshl_b64 s[2:3], s[2:3], 2
	s_add_u32 s2, s26, s2
	s_addc_u32 s3, s27, s3
	global_store_dword v33, v0, s[2:3]

.LBB0_1238:
	s_and_b32 s21, s54, 7
	s_lshl_b32 s0, s21, 3
	s_add_i32 s22, s0, s34
	s_lshl_b32 s14, s22, 6
	s_ashr_i32 s20, s54, 3
	s_ashr_i32 s15, s14, 31
	s_lshl_b32 s55, s20, 6
	s_lshl_b64 s[16:17], s[14:15], 1
	s_waitcnt vmcnt(8)
	v_or_b32_e32 v30, s55, v167
	v_lshl_add_u64 v[28:29], v[158:159], 0, s[16:17]
	v_mad_i64_i32 v[0:1], s[0:1], v30, s77, v[28:29]
	v_or_b32_e32 v4, 8, v30
	global_load_dwordx4 v[0:3], v[0:1], off
	v_mad_i64_i32 v[4:5], s[0:1], v4, s77, v[28:29]
	v_or_b32_e32 v8, 16, v30
	global_load_dwordx4 v[4:7], v[4:5], off
	v_mad_i64_i32 v[8:9], s[0:1], v8, s77, v[28:29]
	v_or_b32_e32 v12, 24, v30
	global_load_dwordx4 v[8:11], v[8:9], off
	v_mad_i64_i32 v[12:13], s[0:1], v12, s77, v[28:29]
	v_or_b32_e32 v16, 32, v30
	global_load_dwordx4 v[12:15], v[12:13], off
	v_mad_i64_i32 v[16:17], s[0:1], v16, s77, v[28:29]
	v_or_b32_e32 v20, 40, v30
	global_load_dwordx4 v[16:19], v[16:17], off
	v_mad_i64_i32 v[20:21], s[0:1], v20, s77, v[28:29]
	v_or_b32_e32 v24, 48, v30
	global_load_dwordx4 v[20:23], v[20:21], off
	v_mad_i64_i32 v[24:25], s[0:1], v24, s77, v[28:29]
	v_or_b32_e32 v30, 56, v30
	global_load_dwordx4 v[24:27], v[24:25], off
	v_mad_i64_i32 v[28:29], s[0:1], v30, s77, v[28:29]
	global_load_dwordx4 v[28:31], v[28:29], off
	s_lshl_b32 s0, s20, 6
	s_add_i32 s0, s0, s22
	s_lshl_b32 s0, s0, 9
	v_lshl_add_u32 v198, v161, 3, s0
	v_mov_b32_e32 v199, 0
	v_lshl_add_u64 v[198:199], s[24:25], 0, v[198:199]
	s_mov_b64 s[0:1], 0x400000
	s_nop 0
	v_lshl_add_u64 v[198:199], v[198:199], 0, s[0:1]
	global_load_dwordx2 v[198:199], v[198:199], off
	s_ashr_i32 s23, s22, 31
	s_lshl_b64 s[18:19], s[22:23], 2
	s_add_u32 s0, s26, s18
	s_addc_u32 s1, s27, s19
	v_or_b32_e32 v174, s55, v166
	v_lshlrev_b32_e32 v32, 1, v160
	s_movk_i32 s56, 0x2000
	v_mov_b32_e32 v173, v33
	s_waitcnt vmcnt(8)
	ds_write_b128 v213, v[0:3]
	s_waitcnt vmcnt(7)
	ds_write_b128 v213, v[4:7] offset:1280
	s_waitcnt vmcnt(6)
	ds_write_b128 v213, v[8:11] offset:2560
	s_waitcnt vmcnt(5)
	ds_write_b128 v213, v[12:15] offset:3840
	s_waitcnt vmcnt(4)
	ds_write_b128 v213, v[16:19] offset:5120
	s_waitcnt vmcnt(3)
	ds_write_b128 v213, v[20:23] offset:6400
	s_waitcnt vmcnt(2)
	ds_write_b128 v213, v[24:27] offset:7680
	s_waitcnt vmcnt(1)
	ds_write_b128 v213, v[28:31] offset:8960
	s_lshl_b32 s86, s21, 8
	s_ashr_i32 s21, s20, 31
	s_waitcnt vmcnt(0)
	ds_write_b32 v190, v198
	ds_write_b32 v191, v199
	v_mov_b64_e32 v[0:1], s[8:9]
	v_mad_i64_i32 v[0:1], s[0:1], v174, s77, v[0:1]
	v_lshl_add_u64 v[0:1], v[0:1], 0, s[86:87]
	v_lshl_add_u64 v[8:9], v[0:1], 0, v[32:33]
	s_mov_b64 s[0:1], 0x2800
	v_lshl_add_u64 v[74:75], v[8:9], 0, s[0:1]
	v_add_co_u32_e64 v0, s[0:1], s56, v8
	s_movk_i32 s77, 0x3000
	s_nop 0
	v_addc_co_u32_e64 v1, s[0:1], 0, v9, s[0:1]
	s_mov_b32 s0, 0x32000
	s_nop 0
	v_add_co_u32_e64 v30, s[0:1], s0, v8
	global_load_dwordx4 v[4:7], v[0:1], off offset:2048
	s_nop 0
	global_load_dwordx4 v[0:3], v[74:75], off offset:64
	global_load_dwordx4 v[70:73], v[74:75], off offset:128
	global_load_dwordx4 v[66:69], v[74:75], off offset:192
	v_addc_co_u32_e64 v31, s[0:1], 0, v9, s[0:1]
	s_mov_b32 s0, 0x62000
	s_nop 0
	v_add_co_u32_e64 v88, s[0:1], s0, v8
	global_load_dwordx4 v[62:65], v[30:31], off offset:2048
	global_load_dwordx4 v[58:61], v[30:31], off offset:2112
	global_load_dwordx4 v[54:57], v[30:31], off offset:2176
	global_load_dwordx4 v[50:53], v[30:31], off offset:2240
	v_addc_co_u32_e64 v89, s[0:1], 0, v9, s[0:1]
	s_mov_b32 s0, 0x92000
	s_nop 0
	v_add_co_u32_e64 v86, s[0:1], s0, v8
	global_load_dwordx4 v[46:49], v[88:89], off offset:2048
	global_load_dwordx4 v[42:45], v[88:89], off offset:2112
	global_load_dwordx4 v[38:41], v[88:89], off offset:2176
	global_load_dwordx4 v[24:27], v[88:89], off offset:2240
	v_addc_co_u32_e64 v87, s[0:1], 0, v9, s[0:1]
	global_load_dwordx4 v[20:23], v[86:87], off offset:2048
	global_load_dwordx4 v[16:19], v[86:87], off offset:2112
	global_load_dwordx4 v[8:11], v[86:87], off offset:2176
	global_load_dwordx4 v[12:15], v[86:87], off offset:2240
	s_waitcnt lgkmcnt(0)
	ds_read2_b32 v[102:103], v192 offset1:16
	ds_read2_b32 v[28:29], v192 offset0:32 offset1:48
	global_load_dwordx4 v[82:85], v[74:75], off offset:-2048
	global_load_dwordx4 v[92:95], v[74:75], off offset:-1984
	global_load_dwordx4 v[96:99], v[74:75], off offset:-1920
	global_load_dwordx4 v[104:107], v[74:75], off offset:-1856
	s_waitcnt vmcnt(3)
	v_mfma_f32_16x16x32_bf16 v[74:77], v[82:85], v[4:7], 0
	ds_read_b64 v[100:101], v193
	ds_read_b32 v32, v195
	ds_read_b32 v90, v196
	ds_read_b32 v118, v197
	ds_read_b32 v91, v208
	s_mov_b32 s0, 0x5040100
	s_waitcnt vmcnt(2)
	v_mfma_f32_16x16x32_bf16 v[74:77], v[92:95], v[0:3], v[74:77]
	s_waitcnt vmcnt(1)
	v_mfma_f32_16x16x32_bf16 v[74:77], v[96:99], v[70:73], v[74:77]
	v_mfma_f32_16x16x32_bf16 v[108:111], v[82:85], v[62:65], 0
	s_waitcnt vmcnt(0)
	v_mfma_f32_16x16x32_bf16 v[78:81], v[104:107], v[66:69], v[74:77]
	s_waitcnt lgkmcnt(4)
	s_nop 3
	v_sub_f32_e32 v76, v103, v100
	v_min_f32_e32 v76, 0, v76
	v_mfma_f32_16x16x32_bf16 v[108:111], v[92:95], v[58:61], v[108:111]
	v_mul_f32_e32 v76, 0x3fb8aa3b, v76
	v_exp_f32_e32 v114, v76
	v_sub_f32_e32 v76, v103, v101
	v_min_f32_e32 v76, 0, v76
	v_mul_f32_e32 v76, 0x3fb8aa3b, v76
	v_mfma_f32_16x16x32_bf16 v[108:111], v[96:99], v[54:57], v[108:111]
	v_exp_f32_e32 v115, v76
	s_waitcnt lgkmcnt(3)
	v_sub_f32_e32 v76, v103, v32
	s_waitcnt lgkmcnt(1)
	v_sub_f32_e32 v77, v103, v118
	v_min_f32_e32 v76, 0, v76
	v_min_f32_e32 v77, 0, v77
	v_mul_f32_e32 v76, 0x3fb8aa3b, v76
	v_mul_f32_e32 v77, 0x3fb8aa3b, v77
	v_exp_f32_e32 v76, v76
	v_exp_f32_e32 v77, v77
	v_mfma_f32_16x16x32_bf16 v[108:111], v[104:107], v[50:53], v[108:111]
	v_sub_f32_e32 v74, v102, v100
	v_min_f32_e32 v74, 0, v74
	v_mul_f32_e32 v74, 0x3fb8aa3b, v74
	s_waitcnt lgkmcnt(0)
	v_pk_mul_f32 v[76:77], v[90:91], v[76:77]
	v_exp_f32_e32 v119, v74
	v_sub_f32_e32 v74, v102, v101
	s_nop 0
	v_pk_mul_f32 v[76:77], v[76:77], v[110:111]
	v_mfma_f32_16x16x32_bf16 v[110:113], v[82:85], v[46:49], 0
	v_min_f32_e32 v74, 0, v74
	v_mul_f32_e32 v74, 0x3fb8aa3b, v74
	v_exp_f32_e32 v120, v74
	v_mfma_f32_16x16x32_bf16 v[82:85], v[82:85], v[20:23], 0
	v_sub_f32_e32 v74, v102, v32
	v_sub_f32_e32 v75, v102, v118
	v_min_f32_e32 v74, 0, v74
	v_min_f32_e32 v75, 0, v75
	v_mfma_f32_16x16x32_bf16 v[82:85], v[92:95], v[16:19], v[82:85]
	v_mul_f32_e32 v74, 0x3fb8aa3b, v74
	v_mul_f32_e32 v75, 0x3fb8aa3b, v75
	v_exp_f32_e32 v74, v74
	v_exp_f32_e32 v75, v75
	v_mfma_f32_16x16x32_bf16 v[82:85], v[96:99], v[8:11], v[82:85]
	v_mul_f32_e64 v74, v90, v74
	v_mul_f32_e64 v75, v91, v75
	v_mfma_f32_16x16x32_bf16 v[110:113], v[92:95], v[42:45], v[110:113]
	v_mul_f32_e64 v74, v74, v80
	v_mul_f32_e64 v75, v75, v81
	v_sub_f32_e32 v80, v28, v100
	v_min_f32_e32 v80, 0, v80
	v_mfma_f32_16x16x32_bf16 v[92:95], v[104:107], v[12:15], v[82:85]
	v_mul_f32_e32 v80, 0x3fb8aa3b, v80
	v_exp_f32_e32 v116, v80
	v_sub_f32_e32 v80, v28, v101
	v_sub_f32_e32 v82, v29, v100
	v_sub_f32_e32 v83, v29, v101
	v_min_f32_e32 v82, 0, v82
	v_min_f32_e32 v83, 0, v83
	v_mfma_f32_16x16x32_bf16 v[110:113], v[96:99], v[38:41], v[110:113]
	v_mul_f32_e32 v82, 0x3fb8aa3b, v82
	v_mul_f32_e32 v83, 0x3fb8aa3b, v83
	ds_read_b64 v[96:97], v194
	v_min_f32_e32 v80, 0, v80
	v_exp_f32_e32 v82, v82
	v_exp_f32_e32 v83, v83
	v_mul_f32_e32 v80, 0x3fb8aa3b, v80
	v_exp_f32_e32 v117, v80
	v_sub_f32_e32 v80, v28, v32
	v_sub_f32_e32 v32, v29, v32
	v_min_f32_e32 v32, 0, v32
	s_waitcnt lgkmcnt(0)
	v_pk_mul_f32 v[82:83], v[96:97], v[82:83]
	v_mul_f32_e32 v32, 0x3fb8aa3b, v32
	v_sub_f32_e32 v81, v28, v118
	v_pk_mul_f32 v[82:83], v[82:83], v[92:93]
	v_exp_f32_e32 v92, v32
	v_sub_f32_e32 v32, v29, v118
	v_min_f32_e32 v80, 0, v80
	v_min_f32_e32 v81, 0, v81
	v_min_f32_e32 v32, 0, v32
	v_mul_f32_e32 v80, 0x3fb8aa3b, v80
	v_mul_f32_e32 v81, 0x3fb8aa3b, v81
	v_mul_f32_e32 v84, v96, v119
	v_mul_f32_e32 v32, 0x3fb8aa3b, v32
	v_exp_f32_e32 v80, v80
	v_exp_f32_e32 v81, v81
	v_mul_f32_e32 v78, v84, v78
	v_exp_f32_e32 v93, v32
	v_mfma_f32_16x16x32_bf16 v[110:113], v[104:107], v[24:27], v[110:113]
	v_cndmask_b32_e64 v126, v78, 0, s[46:47]
	v_mul_f32_e32 v78, v97, v120
	v_mul_f32_e32 v78, v78, v79
	v_cndmask_b32_e64 v127, 0, v78, s[48:49]
	v_pk_mul_f32 v[78:79], v[96:97], v[114:115]
	v_pk_mul_f32 v[80:81], v[90:91], v[80:81]
	v_pk_mul_f32 v[84:85], v[78:79], v[108:109]
	v_pk_mul_f32 v[78:79], v[96:97], v[116:117]
	v_pk_mul_f32 v[90:91], v[90:91], v[92:93]
	v_pk_mul_f32 v[78:79], v[78:79], v[110:111]
	v_pk_mul_f32 v[90:91], v[90:91], v[94:95]
	global_load_dwordx4 v[92:95], v[30:31], off
	global_load_dwordx4 v[96:99], v[30:31], off offset:64
	global_load_dwordx4 v[104:107], v[30:31], off offset:128
	global_load_dwordx4 v[108:111], v[30:31], off offset:192
	v_pk_mul_f32 v[80:81], v[80:81], v[112:113]
	ds_read_b128 v[112:115], v193 offset:64
	s_waitcnt vmcnt(3)
	v_mfma_f32_16x16x32_bf16 v[116:119], v[92:95], v[62:65], 0
	s_waitcnt lgkmcnt(0)
	v_sub_f32_e32 v30, v103, v112
	v_min_f32_e32 v30, 0, v30
	v_mul_f32_e32 v30, 0x3fb8aa3b, v30
	v_mfma_f32_16x16x32_bf16 v[120:123], v[92:95], v[46:49], 0
	v_exp_f32_e32 v32, v30
	v_sub_f32_e32 v30, v103, v113
	v_min_f32_e32 v30, 0, v30
	v_mfma_f32_16x16x32_bf16 v[92:95], v[92:95], v[20:23], 0
	v_mul_f32_e32 v30, 0x3fb8aa3b, v30
	v_exp_f32_e32 v128, v30
	v_sub_f32_e32 v100, v28, v112
	s_waitcnt vmcnt(2)
	v_mfma_f32_16x16x32_bf16 v[116:119], v[96:99], v[58:61], v[116:119]
	v_sub_f32_e32 v101, v28, v113
	v_min_f32_e32 v100, 0, v100
	v_min_f32_e32 v101, 0, v101
	v_mfma_f32_16x16x32_bf16 v[120:123], v[96:99], v[42:45], v[120:123]
	v_mul_f32_e32 v100, 0x3fb8aa3b, v100
	v_mul_f32_e32 v101, 0x3fb8aa3b, v101
	v_exp_f32_e32 v100, v100
	v_mfma_f32_16x16x32_bf16 v[92:95], v[96:99], v[16:19], v[92:95]
	v_sub_f32_e32 v96, v29, v112
	v_min_f32_e32 v96, 0, v96
	v_mul_f32_e32 v96, 0x3fb8aa3b, v96
	s_waitcnt vmcnt(1)
	v_mfma_f32_16x16x32_bf16 v[116:119], v[104:107], v[54:57], v[116:119]
	v_exp_f32_e32 v101, v101
	v_sub_f32_e32 v30, v103, v114
	v_sub_f32_e32 v31, v103, v115
	v_mfma_f32_16x16x32_bf16 v[120:123], v[104:107], v[38:41], v[120:123]
	v_min_f32_e32 v30, 0, v30
	v_min_f32_e32 v31, 0, v31
	v_sub_f32_e32 v124, v28, v114
	v_mfma_f32_16x16x32_bf16 v[92:95], v[104:107], v[8:11], v[92:95]
	v_exp_f32_e32 v104, v96
	v_sub_f32_e32 v96, v29, v113
	v_min_f32_e32 v96, 0, v96
	v_mul_f32_e32 v96, 0x3fb8aa3b, v96
	v_exp_f32_e32 v105, v96
	ds_read_b128 v[96:99], v194 offset:64
	s_waitcnt vmcnt(0)
	v_mfma_f32_16x16x32_bf16 v[116:119], v[108:111], v[50:53], v[116:119]
	v_sub_f32_e32 v125, v28, v115
	v_mul_f32_e32 v30, 0x3fb8aa3b, v30
	v_mul_f32_e32 v31, 0x3fb8aa3b, v31
	s_waitcnt lgkmcnt(0)
	v_mul_f32_e32 v32, v96, v32
	v_mfma_f32_16x16x32_bf16 v[120:123], v[108:111], v[24:27], v[120:123]
	s_nop 1
	v_mul_f32_e32 v32, v32, v116
	v_pk_mul_f32 v[100:101], v[96:97], v[100:101]
	v_min_f32_e32 v124, 0, v124
	v_mfma_f32_16x16x32_bf16 v[92:95], v[108:111], v[12:15], v[92:95]
	v_cndmask_b32_e64 v108, v32, 0, s[46:47]
	v_mul_f32_e32 v32, v97, v128
	v_mul_f32_e32 v32, v32, v117
	v_cndmask_b32_e64 v109, 0, v32, s[48:49]
	v_sub_f32_e32 v32, v29, v114
	v_min_f32_e32 v32, 0, v32
	v_pk_mul_f32 v[96:97], v[96:97], v[104:105]
	v_mul_f32_e32 v32, 0x3fb8aa3b, v32
	v_min_f32_e32 v125, 0, v125
	v_pk_mul_f32 v[92:93], v[96:97], v[92:93]
	v_exp_f32_e32 v96, v32
	v_sub_f32_e32 v32, v29, v115
	v_exp_f32_e32 v30, v30
	v_exp_f32_e32 v31, v31
	v_mul_f32_e32 v124, 0x3fb8aa3b, v124
	v_mul_f32_e32 v125, 0x3fb8aa3b, v125
	v_min_f32_e32 v32, 0, v32
	v_exp_f32_e32 v124, v124
	v_exp_f32_e32 v125, v125
	v_mul_f32_e32 v32, 0x3fb8aa3b, v32
	v_exp_f32_e32 v97, v32
	v_pk_mul_f32 v[30:31], v[98:99], v[30:31]
	v_pk_mul_f32 v[100:101], v[100:101], v[120:121]
	v_pk_mul_f32 v[104:105], v[30:31], v[118:119]
	v_pk_mul_f32 v[30:31], v[98:99], v[124:125]
	v_cvt_pk_bf16_f32 v78, v78, v79
	v_pk_mul_f32 v[106:107], v[30:31], v[122:123]
	v_pk_mul_f32 v[30:31], v[98:99], v[96:97]
	v_cvt_pk_bf16_f32 v79, v80, v81
	v_pk_mul_f32 v[94:95], v[30:31], v[94:95]
	v_cvt_pk_bf16_f32 v31, v74, v75
	v_cvt_pk_bf16_f32 v75, v76, v77
	v_cvt_pk_bf16_f32 v77, v104, v105
	v_cvt_pk_bf16_f32 v74, v84, v85
	v_cndmask_b32_e64 v84, v77, 0, s[52:53]
	v_lshrrev_b32_e32 v77, 16, v77
	v_cndmask_b32_e64 v77, v77, 0, s[50:51]
	v_perm_b32 v77, v77, v84, s0
	v_cvt_pk_bf16_f32 v80, v100, v101
	v_cvt_pk_bf16_f32 v81, v106, v107
	v_cvt_pk_bf16_f32 v82, v82, v83
	v_cvt_pk_bf16_f32 v83, v90, v91
	v_cvt_pk_bf16_f32 v84, v92, v93
	v_cvt_pk_bf16_f32 v85, v94, v95
	global_load_dwordx4 v[90:93], v[88:89], off
	global_load_dwordx4 v[94:97], v[88:89], off offset:64
	global_load_dwordx4 v[98:101], v[88:89], off offset:128
	global_load_dwordx4 v[104:107], v[88:89], off offset:192
	v_cvt_pk_bf16_f32 v76, v108, v109
	ds_read_b128 v[108:111], v193 offset:128
	s_waitcnt vmcnt(3)
	v_mfma_f32_16x16x32_bf16 v[112:115], v[90:93], v[46:49], 0
	s_waitcnt lgkmcnt(0)
	v_sub_f32_e32 v88, v28, v108
	v_min_f32_e32 v88, 0, v88
	v_mul_f32_e32 v88, 0x3fb8aa3b, v88
	v_exp_f32_e32 v118, v88
	v_sub_f32_e32 v88, v28, v109
	v_min_f32_e32 v88, 0, v88
	v_mul_f32_e32 v88, 0x3fb8aa3b, v88
	v_exp_f32_e32 v119, v88
	v_sub_f32_e32 v88, v28, v110
	v_min_f32_e32 v88, 0, v88
	v_mul_f32_e32 v88, 0x3fb8aa3b, v88
	v_exp_f32_e32 v116, v88
	v_sub_f32_e32 v88, v28, v111
	v_min_f32_e32 v88, 0, v88
	v_mul_f32_e32 v88, 0x3fb8aa3b, v88
	v_exp_f32_e32 v117, v88
	v_mfma_f32_16x16x32_bf16 v[88:91], v[90:93], v[20:23], 0
	v_cndmask_b32_e64 v32, v31, 0, s[52:53]
	v_lshrrev_b32_e32 v31, 16, v31
	v_cndmask_b32_e64 v31, v31, 0, s[50:51]
	s_waitcnt vmcnt(2)
	v_mfma_f32_16x16x32_bf16 v[88:91], v[94:97], v[16:19], v[88:91]
	v_perm_b32 v31, v31, v32, s0
	v_cvt_pk_bf16_f32 v30, v126, v127
	v_mul_f32_e32 v28, 0x3fb8aa3b, v28
	s_waitcnt vmcnt(1)
	v_mfma_f32_16x16x32_bf16 v[88:91], v[98:101], v[8:11], v[88:91]
	v_exp_f32_e32 v178, v28
	v_mul_f32_e32 v28, 0x3fb8aa3b, v29
	v_exp_f32_e32 v28, v28
	s_waitcnt vmcnt(0)
	v_mfma_f32_16x16x32_bf16 v[90:93], v[104:107], v[12:15], v[88:91]
	v_mov_b32_e32 v32, v33
	s_nop 1
	v_sub_f32_e32 v88, v29, v108
	v_sub_f32_e32 v89, v29, v109
	v_mfma_f32_16x16x32_bf16 v[112:115], v[94:97], v[42:45], v[112:115]
	v_min_f32_e32 v88, 0, v88
	v_min_f32_e32 v89, 0, v89
	v_mul_f32_e32 v88, 0x3fb8aa3b, v88
	v_mul_f32_e32 v89, 0x3fb8aa3b, v89
	ds_read_b128 v[94:97], v194 offset:128
	v_exp_f32_e32 v88, v88
	v_exp_f32_e32 v89, v89
	v_mfma_f32_16x16x32_bf16 v[112:115], v[98:101], v[38:41], v[112:115]
	s_waitcnt lgkmcnt(0)
	v_mul_f32_e32 v98, v94, v118
	v_pk_mul_f32 v[88:89], v[94:95], v[88:89]
	v_mfma_f32_16x16x32_bf16 v[112:115], v[104:107], v[24:27], v[112:115]
	v_mul_f32_e64 v90, v88, v90
	v_mul_f32_e64 v91, v89, v91
	v_sub_f32_e32 v88, v29, v110
	v_min_f32_e32 v88, 0, v88
	v_mul_f32_e32 v88, 0x3fb8aa3b, v88
	v_exp_f32_e32 v94, v88
	v_sub_f32_e32 v88, v29, v111
	v_min_f32_e32 v88, 0, v88
	v_mul_f32_e32 v98, v98, v112
	v_mul_f32_e32 v88, 0x3fb8aa3b, v88
	v_cndmask_b32_e64 v120, v98, 0, s[46:47]
	v_mul_f32_e32 v98, v95, v119
	v_exp_f32_e32 v95, v88
	v_mul_f32_e32 v98, v98, v113
	v_cndmask_b32_e64 v121, 0, v98, s[48:49]
	v_pk_mul_f32 v[88:89], v[96:97], v[116:117]
	v_pk_mul_f32 v[94:95], v[96:97], v[94:95]
	v_pk_mul_f32 v[88:89], v[88:89], v[114:115]
	v_pk_mul_f32 v[92:93], v[94:95], v[92:93]
	global_load_dwordx4 v[94:97], v[86:87], off
	global_load_dwordx4 v[98:101], v[86:87], off offset:64
	global_load_dwordx4 v[104:107], v[86:87], off offset:128
	global_load_dwordx4 v[108:111], v[86:87], off offset:192
	s_waitcnt vmcnt(3)
	v_mfma_f32_16x16x32_bf16 v[94:97], v[94:97], v[20:23], 0
	ds_read_b128 v[112:115], v193 offset:192
	ds_read_b128 v[116:119], v194 offset:192
	v_cvt_pk_bf16_f32 v90, v90, v91
	v_cvt_pk_bf16_f32 v91, v92, v93
	s_waitcnt vmcnt(2)
	v_mfma_f32_16x16x32_bf16 v[94:97], v[98:101], v[16:19], v[94:97]
	s_waitcnt lgkmcnt(1)
	v_sub_f32_e32 v86, v29, v112
	v_min_f32_e32 v86, 0, v86
	v_mul_f32_e32 v86, 0x3fb8aa3b, v86
	s_waitcnt vmcnt(1)
	v_mfma_f32_16x16x32_bf16 v[94:97], v[104:107], v[8:11], v[94:97]
	v_exp_f32_e32 v86, v86
	v_sub_f32_e32 v87, v29, v115
	v_min_f32_e32 v87, 0, v87
	s_waitcnt vmcnt(0)
	v_mfma_f32_16x16x32_bf16 v[94:97], v[108:111], v[12:15], v[94:97]
	s_waitcnt lgkmcnt(0)
	v_mul_f32_e32 v86, v116, v86
	v_mul_f32_e32 v87, 0x3fb8aa3b, v87
	v_exp_f32_e32 v87, v87
	s_nop 3
	v_mul_f32_e32 v86, v86, v94
	v_cndmask_b32_e64 v98, v86, 0, s[46:47]
	v_sub_f32_e32 v86, v29, v113
	v_min_f32_e32 v86, 0, v86
	v_mul_f32_e32 v86, 0x3fb8aa3b, v86
	v_exp_f32_e32 v86, v86
	s_nop 0
	v_mul_f32_e32 v86, v117, v86
	v_mul_f32_e32 v86, v86, v95
	v_cndmask_b32_e64 v99, 0, v86, s[48:49]
	v_sub_f32_e32 v86, v29, v114
	v_min_f32_e32 v86, 0, v86
	v_mul_f32_e32 v86, 0x3fb8aa3b, v86
	v_exp_f32_e32 v86, v86
	v_cvt_pk_bf16_f32 v92, v98, v99
	v_mul_f32_e32 v98, 0x3fb8aa3b, v102
	v_mul_f32_e32 v102, 0x3fb8aa3b, v103
	v_pk_mul_f32 v[86:87], v[118:119], v[86:87]
	v_exp_f32_e32 v180, v98
	v_pk_mul_f32 v[94:95], v[86:87], v[96:97]
	v_cvt_pk_bf16_f32 v87, v88, v89
	v_cvt_pk_bf16_f32 v93, v94, v95
	v_cndmask_b32_e64 v88, v87, 0, s[52:53]
	v_lshrrev_b32_e32 v87, 16, v87
	v_cndmask_b32_e64 v94, v93, 0, s[52:53]
	v_lshrrev_b32_e32 v93, 16, v93
	v_cndmask_b32_e64 v87, v87, 0, s[50:51]
	v_cndmask_b32_e64 v93, v93, 0, s[50:51]
	v_perm_b32 v87, v87, v88, s0
	v_perm_b32 v93, v93, v94, s0
	s_lshl_b64 s[0:1], s[20:21], 12
	s_lshl_b64 s[20:21], s[22:23], 6
	s_add_u32 s0, s20, s0
	s_addc_u32 s1, s21, s1
	v_mov_b32_e32 v95, s1
	v_or_b32_e32 v94, s0, v166
	v_lshlrev_b64 v[94:95], 8, v[94:95]
	v_lshl_add_u64 v[142:143], v[164:165], 0, v[94:95]
	v_cvt_pk_bf16_f32 v86, v120, v121
	global_load_dwordx4 v[106:109], v[142:143], off
	global_load_dwordx4 v[110:113], v[142:143], off offset:64
	global_load_dwordx4 v[114:117], v[142:143], off offset:128
	global_load_dwordx4 v[118:121], v[142:143], off offset:192
	s_waitcnt vmcnt(3)
	v_mfma_f32_16x16x32_bf16 v[94:97], v[106:109], v[4:7], 0
	v_exp_f32_e32 v176, v102
	s_movk_i32 s0, 0x1000
	v_mfma_f32_16x16x32_bf16 v[98:101], v[106:109], v[62:65], 0
	v_mov_b32_e32 v88, v33
	v_mov_b32_e32 v89, v33
	v_mfma_f32_16x16x32_bf16 v[102:105], v[106:109], v[46:49], 0
	v_mfma_f32_16x16x32_bf16 v[106:109], v[106:109], v[20:23], 0
	s_waitcnt vmcnt(2)
	v_mfma_f32_16x16x32_bf16 v[94:97], v[110:113], v[0:3], v[94:97]
	v_mfma_f32_16x16x32_bf16 v[98:101], v[110:113], v[58:61], v[98:101]
	v_mfma_f32_16x16x32_bf16 v[102:105], v[110:113], v[42:45], v[102:105]
	v_mfma_f32_16x16x32_bf16 v[106:109], v[110:113], v[16:19], v[106:109]
	v_add_co_u32_e64 v110, s[0:1], s0, v142
	s_nop 1
	v_addc_co_u32_e64 v111, s[0:1], 0, v143, s[0:1]
	v_add_co_u32_e64 v126, s[0:1], s56, v142
	s_waitcnt vmcnt(1)
	v_mfma_f32_16x16x32_bf16 v[94:97], v[114:117], v[70:73], v[94:97]
	v_addc_co_u32_e64 v127, s[0:1], 0, v143, s[0:1]
	global_load_dwordx4 v[122:125], v[126:127], off offset:-4096
	global_load_dwordx4 v[128:131], v[110:111], off offset:64
	global_load_dwordx4 v[132:135], v[110:111], off offset:128
	global_load_dwordx4 v[136:139], v[110:111], off offset:192
	v_mfma_f32_16x16x32_bf16 v[98:101], v[114:117], v[54:57], v[98:101]
	v_mfma_f32_16x16x32_bf16 v[102:105], v[114:117], v[38:41], v[102:105]
	v_mfma_f32_16x16x32_bf16 v[106:109], v[114:117], v[8:11], v[106:109]
	s_waitcnt vmcnt(4)
	v_mfma_f32_16x16x32_bf16 v[94:97], v[118:121], v[66:69], v[94:97]
	v_mfma_f32_16x16x32_bf16 v[98:101], v[118:121], v[50:53], v[98:101]
	v_mfma_f32_16x16x32_bf16 v[102:105], v[118:121], v[24:27], v[102:105]
	s_nop 5
	v_mul_f32_e64 v96, v180, v96
	v_mul_f32_e64 v97, v180, v97
	v_pk_mul_f32 v[94:95], v[180:181], v[94:95] op_sel_hi:[0,1]
	v_mfma_f32_16x16x32_bf16 v[106:109], v[118:121], v[12:15], v[106:109]
	s_waitcnt vmcnt(3)
	v_mfma_f32_16x16x32_bf16 v[110:113], v[122:125], v[4:7], 0
	v_mul_f32_e64 v104, v178, v104
	v_mul_f32_e64 v105, v178, v105
	v_pk_mul_f32 v[102:103], v[178:179], v[102:103] op_sel_hi:[0,1]
	s_nop 2
	v_pk_mul_f32 v[108:109], v[28:29], v[108:109] op_sel_hi:[0,1]
	v_mfma_f32_16x16x32_bf16 v[114:117], v[122:125], v[62:65], 0
	v_mul_f32_e64 v106, v28, v106
	v_mul_f32_e64 v107, v28, v107
	v_mfma_f32_16x16x32_bf16 v[118:121], v[122:125], v[46:49], 0
	v_mfma_f32_16x16x32_bf16 v[122:125], v[122:125], v[20:23], 0
	s_waitcnt vmcnt(2)
	v_mfma_f32_16x16x32_bf16 v[110:113], v[128:131], v[0:3], v[110:113]
	v_mfma_f32_16x16x32_bf16 v[114:117], v[128:131], v[58:61], v[114:117]
	v_mfma_f32_16x16x32_bf16 v[118:121], v[128:131], v[42:45], v[118:121]
	v_mfma_f32_16x16x32_bf16 v[122:125], v[128:131], v[16:19], v[122:125]
	s_waitcnt vmcnt(1)
	v_mfma_f32_16x16x32_bf16 v[110:113], v[132:135], v[70:73], v[110:113]
	v_mfma_f32_16x16x32_bf16 v[114:117], v[132:135], v[54:57], v[114:117]
	v_mfma_f32_16x16x32_bf16 v[118:121], v[132:135], v[38:41], v[118:121]
	v_mfma_f32_16x16x32_bf16 v[122:125], v[132:135], v[8:11], v[122:125]
	s_waitcnt vmcnt(0)
	v_mfma_f32_16x16x32_bf16 v[110:113], v[136:139], v[66:69], v[110:113]
	v_mfma_f32_16x16x32_bf16 v[114:117], v[136:139], v[50:53], v[114:117]
	v_mfma_f32_16x16x32_bf16 v[118:121], v[136:139], v[24:27], v[118:121]
	s_nop 5
	v_mul_f32_e64 v112, v180, v112
	v_mul_f32_e64 v113, v180, v113
	v_pk_mul_f32 v[110:111], v[180:181], v[110:111] op_sel_hi:[0,1]
	v_pk_mul_f32 v[116:117], v[176:177], v[116:117] op_sel_hi:[0,1]
	v_mfma_f32_16x16x32_bf16 v[122:125], v[136:139], v[12:15], v[122:125]
	global_load_dwordx4 v[138:141], v[126:127], off
	global_load_dwordx4 v[144:147], v[126:127], off offset:64
	global_load_dwordx4 v[148:151], v[126:127], off offset:128
	global_load_dwordx4 v[152:155], v[126:127], off offset:192
	v_pk_mul_f32 v[114:115], v[176:177], v[114:115] op_sel_hi:[0,1]
	s_waitcnt vmcnt(3)
	v_mfma_f32_16x16x32_bf16 v[126:129], v[138:141], v[4:7], 0
	v_mul_f32_e64 v120, v178, v120
	v_mul_f32_e64 v121, v178, v121
	v_pk_mul_f32 v[118:119], v[178:179], v[118:119] op_sel_hi:[0,1]
	v_pk_mul_f32 v[124:125], v[28:29], v[124:125] op_sel_hi:[0,1]
	v_mfma_f32_16x16x32_bf16 v[130:133], v[138:141], v[62:65], 0
	v_mul_f32_e64 v122, v28, v122
	v_mul_f32_e64 v123, v28, v123
	v_mfma_f32_16x16x32_bf16 v[134:137], v[138:141], v[46:49], 0
	v_mfma_f32_16x16x32_bf16 v[138:141], v[138:141], v[20:23], 0
	s_waitcnt vmcnt(2)
	v_mfma_f32_16x16x32_bf16 v[126:129], v[144:147], v[0:3], v[126:129]
	v_mfma_f32_16x16x32_bf16 v[130:133], v[144:147], v[58:61], v[130:133]
	v_mfma_f32_16x16x32_bf16 v[134:137], v[144:147], v[42:45], v[134:137]
	v_mfma_f32_16x16x32_bf16 v[138:141], v[144:147], v[16:19], v[138:141]
	s_waitcnt vmcnt(1)
	v_mfma_f32_16x16x32_bf16 v[126:129], v[148:151], v[70:73], v[126:129]
	v_mfma_f32_16x16x32_bf16 v[130:133], v[148:151], v[54:57], v[130:133]
	v_mfma_f32_16x16x32_bf16 v[134:137], v[148:151], v[38:41], v[134:137]
	v_mfma_f32_16x16x32_bf16 v[138:141], v[148:151], v[8:11], v[138:141]
	s_waitcnt vmcnt(0)
	v_mfma_f32_16x16x32_bf16 v[126:129], v[152:155], v[66:69], v[126:129]
	v_mfma_f32_16x16x32_bf16 v[130:133], v[152:155], v[50:53], v[130:133]
	v_mfma_f32_16x16x32_bf16 v[134:137], v[152:155], v[24:27], v[134:137]
	s_nop 5
	v_mul_f32_e64 v128, v180, v128
	v_mul_f32_e64 v129, v180, v129
	v_pk_mul_f32 v[126:127], v[180:181], v[126:127] op_sel_hi:[0,1]
	v_pk_mul_f32 v[132:133], v[176:177], v[132:133] op_sel_hi:[0,1]
	v_mfma_f32_16x16x32_bf16 v[138:141], v[152:155], v[12:15], v[138:141]
	v_add_co_u32_e64 v154, s[0:1], s77, v142
	v_pk_mul_f32 v[130:131], v[176:177], v[130:131] op_sel_hi:[0,1]
	s_nop 0
	v_addc_co_u32_e64 v155, s[0:1], 0, v143, s[0:1]
	global_load_dwordx4 v[142:145], v[154:155], off
	global_load_dwordx4 v[146:149], v[154:155], off offset:64
	global_load_dwordx4 v[150:153], v[154:155], off offset:128
	s_nop 0
	global_load_dwordx4 v[154:157], v[154:155], off offset:192
	s_waitcnt vmcnt(3)
	v_mfma_f32_16x16x32_bf16 v[4:7], v[142:145], v[4:7], 0
	v_mul_f32_e64 v136, v178, v136
	v_mul_f32_e64 v137, v178, v137
	v_pk_mul_f32 v[134:135], v[178:179], v[134:135] op_sel_hi:[0,1]
	s_waitcnt vmcnt(2)
	v_mfma_f32_16x16x32_bf16 v[0:3], v[146:149], v[0:3], v[4:7]
	v_mul_f32_e64 v140, v28, v140
	v_mul_f32_e64 v141, v28, v141
	v_pk_mul_f32 v[138:139], v[28:29], v[138:139] op_sel_hi:[0,1]
	s_add_u32 s0, s30, s18
	s_waitcnt vmcnt(1)
	v_mfma_f32_16x16x32_bf16 v[0:3], v[150:153], v[70:73], v[0:3]
	s_addc_u32 s1, s31, s19
	s_waitcnt vmcnt(0)
	v_mfma_f32_16x16x32_bf16 v[0:3], v[154:157], v[66:69], v[0:3]
	s_nop 7
	v_pk_mul_f32 v[68:69], v[180:181], v[2:3] op_sel_hi:[0,1]
	v_pk_mul_f32 v[66:67], v[180:181], v[0:1] op_sel_hi:[0,1]
	v_mfma_f32_16x16x32_bf16 v[0:3], v[142:145], v[62:65], 0
	v_mfma_f32_16x16x32_bf16 v[0:3], v[146:149], v[58:61], v[0:3]
	v_mfma_f32_16x16x32_bf16 v[0:3], v[150:153], v[54:57], v[0:3]
	v_mfma_f32_16x16x32_bf16 v[0:3], v[154:157], v[50:53], v[0:3]
	s_nop 7
	v_pk_mul_f32 v[72:73], v[176:177], v[2:3] op_sel_hi:[0,1]
	v_pk_mul_f32 v[70:71], v[176:177], v[0:1] op_sel_hi:[0,1]
	v_mfma_f32_16x16x32_bf16 v[0:3], v[142:145], v[46:49], 0
	v_mfma_f32_16x16x32_bf16 v[0:3], v[146:149], v[42:45], v[0:3]
	v_mfma_f32_16x16x32_bf16 v[0:3], v[150:153], v[38:41], v[0:3]
	v_mfma_f32_16x16x32_bf16 v[0:3], v[154:157], v[24:27], v[0:3]
	s_nop 7
	v_pk_mul_f32 v[26:27], v[178:179], v[2:3] op_sel_hi:[0,1]
	v_pk_mul_f32 v[24:25], v[178:179], v[0:1] op_sel_hi:[0,1]
	v_mfma_f32_16x16x32_bf16 v[0:3], v[142:145], v[20:23], 0
	v_mfma_f32_16x16x32_bf16 v[0:3], v[146:149], v[16:19], v[0:3]
	v_mul_f32_e64 v18, v176, v100
	v_mul_f32_e64 v19, v176, v101
	v_pk_mul_f32 v[16:17], v[176:177], v[98:99] op_sel_hi:[0,1]
	v_mfma_f32_16x16x32_bf16 v[0:3], v[150:153], v[8:11], v[0:3]
	v_mfma_f32_16x16x32_bf16 v[0:3], v[154:157], v[12:15], v[0:3]
	s_nop 7
	v_pk_mul_f32 v[10:11], v[28:29], v[2:3] op_sel_hi:[0,1]
	v_pk_mul_f32 v[8:9], v[28:29], v[0:1] op_sel_hi:[0,1]
	ds_read_b64_tr_b16 v[2:3], v214 offset:2560
	ds_read_b64_tr_b16 v[0:1], v214
	ds_read_b64_tr_b16 v[4:5], v214 offset:32
	ds_read_b64_tr_b16 v[12:13], v214 offset:5120
	ds_read_b64_tr_b16 v[14:15], v214 offset:7680
	s_waitcnt lgkmcnt(3)
	v_mfma_f32_16x16x32_bf16 v[94:97], v[0:3], v[30:33], v[94:97]
	v_mfma_f32_16x16x32_bf16 v[50:53], v[0:3], v[74:77], v[16:19]
	v_mfma_f32_16x16x32_bf16 v[16:19], v[0:3], v[78:81], v[102:105]
	v_mfma_f32_16x16x32_bf16 v[0:3], v[0:3], v[82:85], v[106:109]
	s_waitcnt lgkmcnt(0)
	v_mfma_f32_16x16x32_bf16 v[38:41], v[12:15], v[86:89], v[16:19]
	v_mfma_f32_16x16x32_bf16 v[12:15], v[12:15], v[90:93], v[0:3]
	ds_read_b64_tr_b16 v[6:7], v214 offset:2592
	s_nop 3
	ds_read_b64_tr_b16 v[0:1], v214 offset:5152
	ds_read_b64_tr_b16 v[2:3], v214 offset:7712
	s_waitcnt lgkmcnt(2)
	v_mfma_f32_16x16x32_bf16 v[62:65], v[4:7], v[30:33], v[110:113]
	v_mfma_f32_16x16x32_bf16 v[46:49], v[4:7], v[74:77], v[114:117]
	v_mfma_f32_16x16x32_bf16 v[16:19], v[4:7], v[78:81], v[118:121]
	v_mfma_f32_16x16x32_bf16 v[4:7], v[4:7], v[82:85], v[122:125]
	s_waitcnt lgkmcnt(0)
	v_mfma_f32_16x16x32_bf16 v[20:23], v[0:3], v[86:89], v[16:19]
	v_mfma_f32_16x16x32_bf16 v[4:7], v[0:3], v[90:93], v[4:7]
	ds_read_b64_tr_b16 v[0:1], v214 offset:64
	ds_read_b64_tr_b16 v[2:3], v214 offset:2624
	ds_read_b64_tr_b16 v[54:55], v214 offset:5184
	ds_read_b64_tr_b16 v[56:57], v214 offset:7744
	ds_read_b64_tr_b16 v[98:99], v214 offset:96
	ds_read_b64_tr_b16 v[100:101], v214 offset:2656
	ds_read_b64_tr_b16 v[102:103], v214 offset:5216
	ds_read_b64_tr_b16 v[104:105], v214 offset:7776
	s_waitcnt lgkmcnt(6)
	v_mfma_f32_16x16x32_bf16 v[58:61], v[0:3], v[30:33], v[126:129]
	v_mfma_f32_16x16x32_bf16 v[42:45], v[0:3], v[74:77], v[130:133]
	v_mfma_f32_16x16x32_bf16 v[16:19], v[0:3], v[78:81], v[134:137]
	v_mfma_f32_16x16x32_bf16 v[0:3], v[0:3], v[82:85], v[138:141]
	s_waitcnt lgkmcnt(4)
	v_mfma_f32_16x16x32_bf16 v[16:19], v[54:57], v[86:89], v[16:19]
	v_mfma_f32_16x16x32_bf16 v[0:3], v[54:57], v[90:93], v[0:3]
	s_waitcnt lgkmcnt(2)
	v_mfma_f32_16x16x32_bf16 v[54:57], v[98:101], v[30:33], v[66:69]
	v_add_u32_e32 v32, v209, v160
	v_mfma_f32_16x16x32_bf16 v[28:31], v[98:101], v[74:77], v[70:73]
	s_nop 0
	ds_read_b64 v[68:69], v32
	s_nop 0
	global_load_dword v70, v33, s[0:1]
	s_add_u32 s0, s2, s16
	s_addc_u32 s1, s3, s17
	v_mfma_f32_16x16x32_bf16 v[24:27], v[98:101], v[78:81], v[24:27]
	v_mov_b64_e32 v[78:79], s[0:1]
	v_mad_i64_i32 v[66:67], s[0:1], v174, s96, v[78:79]
	v_lshl_add_u64 v[72:73], v[66:67], 0, v[172:173]
	global_load_dwordx2 v[74:75], v[72:73], off
	s_waitcnt lgkmcnt(0)
	v_lshlrev_b32_e32 v66, 16, v68
	v_and_b32_e32 v67, 0xffff0000, v68
	v_lshlrev_b32_e32 v68, 16, v69
	v_and_b32_e32 v69, 0xffff0000, v69
	v_mfma_f32_16x16x32_bf16 v[8:11], v[98:101], v[82:85], v[8:11]
	s_waitcnt vmcnt(1)
	v_pk_fma_f32 v[66:67], v[70:71], v[66:67], v[94:95] op_sel_hi:[0,1,1]
	v_pk_fma_f32 v[68:69], v[70:71], v[68:69], v[96:97] op_sel_hi:[0,1,1]
	v_mfma_f32_16x16x32_bf16 v[24:27], v[102:105], v[86:89], v[24:27]
	s_waitcnt vmcnt(0)
	v_lshlrev_b32_e32 v76, 16, v74
	v_mul_f32_e32 v32, 0xbfb8aa3b, v76
	v_exp_f32_e32 v32, v32
	v_and_b32_e32 v77, 0xffff0000, v74
	v_pk_mul_f32 v[66:67], v[66:67], v[76:77]
	v_lshlrev_b32_e32 v74, 16, v75
	v_add_f32_e32 v32, 1.0, v32
	v_rcp_f32_e32 v80, v32
	v_mul_f32_e32 v32, 0xbfb8aa3b, v77
	v_exp_f32_e32 v32, v32
	v_and_b32_e32 v75, 0xffff0000, v75
	v_pk_mul_f32 v[68:69], v[68:69], v[74:75]
	v_mfma_f32_16x16x32_bf16 v[8:11], v[102:105], v[90:93], v[8:11]
	v_add_f32_e32 v32, 1.0, v32
	v_rcp_f32_e32 v81, v32
	s_nop 0
	v_pk_mul_f32 v[66:67], v[66:67], v[80:81]
	s_nop 0
	v_mul_f32_e32 v32, v67, v67
	v_pk_fma_f32 v[76:77], v[66:67], v[66:67], v[32:33] op_sel_hi:[1,1,0]
	v_mul_f32_e32 v32, 0xbfb8aa3b, v74
	v_exp_f32_e32 v32, v32
	s_nop 0
	v_add_f32_e32 v32, 1.0, v32
	v_rcp_f32_e32 v80, v32
	v_mul_f32_e32 v32, 0xbfb8aa3b, v75
	v_exp_f32_e32 v32, v32
	s_nop 0
	v_add_f32_e32 v32, 1.0, v32
	v_rcp_f32_e32 v81, v32
	s_nop 0
	v_pk_mul_f32 v[68:69], v[68:69], v[80:81]
	global_load_dwordx2 v[80:81], v[72:73], off offset:32
	v_pk_fma_f32 v[74:75], v[68:69], v[68:69], v[76:77]
	v_mul_f32_e32 v32, v69, v69
	v_pk_add_f32 v[74:75], v[32:33], v[74:75] op_sel_hi:[0,1]
	v_add_u32_e32 v32, v209, v189
	ds_read_b64 v[76:77], v32
	s_waitcnt lgkmcnt(0)
	v_lshlrev_b32_e32 v82, 16, v76
	v_and_b32_e32 v83, 0xffff0000, v76
	v_pk_fma_f32 v[62:63], v[70:71], v[82:83], v[62:63] op_sel_hi:[0,1,1]
	v_lshlrev_b32_e32 v76, 16, v77
	v_and_b32_e32 v77, 0xffff0000, v77
	v_pk_fma_f32 v[64:65], v[70:71], v[76:77], v[64:65] op_sel_hi:[0,1,1]
	s_waitcnt vmcnt(0)
	v_lshlrev_b32_e32 v84, 16, v80
	v_mul_f32_e32 v32, 0xbfb8aa3b, v84
	v_exp_f32_e32 v32, v32
	v_and_b32_e32 v85, 0xffff0000, v80
	v_pk_mul_f32 v[62:63], v[62:63], v[84:85]
	v_lshlrev_b32_e32 v80, 16, v81
	v_add_f32_e32 v32, 1.0, v32
	v_rcp_f32_e32 v86, v32
	v_mul_f32_e32 v32, 0xbfb8aa3b, v85
	v_exp_f32_e32 v32, v32
	v_and_b32_e32 v81, 0xffff0000, v81
	v_pk_mul_f32 v[64:65], v[64:65], v[80:81]
	v_add_f32_e32 v32, 1.0, v32
	v_rcp_f32_e32 v87, v32
	s_nop 0
	v_pk_mul_f32 v[62:63], v[62:63], v[86:87]
	s_nop 0
	v_pk_fma_f32 v[74:75], v[62:63], v[62:63], v[74:75]
	v_mul_f32_e32 v32, v63, v63
	v_pk_add_f32 v[74:75], v[32:33], v[74:75] op_sel_hi:[0,1]
	v_mul_f32_e32 v32, 0xbfb8aa3b, v80
	v_exp_f32_e32 v32, v32
	s_nop 0
	v_add_f32_e32 v32, 1.0, v32
	v_rcp_f32_e32 v82, v32
	v_mul_f32_e32 v32, 0xbfb8aa3b, v81
	global_load_dwordx2 v[80:81], v[72:73], off offset:64
	v_exp_f32_e32 v32, v32
	s_waitcnt vmcnt(0)
	v_lshlrev_b32_e32 v84, 16, v80
	v_add_f32_e32 v32, 1.0, v32
	v_rcp_f32_e32 v83, v32
	v_and_b32_e32 v85, 0xffff0000, v80
	v_lshlrev_b32_e32 v80, 16, v81
	v_and_b32_e32 v81, 0xffff0000, v81
	v_pk_mul_f32 v[64:65], v[64:65], v[82:83]
	s_nop 0
	v_pk_fma_f32 v[74:75], v[64:65], v[64:65], v[74:75]
	v_mul_f32_e32 v32, v65, v65
	v_pk_add_f32 v[74:75], v[32:33], v[74:75] op_sel_hi:[0,1]
	v_add_u32_e32 v32, v209, v188
	ds_read_b64 v[76:77], v32
	v_mul_f32_e32 v32, 0xbfb8aa3b, v84
	v_exp_f32_e32 v32, v32
	s_waitcnt lgkmcnt(0)
	v_lshlrev_b32_e32 v82, 16, v76
	v_add_f32_e32 v32, 1.0, v32
	v_rcp_f32_e32 v86, v32
	v_mul_f32_e32 v32, 0xbfb8aa3b, v85
	v_exp_f32_e32 v32, v32
	v_and_b32_e32 v83, 0xffff0000, v76
	v_pk_fma_f32 v[58:59], v[70:71], v[82:83], v[58:59] op_sel_hi:[0,1,1]
	v_pk_mul_f32 v[58:59], v[58:59], v[84:85]
	v_add_f32_e32 v32, 1.0, v32
	v_rcp_f32_e32 v87, v32
	v_lshlrev_b32_e32 v76, 16, v77
	v_and_b32_e32 v77, 0xffff0000, v77
	v_pk_fma_f32 v[60:61], v[70:71], v[76:77], v[60:61] op_sel_hi:[0,1,1]
	v_pk_mul_f32 v[58:59], v[58:59], v[86:87]
	v_pk_mul_f32 v[60:61], v[60:61], v[80:81]
	v_pk_fma_f32 v[74:75], v[58:59], v[58:59], v[74:75]
	v_mul_f32_e32 v32, v59, v59
	v_pk_add_f32 v[74:75], v[32:33], v[74:75] op_sel_hi:[0,1]
	v_mul_f32_e32 v32, 0xbfb8aa3b, v80
	v_exp_f32_e32 v32, v32
	s_nop 0
	v_add_f32_e32 v32, 1.0, v32
	v_rcp_f32_e32 v82, v32
	v_mul_f32_e32 v32, 0xbfb8aa3b, v81
	global_load_dwordx2 v[80:81], v[72:73], off offset:96
	v_exp_f32_e32 v32, v32
	s_nop 0
	v_add_f32_e32 v32, 1.0, v32
	v_rcp_f32_e32 v83, v32
	s_nop 0
	v_pk_mul_f32 v[60:61], v[60:61], v[82:83]
	s_nop 0
	v_pk_fma_f32 v[74:75], v[60:61], v[60:61], v[74:75]
	v_mul_f32_e32 v32, v61, v61
	v_pk_add_f32 v[74:75], v[32:33], v[74:75] op_sel_hi:[0,1]
	v_add_u32_e32 v32, v209, v187
	ds_read_b64 v[76:77], v32
	s_waitcnt lgkmcnt(0)
	v_lshlrev_b32_e32 v72, 16, v76
	v_and_b32_e32 v73, 0xffff0000, v76
	v_pk_fma_f32 v[54:55], v[70:71], v[72:73], v[54:55] op_sel_hi:[0,1,1]
	s_waitcnt vmcnt(0)
	v_lshlrev_b32_e32 v82, 16, v80
	v_mul_f32_e32 v32, 0xbfb8aa3b, v82
	v_exp_f32_e32 v32, v32
	v_and_b32_e32 v83, 0xffff0000, v80
	v_pk_mul_f32 v[54:55], v[54:55], v[82:83]
	v_lshlrev_b32_e32 v76, 16, v81
	v_add_f32_e32 v32, 1.0, v32
	v_rcp_f32_e32 v84, v32
	v_mul_f32_e32 v32, 0xbfb8aa3b, v83
	v_exp_f32_e32 v32, v32
	s_nop 0
	v_add_f32_e32 v32, 1.0, v32
	v_rcp_f32_e32 v85, v32
	s_nop 0
	v_pk_mul_f32 v[72:73], v[54:55], v[84:85]
	s_nop 0
	v_pk_fma_f32 v[54:55], v[72:73], v[72:73], v[74:75]
	v_mul_f32_e32 v32, v73, v73
	v_pk_add_f32 v[54:55], v[32:33], v[54:55] op_sel_hi:[0,1]
	v_mul_f32_e32 v32, 0xbfb8aa3b, v76
	v_exp_f32_e32 v32, v32
	v_lshlrev_b32_e32 v74, 16, v77
	v_and_b32_e32 v75, 0xffff0000, v77
	v_and_b32_e32 v77, 0xffff0000, v81
	v_add_f32_e32 v32, 1.0, v32
	v_rcp_f32_e32 v80, v32
	v_mul_f32_e32 v32, 0xbfb8aa3b, v77
	v_exp_f32_e32 v32, v32
	v_pk_fma_f32 v[56:57], v[70:71], v[74:75], v[56:57] op_sel_hi:[0,1,1]
	v_pk_mul_f32 v[56:57], v[56:57], v[76:77]
	v_or_b32_e32 v76, s55, v185
	v_add_f32_e32 v32, 1.0, v32
	v_rcp_f32_e32 v81, v32
	s_nop 0
	v_pk_mul_f32 v[56:57], v[56:57], v[80:81]
	s_nop 0
	v_pk_fma_f32 v[54:55], v[56:57], v[56:57], v[54:55]
	v_mul_f32_e32 v32, v57, v57
	v_pk_add_f32 v[110:111], v[32:33], v[54:55] op_sel_hi:[0,1]
	v_or_b32_e32 v54, s55, v184
	v_mad_i64_i32 v[74:75], s[0:1], v54, s96, v[78:79]
	v_lshl_add_u64 v[74:75], v[74:75], 0, v[172:173]
	global_load_dwordx2 v[126:127], v[74:75], off
	global_load_dwordx2 v[122:123], v[74:75], off offset:32
	global_load_dwordx2 v[116:117], v[74:75], off offset:64
	global_load_dwordx2 v[112:113], v[74:75], off offset:96
	v_mad_i64_i32 v[74:75], s[0:1], v76, s96, v[78:79]
	v_lshl_add_u64 v[74:75], v[74:75], 0, v[172:173]
	global_load_dwordx2 v[106:107], v[74:75], off
	global_load_dwordx2 v[102:103], v[74:75], off offset:32
	global_load_dwordx2 v[98:99], v[74:75], off offset:64
	global_load_dwordx2 v[94:95], v[74:75], off offset:96
	v_or_b32_e32 v74, s55, v186
	v_mad_i64_i32 v[78:79], s[0:1], v74, s96, v[78:79]
	v_lshl_add_u64 v[78:79], v[78:79], 0, v[172:173]
	global_load_dwordx2 v[90:91], v[78:79], off
	global_load_dwordx2 v[86:87], v[78:79], off offset:32
	global_load_dwordx2 v[82:83], v[78:79], off offset:64
	v_add_u32_e32 v32, v211, v160
	global_load_dwordx2 v[78:79], v[78:79], off offset:96
	ds_read_b64 v[120:121], v32
	v_add_u32_e32 v32, v211, v189
	ds_read_b64 v[124:125], v32
	v_add_u32_e32 v32, v211, v188
	ds_read_b64 v[118:119], v32
	v_add_u32_e32 v32, v211, v187
	ds_read_b64 v[114:115], v32
	v_add_u32_e32 v32, v212, v160
	ds_read_b64 v[108:109], v32
	v_add_u32_e32 v32, v212, v189
	ds_read_b64 v[104:105], v32
	v_add_u32_e32 v32, v212, v188
	ds_read_b64 v[100:101], v32
	v_add_u32_e32 v32, v212, v187
	ds_read_b64 v[96:97], v32
	v_add_u32_e32 v32, v210, v160
	ds_read_b64 v[92:93], v32
	v_add_u32_e32 v32, v210, v189
	ds_read_b64 v[88:89], v32
	v_add_u32_e32 v32, v210, v188
	ds_read_b64 v[84:85], v32
	v_add_u32_e32 v32, v210, v187
	ds_read_b64 v[80:81], v32
	s_lshl_b32 s0, s33, 11
	v_mov_b32_e32 v55, v110
	s_add_i32 s16, s0, 0
	s_nop 0
	v_permlane16_swap_b32_e32 v110, v55
	s_add_i32 s16, s16, 0x15000
	v_add_f32_e32 v55, v110, v55
	s_add_i32 s0, s16, s35
	v_mov_b32_e32 v71, v55
	v_lshl_add_u32 v32, v166, 2, s0
	s_nop 0
	v_permlane32_swap_b32_e32 v55, v71
	s_and_saveexec_b64 s[0:1], s[42:43]
	v_add_f32_e32 v55, v55, v71
	ds_write_b32 v32, v55
	s_or_b64 exec, exec, s[0:1]
	s_waitcnt vmcnt(11)
	v_lshlrev_b32_e32 v128, 16, v126
	v_mul_f32_e32 v55, 0xbfb8aa3b, v128
	v_exp_f32_e32 v55, v55
	v_and_b32_e32 v129, 0xffff0000, v126
	v_lshlrev_b32_e32 v126, 16, v127
	v_mov_b32_e32 v71, v70
	v_add_f32_e32 v55, 1.0, v55
	v_rcp_f32_e32 v130, v55
	v_mul_f32_e32 v55, 0xbfb8aa3b, v129
	v_exp_f32_e32 v55, v55
	s_waitcnt lgkmcnt(11)
	v_lshlrev_b32_e32 v110, 16, v120
	v_and_b32_e32 v111, 0xffff0000, v120
	v_pk_fma_f32 v[50:51], v[70:71], v[110:111], v[50:51]
	v_add_f32_e32 v55, 1.0, v55
	v_rcp_f32_e32 v131, v55
	v_mul_f32_e32 v55, 0xbfb8aa3b, v126
	v_exp_f32_e32 v55, v55
	v_and_b32_e32 v127, 0xffff0000, v127
	v_pk_mul_f32 v[50:51], v[50:51], v[128:129]
	v_lshlrev_b32_e32 v120, 16, v121
	v_add_f32_e32 v55, 1.0, v55
	v_rcp_f32_e32 v128, v55
	v_mul_f32_e32 v55, 0xbfb8aa3b, v127
	v_exp_f32_e32 v55, v55
	v_and_b32_e32 v121, 0xffff0000, v121
	v_pk_fma_f32 v[52:53], v[70:71], v[120:121], v[52:53]
	v_pk_mul_f32 v[50:51], v[50:51], v[130:131]
	v_pk_mul_f32 v[52:53], v[52:53], v[126:127]
	v_add_f32_e32 v55, 1.0, v55
	s_waitcnt vmcnt(10)
	v_lshlrev_b32_e32 v126, 16, v122
	v_rcp_f32_e32 v129, v55
	v_mul_f32_e32 v55, 0xbfb8aa3b, v126
	v_exp_f32_e32 v55, v55
	v_and_b32_e32 v127, 0xffff0000, v122
	v_pk_mul_f32 v[52:53], v[52:53], v[128:129]
	v_lshlrev_b32_e32 v122, 16, v123
	v_add_f32_e32 v55, 1.0, v55
	v_rcp_f32_e32 v128, v55
	v_mul_f32_e32 v55, 0xbfb8aa3b, v127
	v_exp_f32_e32 v55, v55
	v_mul_f32_e32 v110, v51, v51
	v_pk_fma_f32 v[110:111], v[50:51], v[50:51], v[110:111] op_sel_hi:[1,1,0]
	v_mul_f32_e32 v120, v53, v53
	v_add_f32_e32 v55, 1.0, v55
	v_rcp_f32_e32 v129, v55
	v_mul_f32_e32 v55, 0xbfb8aa3b, v122
	v_exp_f32_e32 v55, v55
	v_pk_fma_f32 v[110:111], v[52:53], v[52:53], v[110:111]
	v_and_b32_e32 v123, 0xffff0000, v123
	v_pk_add_f32 v[110:111], v[120:121], v[110:111] op_sel_hi:[0,1]
	s_waitcnt lgkmcnt(10)
	v_lshlrev_b32_e32 v120, 16, v124
	v_and_b32_e32 v121, 0xffff0000, v124
	v_pk_fma_f32 v[46:47], v[70:71], v[120:121], v[46:47]
	v_add_f32_e32 v55, 1.0, v55
	v_pk_mul_f32 v[46:47], v[46:47], v[126:127]
	v_rcp_f32_e32 v124, v55
	v_mul_f32_e32 v55, 0xbfb8aa3b, v123
	v_pk_mul_f32 v[46:47], v[46:47], v[128:129]
	v_exp_f32_e32 v55, v55
	v_pk_fma_f32 v[110:111], v[46:47], v[46:47], v[110:111]
	v_mul_f32_e32 v120, v47, v47
	v_pk_add_f32 v[110:111], v[120:121], v[110:111] op_sel_hi:[0,1]
	v_lshlrev_b32_e32 v120, 16, v125
	v_and_b32_e32 v121, 0xffff0000, v125
	v_pk_fma_f32 v[48:49], v[70:71], v[120:121], v[48:49]
	v_add_f32_e32 v55, 1.0, v55
	v_pk_mul_f32 v[48:49], v[48:49], v[122:123]
	s_waitcnt vmcnt(9)
	v_lshlrev_b32_e32 v122, 16, v116
	v_rcp_f32_e32 v125, v55
	v_mul_f32_e32 v55, 0xbfb8aa3b, v122
	v_exp_f32_e32 v55, v55
	v_and_b32_e32 v123, 0xffff0000, v116
	v_pk_mul_f32 v[48:49], v[48:49], v[124:125]
	v_add_f32_e32 v55, 1.0, v55
	v_rcp_f32_e32 v124, v55
	v_mul_f32_e32 v55, 0xbfb8aa3b, v123
	v_exp_f32_e32 v55, v55
	v_pk_fma_f32 v[110:111], v[48:49], v[48:49], v[110:111]
	v_mul_f32_e32 v120, v49, v49
	v_pk_add_f32 v[110:111], v[120:121], v[110:111] op_sel_hi:[0,1]
	v_add_f32_e32 v55, 1.0, v55
	v_rcp_f32_e32 v125, v55
	s_waitcnt lgkmcnt(9)
	v_lshlrev_b32_e32 v120, 16, v118
	v_and_b32_e32 v121, 0xffff0000, v118
	v_pk_fma_f32 v[42:43], v[70:71], v[120:121], v[42:43]
	v_lshlrev_b32_e32 v118, 16, v119
	v_pk_mul_f32 v[42:43], v[42:43], v[122:123]
	v_and_b32_e32 v119, 0xffff0000, v119
	v_pk_mul_f32 v[42:43], v[42:43], v[124:125]
	v_pk_fma_f32 v[44:45], v[70:71], v[118:119], v[44:45]
	v_pk_fma_f32 v[110:111], v[42:43], v[42:43], v[110:111]
	v_mul_f32_e32 v116, v43, v43
	v_pk_add_f32 v[110:111], v[116:117], v[110:111] op_sel_hi:[0,1]
	v_lshlrev_b32_e32 v116, 16, v117
	v_mul_f32_e32 v55, 0xbfb8aa3b, v116
	v_exp_f32_e32 v55, v55
	v_and_b32_e32 v117, 0xffff0000, v117
	s_waitcnt vmcnt(8)
	v_lshlrev_b32_e32 v118, 16, v112
	v_pk_mul_f32 v[44:45], v[44:45], v[116:117]
	v_add_f32_e32 v55, 1.0, v55
	v_rcp_f32_e32 v120, v55
	v_mul_f32_e32 v55, 0xbfb8aa3b, v117
	v_exp_f32_e32 v55, v55
	v_and_b32_e32 v119, 0xffff0000, v112
	v_add_f32_e32 v55, 1.0, v55
	v_rcp_f32_e32 v121, v55
	v_mul_f32_e32 v55, 0xbfb8aa3b, v118
	v_exp_f32_e32 v55, v55
	v_pk_mul_f32 v[44:45], v[44:45], v[120:121]
	s_nop 0
	v_pk_fma_f32 v[110:111], v[44:45], v[44:45], v[110:111]
	v_add_f32_e32 v55, 1.0, v55
	v_rcp_f32_e32 v120, v55
	v_mul_f32_e32 v55, 0xbfb8aa3b, v119
	v_exp_f32_e32 v55, v55
	v_mul_f32_e32 v116, v45, v45
	v_pk_add_f32 v[110:111], v[116:117], v[110:111] op_sel_hi:[0,1]
	s_waitcnt lgkmcnt(8)
	v_lshlrev_b32_e32 v116, 16, v114
	v_add_f32_e32 v55, 1.0, v55
	v_rcp_f32_e32 v121, v55
	v_and_b32_e32 v117, 0xffff0000, v114
	v_pk_fma_f32 v[28:29], v[70:71], v[116:117], v[28:29]
	v_lshlrev_b32_e32 v114, 16, v115
	v_pk_mul_f32 v[28:29], v[28:29], v[118:119]
	v_and_b32_e32 v115, 0xffff0000, v115
	v_pk_mul_f32 v[28:29], v[28:29], v[120:121]
	v_pk_fma_f32 v[30:31], v[70:71], v[114:115], v[30:31]
	v_pk_fma_f32 v[110:111], v[28:29], v[28:29], v[110:111]
	v_mul_f32_e32 v112, v29, v29
	v_pk_add_f32 v[110:111], v[112:113], v[110:111] op_sel_hi:[0,1]
	v_lshlrev_b32_e32 v112, 16, v113
	v_mul_f32_e32 v55, 0xbfb8aa3b, v112
	v_exp_f32_e32 v55, v55
	v_and_b32_e32 v113, 0xffff0000, v113
	v_pk_mul_f32 v[30:31], v[30:31], v[112:113]
	v_add_f32_e32 v55, 1.0, v55
	v_rcp_f32_e32 v116, v55
	v_mul_f32_e32 v55, 0xbfb8aa3b, v113
	v_exp_f32_e32 v55, v55
	s_nop 0
	v_add_f32_e32 v55, 1.0, v55
	v_rcp_f32_e32 v117, v55
	s_nop 0
	v_pk_mul_f32 v[30:31], v[30:31], v[116:117]
	s_nop 0
	v_pk_fma_f32 v[110:111], v[30:31], v[30:31], v[110:111]
	v_mul_f32_e32 v112, v31, v31
	v_pk_add_f32 v[110:111], v[112:113], v[110:111] op_sel_hi:[0,1]
	v_mov_b32_e32 v55, v110
	s_nop 1
	v_permlane16_swap_b32_e32 v110, v55
	v_add_f32_e32 v55, v110, v55
	v_mov_b32_e32 v75, v55
	s_nop 1
	v_permlane32_swap_b32_e32 v55, v75
	s_and_saveexec_b64 s[0:1], s[42:43]
	v_add_f32_e32 v55, v55, v75
	ds_write_b32 v32, v55 offset:64
	s_or_b64 exec, exec, s[0:1]
	s_waitcnt vmcnt(7)
	v_lshlrev_b32_e32 v112, 16, v106
	v_mul_f32_e32 v55, 0xbfb8aa3b, v112
	v_exp_f32_e32 v55, v55
	v_and_b32_e32 v113, 0xffff0000, v106
	s_waitcnt lgkmcnt(7)
	v_lshlrev_b32_e32 v110, 16, v108
	v_and_b32_e32 v111, 0xffff0000, v108
	v_add_f32_e32 v55, 1.0, v55
	v_rcp_f32_e32 v114, v55
	v_mul_f32_e32 v55, 0xbfb8aa3b, v113
	v_exp_f32_e32 v55, v55
	v_pk_fma_f32 v[38:39], v[70:71], v[110:111], v[38:39]
	v_lshlrev_b32_e32 v108, 16, v109
	v_pk_mul_f32 v[38:39], v[38:39], v[112:113]
	v_add_f32_e32 v55, 1.0, v55
	v_rcp_f32_e32 v115, v55
	v_and_b32_e32 v109, 0xffff0000, v109
	v_pk_fma_f32 v[40:41], v[70:71], v[108:109], v[40:41]
	v_pk_mul_f32 v[38:39], v[38:39], v[114:115]
	s_nop 0
	v_mul_f32_e32 v106, v39, v39
	v_pk_fma_f32 v[110:111], v[38:39], v[38:39], v[106:107] op_sel_hi:[1,1,0]
	v_lshlrev_b32_e32 v106, 16, v107
	v_mul_f32_e32 v55, 0xbfb8aa3b, v106
	v_exp_f32_e32 v55, v55
	v_and_b32_e32 v107, 0xffff0000, v107
	v_pk_mul_f32 v[40:41], v[40:41], v[106:107]
	v_add_f32_e32 v55, 1.0, v55
	v_rcp_f32_e32 v112, v55
	v_mul_f32_e32 v55, 0xbfb8aa3b, v107
	v_exp_f32_e32 v55, v55
	s_nop 0
	v_add_f32_e32 v55, 1.0, v55
	v_rcp_f32_e32 v113, v55
	s_nop 0
	v_pk_mul_f32 v[40:41], v[40:41], v[112:113]
	s_nop 0
	v_pk_fma_f32 v[106:107], v[40:41], v[40:41], v[110:111]
	s_waitcnt vmcnt(6)
	v_lshlrev_b32_e32 v110, 16, v102
	v_mul_f32_e32 v55, 0xbfb8aa3b, v110
	v_exp_f32_e32 v55, v55
	v_and_b32_e32 v111, 0xffff0000, v102
	v_mul_f32_e32 v108, v41, v41
	v_pk_add_f32 v[106:107], v[108:109], v[106:107] op_sel_hi:[0,1]
	v_add_f32_e32 v55, 1.0, v55
	v_rcp_f32_e32 v112, v55
	v_mul_f32_e32 v55, 0xbfb8aa3b, v111
	v_exp_f32_e32 v55, v55
	s_waitcnt lgkmcnt(6)
	v_lshlrev_b32_e32 v108, 16, v104
	v_and_b32_e32 v109, 0xffff0000, v104
	v_pk_fma_f32 v[20:21], v[70:71], v[108:109], v[20:21]
	v_add_f32_e32 v55, 1.0, v55
	v_rcp_f32_e32 v113, v55
	v_pk_mul_f32 v[20:21], v[20:21], v[110:111]
	v_lshlrev_b32_e32 v104, 16, v105
	v_and_b32_e32 v105, 0xffff0000, v105
	v_pk_mul_f32 v[20:21], v[20:21], v[112:113]
	v_pk_fma_f32 v[22:23], v[70:71], v[104:105], v[22:23]
	v_pk_fma_f32 v[106:107], v[20:21], v[20:21], v[106:107]
	v_mul_f32_e32 v102, v21, v21
	v_pk_add_f32 v[106:107], v[102:103], v[106:107] op_sel_hi:[0,1]
	v_lshlrev_b32_e32 v102, 16, v103
	v_mul_f32_e32 v55, 0xbfb8aa3b, v102
	v_exp_f32_e32 v55, v55
	v_and_b32_e32 v103, 0xffff0000, v103
	v_pk_mul_f32 v[22:23], v[22:23], v[102:103]
	v_add_f32_e32 v55, 1.0, v55
	v_rcp_f32_e32 v108, v55
	v_mul_f32_e32 v55, 0xbfb8aa3b, v103
	v_exp_f32_e32 v55, v55
	s_nop 0
	v_add_f32_e32 v55, 1.0, v55
	v_rcp_f32_e32 v109, v55
	s_nop 0
	v_pk_mul_f32 v[22:23], v[22:23], v[108:109]
	s_nop 0
	v_pk_fma_f32 v[102:103], v[22:23], v[22:23], v[106:107]
	s_waitcnt vmcnt(5)
	v_lshlrev_b32_e32 v106, 16, v98
	v_mul_f32_e32 v55, 0xbfb8aa3b, v106
	v_exp_f32_e32 v55, v55
	v_and_b32_e32 v107, 0xffff0000, v98
	v_mul_f32_e32 v104, v23, v23
	v_pk_add_f32 v[102:103], v[104:105], v[102:103] op_sel_hi:[0,1]
	v_add_f32_e32 v55, 1.0, v55
	v_rcp_f32_e32 v108, v55
	v_mul_f32_e32 v55, 0xbfb8aa3b, v107
	v_exp_f32_e32 v55, v55
	s_waitcnt lgkmcnt(5)
	v_lshlrev_b32_e32 v104, 16, v100
	v_and_b32_e32 v105, 0xffff0000, v100
	v_pk_fma_f32 v[16:17], v[70:71], v[104:105], v[16:17]
	v_add_f32_e32 v55, 1.0, v55
	v_rcp_f32_e32 v109, v55
	v_pk_mul_f32 v[16:17], v[16:17], v[106:107]
	v_lshlrev_b32_e32 v100, 16, v101
	v_and_b32_e32 v101, 0xffff0000, v101
	v_pk_mul_f32 v[16:17], v[16:17], v[108:109]
	v_pk_fma_f32 v[18:19], v[70:71], v[100:101], v[18:19]
	v_pk_fma_f32 v[102:103], v[16:17], v[16:17], v[102:103]
	v_mul_f32_e32 v98, v17, v17
	v_pk_add_f32 v[102:103], v[98:99], v[102:103] op_sel_hi:[0,1]
	v_lshlrev_b32_e32 v98, 16, v99
	v_mul_f32_e32 v55, 0xbfb8aa3b, v98
	v_exp_f32_e32 v55, v55
	v_and_b32_e32 v99, 0xffff0000, v99
	v_pk_mul_f32 v[18:19], v[18:19], v[98:99]
	v_add_f32_e32 v55, 1.0, v55
	v_rcp_f32_e32 v104, v55
	v_mul_f32_e32 v55, 0xbfb8aa3b, v99
	v_exp_f32_e32 v55, v55
	s_nop 0
	v_add_f32_e32 v55, 1.0, v55
	v_rcp_f32_e32 v105, v55
	s_nop 0
	v_pk_mul_f32 v[18:19], v[18:19], v[104:105]
	s_nop 0
	v_pk_fma_f32 v[98:99], v[18:19], v[18:19], v[102:103]
	s_waitcnt vmcnt(4)
	v_lshlrev_b32_e32 v102, 16, v94
	v_mul_f32_e32 v55, 0xbfb8aa3b, v102
	v_exp_f32_e32 v55, v55
	v_and_b32_e32 v103, 0xffff0000, v94
	v_mul_f32_e32 v100, v19, v19
	v_pk_add_f32 v[98:99], v[100:101], v[98:99] op_sel_hi:[0,1]
	v_add_f32_e32 v55, 1.0, v55
	v_rcp_f32_e32 v104, v55
	v_mul_f32_e32 v55, 0xbfb8aa3b, v103
	v_exp_f32_e32 v55, v55
	s_waitcnt lgkmcnt(4)
	v_lshlrev_b32_e32 v100, 16, v96
	v_and_b32_e32 v101, 0xffff0000, v96
	v_pk_fma_f32 v[24:25], v[70:71], v[100:101], v[24:25]
	v_add_f32_e32 v55, 1.0, v55
	v_rcp_f32_e32 v105, v55
	v_pk_mul_f32 v[24:25], v[24:25], v[102:103]
	v_lshlrev_b32_e32 v96, 16, v97
	v_and_b32_e32 v97, 0xffff0000, v97
	v_pk_mul_f32 v[24:25], v[24:25], v[104:105]
	v_pk_fma_f32 v[26:27], v[70:71], v[96:97], v[26:27]
	v_pk_fma_f32 v[98:99], v[24:25], v[24:25], v[98:99]
	v_mul_f32_e32 v94, v25, v25
	v_pk_add_f32 v[98:99], v[94:95], v[98:99] op_sel_hi:[0,1]
	v_lshlrev_b32_e32 v94, 16, v95
	v_mul_f32_e32 v55, 0xbfb8aa3b, v94
	v_exp_f32_e32 v55, v55
	v_and_b32_e32 v95, 0xffff0000, v95
	v_pk_mul_f32 v[26:27], v[26:27], v[94:95]
	v_add_f32_e32 v55, 1.0, v55
	v_rcp_f32_e32 v100, v55
	v_mul_f32_e32 v55, 0xbfb8aa3b, v95
	v_exp_f32_e32 v55, v55
	s_nop 0
	v_add_f32_e32 v55, 1.0, v55
	v_rcp_f32_e32 v101, v55
	s_nop 0
	v_pk_mul_f32 v[26:27], v[26:27], v[100:101]
	s_nop 0
	v_pk_fma_f32 v[94:95], v[26:27], v[26:27], v[98:99]
	v_mul_f32_e32 v96, v27, v27
	v_pk_add_f32 v[94:95], v[96:97], v[94:95] op_sel_hi:[0,1]
	v_mov_b32_e32 v55, v94
	s_nop 1
	v_permlane16_swap_b32_e32 v94, v55
	v_add_f32_e32 v55, v94, v55
	v_mov_b32_e32 v75, v55
	s_nop 1
	v_permlane32_swap_b32_e32 v55, v75
	s_and_saveexec_b64 s[0:1], s[42:43]
	v_add_f32_e32 v55, v55, v75
	ds_write_b32 v32, v55 offset:128
	s_or_b64 exec, exec, s[0:1]
	s_waitcnt vmcnt(3)
	v_lshlrev_b32_e32 v96, 16, v90
	v_mul_f32_e32 v55, 0xbfb8aa3b, v96
	v_exp_f32_e32 v55, v55
	v_and_b32_e32 v97, 0xffff0000, v90
	v_lshlrev_b32_e32 v90, 16, v91
	s_waitcnt lgkmcnt(3)
	v_lshlrev_b32_e32 v94, 16, v92
	v_add_f32_e32 v55, 1.0, v55
	v_rcp_f32_e32 v98, v55
	v_mul_f32_e32 v55, 0xbfb8aa3b, v97
	v_exp_f32_e32 v55, v55
	v_and_b32_e32 v95, 0xffff0000, v92
	v_pk_fma_f32 v[12:13], v[70:71], v[94:95], v[12:13]
	v_and_b32_e32 v91, 0xffff0000, v91
	v_add_f32_e32 v55, 1.0, v55
	v_rcp_f32_e32 v99, v55
	v_mul_f32_e32 v55, 0xbfb8aa3b, v90
	v_exp_f32_e32 v55, v55
	v_pk_mul_f32 v[12:13], v[12:13], v[96:97]
	v_lshlrev_b32_e32 v92, 16, v93
	v_and_b32_e32 v93, 0xffff0000, v93
	v_add_f32_e32 v55, 1.0, v55
	v_rcp_f32_e32 v96, v55
	v_mul_f32_e32 v55, 0xbfb8aa3b, v91
	v_exp_f32_e32 v55, v55
	v_pk_mul_f32 v[94:95], v[12:13], v[98:99]
	v_pk_fma_f32 v[14:15], v[70:71], v[92:93], v[14:15]
	v_mul_f32_e32 v12, v95, v95
	v_add_f32_e32 v55, 1.0, v55
	v_rcp_f32_e32 v97, v55
	v_pk_mul_f32 v[14:15], v[14:15], v[90:91]
	v_pk_fma_f32 v[12:13], v[94:95], v[94:95], v[12:13] op_sel_hi:[1,1,0]
	s_waitcnt vmcnt(2)
	v_lshlrev_b32_e32 v92, 16, v86
	v_pk_mul_f32 v[90:91], v[14:15], v[96:97]
	v_and_b32_e32 v93, 0xffff0000, v86
	v_pk_fma_f32 v[12:13], v[90:91], v[90:91], v[12:13]
	v_mul_f32_e32 v14, v91, v91
	v_pk_add_f32 v[12:13], v[14:15], v[12:13] op_sel_hi:[0,1]
	s_waitcnt lgkmcnt(2)
	v_lshlrev_b32_e32 v14, 16, v88
	v_and_b32_e32 v15, 0xffff0000, v88
	v_mul_f32_e32 v55, 0xbfb8aa3b, v92
	v_pk_fma_f32 v[4:5], v[70:71], v[14:15], v[4:5]
	v_mul_f32_e32 v14, 0xbfb8aa3b, v93
	v_exp_f32_e32 v55, v55
	v_exp_f32_e32 v14, v14
	v_pk_mul_f32 v[4:5], v[4:5], v[92:93]
	v_and_b32_e32 v15, 0xffff0000, v87
	v_add_f32_e32 v55, 1.0, v55
	v_add_f32_e32 v14, 1.0, v14
	v_rcp_f32_e32 v96, v55
	v_rcp_f32_e32 v97, v14
	v_lshlrev_b32_e32 v14, 16, v87
	v_mul_f32_e32 v55, 0xbfb8aa3b, v14
	v_exp_f32_e32 v55, v55
	v_pk_mul_f32 v[92:93], v[4:5], v[96:97]
	v_add_f32_e32 v55, 1.0, v55
	v_pk_fma_f32 v[4:5], v[92:93], v[92:93], v[12:13]
	v_mul_f32_e32 v12, v93, v93
	v_pk_add_f32 v[4:5], v[12:13], v[4:5] op_sel_hi:[0,1]
	v_lshlrev_b32_e32 v12, 16, v89
	v_and_b32_e32 v13, 0xffff0000, v89
	v_pk_fma_f32 v[6:7], v[70:71], v[12:13], v[6:7]
	v_mul_f32_e32 v12, 0xbfb8aa3b, v15
	v_exp_f32_e32 v12, v12
	v_rcp_f32_e32 v86, v55
	v_pk_mul_f32 v[6:7], v[6:7], v[14:15]
	s_waitcnt vmcnt(1)
	v_and_b32_e32 v13, 0xffff0000, v82
	v_add_f32_e32 v12, 1.0, v12
	v_rcp_f32_e32 v87, v12
	v_lshlrev_b32_e32 v12, 16, v82
	v_mul_f32_e32 v14, 0xbfb8aa3b, v12
	v_exp_f32_e32 v14, v14
	v_pk_mul_f32 v[86:87], v[6:7], v[86:87]
	v_add_f32_e32 v14, 1.0, v14
	v_pk_fma_f32 v[4:5], v[86:87], v[86:87], v[4:5]
	v_mul_f32_e32 v6, v87, v87
	v_pk_add_f32 v[4:5], v[6:7], v[4:5] op_sel_hi:[0,1]
	s_waitcnt lgkmcnt(1)
	v_lshlrev_b32_e32 v6, 16, v84
	v_and_b32_e32 v7, 0xffff0000, v84
	v_pk_fma_f32 v[0:1], v[70:71], v[6:7], v[0:1]
	v_mul_f32_e32 v6, 0xbfb8aa3b, v13
	v_exp_f32_e32 v6, v6
	v_rcp_f32_e32 v14, v14
	v_pk_mul_f32 v[0:1], v[0:1], v[12:13]
	v_and_b32_e32 v7, 0xffff0000, v83
	v_add_f32_e32 v6, 1.0, v6
	v_rcp_f32_e32 v15, v6
	v_lshlrev_b32_e32 v6, 16, v83
	v_mul_f32_e32 v12, 0xbfb8aa3b, v6
	v_exp_f32_e32 v12, v12
	v_pk_mul_f32 v[88:89], v[0:1], v[14:15]
	v_add_f32_e32 v12, 1.0, v12
	v_pk_fma_f32 v[0:1], v[88:89], v[88:89], v[4:5]
	v_mul_f32_e32 v4, v89, v89
	v_pk_add_f32 v[0:1], v[4:5], v[0:1] op_sel_hi:[0,1]
	v_lshlrev_b32_e32 v4, 16, v85
	v_and_b32_e32 v5, 0xffff0000, v85
	v_pk_fma_f32 v[2:3], v[70:71], v[4:5], v[2:3]
	v_mul_f32_e32 v4, 0xbfb8aa3b, v7
	v_exp_f32_e32 v4, v4
	v_rcp_f32_e32 v12, v12
	v_pk_mul_f32 v[2:3], v[2:3], v[6:7]
	s_waitcnt vmcnt(0)
	v_and_b32_e32 v5, 0xffff0000, v78
	v_add_f32_e32 v4, 1.0, v4
	v_rcp_f32_e32 v13, v4
	v_lshlrev_b32_e32 v4, 16, v78
	v_mul_f32_e32 v6, 0xbfb8aa3b, v4
	v_exp_f32_e32 v6, v6
	v_pk_mul_f32 v[82:83], v[2:3], v[12:13]
	v_add_f32_e32 v6, 1.0, v6
	v_pk_fma_f32 v[0:1], v[82:83], v[82:83], v[0:1]
	v_mul_f32_e32 v2, v83, v83
	v_pk_add_f32 v[0:1], v[2:3], v[0:1] op_sel_hi:[0,1]
	s_waitcnt lgkmcnt(0)
	v_lshlrev_b32_e32 v2, 16, v80
	v_and_b32_e32 v3, 0xffff0000, v80
	v_pk_fma_f32 v[2:3], v[70:71], v[2:3], v[8:9]
	v_rcp_f32_e32 v6, v6
	v_pk_mul_f32 v[2:3], v[2:3], v[4:5]
	v_mul_f32_e32 v4, 0xbfb8aa3b, v5
	v_exp_f32_e32 v4, v4
	v_and_b32_e32 v5, 0xffff0000, v79
	v_add_f32_e32 v4, 1.0, v4
	v_rcp_f32_e32 v7, v4
	v_lshlrev_b32_e32 v4, 16, v79
	v_pk_mul_f32 v[84:85], v[2:3], v[6:7]
	s_nop 0
	v_pk_fma_f32 v[0:1], v[84:85], v[84:85], v[0:1]
	v_mul_f32_e32 v2, v85, v85
	v_pk_add_f32 v[0:1], v[2:3], v[0:1] op_sel_hi:[0,1]
	v_lshlrev_b32_e32 v2, 16, v81
	v_and_b32_e32 v3, 0xffff0000, v81
	v_pk_fma_f32 v[2:3], v[70:71], v[2:3], v[10:11]
	v_mul_f32_e32 v6, 0xbfb8aa3b, v4
	v_pk_mul_f32 v[2:3], v[2:3], v[4:5]
	v_mul_f32_e32 v4, 0xbfb8aa3b, v5
	v_exp_f32_e32 v6, v6
	v_exp_f32_e32 v4, v4
	v_add_f32_e32 v6, 1.0, v6
	v_add_f32_e32 v4, 1.0, v4
	v_rcp_f32_e32 v6, v6
	v_rcp_f32_e32 v7, v4
	s_nop 0
	v_pk_mul_f32 v[70:71], v[2:3], v[6:7]
	s_nop 0
	v_pk_fma_f32 v[0:1], v[70:71], v[70:71], v[0:1]
	v_mul_f32_e32 v2, v71, v71
	v_pk_add_f32 v[0:1], v[2:3], v[0:1] op_sel_hi:[0,1]
	v_mov_b32_e32 v1, v0
	s_nop 1
	v_permlane16_swap_b32_e32 v0, v1
	v_add_f32_e32 v0, v0, v1
	v_mov_b32_e32 v1, v0
	s_nop 1
	v_permlane32_swap_b32_e32 v0, v1
	s_and_saveexec_b64 s[0:1], s[42:43]
	s_cbranch_execz .LBB0_1237
	v_add_f32_e32 v0, v0, v1
	ds_write_b32 v32, v0 offset:192
	s_branch .LBB0_1237

.LBB0_1268:
	s_and_b32 s19, s27, 7
	s_lshl_b32 s0, s19, 3
	s_add_i32 s20, s0, s22
	s_lshl_b32 s12, s20, 6
	s_ashr_i32 s18, s27, 3
	s_ashr_i32 s13, s12, 31
	s_lshl_b32 s28, s18, 6
	s_lshl_b64 s[14:15], s[12:13], 1
	s_waitcnt vmcnt(8)
	v_or_b32_e32 v30, s28, v171
	v_lshl_add_u64 v[28:29], v[160:161], 0, s[14:15]
	v_mad_i64_i32 v[0:1], s[0:1], v30, s77, v[28:29]
	v_or_b32_e32 v4, 8, v30
	global_load_dwordx4 v[0:3], v[0:1], off
	v_mad_i64_i32 v[4:5], s[0:1], v4, s77, v[28:29]
	v_or_b32_e32 v8, 16, v30
	global_load_dwordx4 v[4:7], v[4:5], off
	v_mad_i64_i32 v[8:9], s[0:1], v8, s77, v[28:29]
	v_or_b32_e32 v12, 24, v30
	global_load_dwordx4 v[8:11], v[8:9], off
	v_mad_i64_i32 v[12:13], s[0:1], v12, s77, v[28:29]
	v_or_b32_e32 v16, 32, v30
	global_load_dwordx4 v[12:15], v[12:13], off
	v_mad_i64_i32 v[16:17], s[0:1], v16, s77, v[28:29]
	v_or_b32_e32 v20, 40, v30
	global_load_dwordx4 v[16:19], v[16:17], off
	v_mad_i64_i32 v[20:21], s[0:1], v20, s77, v[28:29]
	v_or_b32_e32 v24, 48, v30
	global_load_dwordx4 v[20:23], v[20:21], off
	v_mad_i64_i32 v[24:25], s[0:1], v24, s77, v[28:29]
	v_or_b32_e32 v30, 56, v30
	global_load_dwordx4 v[24:27], v[24:25], off
	v_mad_i64_i32 v[28:29], s[0:1], v30, s77, v[28:29]
	global_load_dwordx4 v[28:31], v[28:29], off
	s_lshl_b32 s0, s18, 6
	s_add_i32 s0, s0, s20
	s_lshl_b32 s0, s0, 9
	v_lshl_add_u32 v198, v169, 3, s0
	v_mov_b32_e32 v199, 0
	v_lshl_add_u64 v[198:199], s[24:25], 0, v[198:199]
	s_mov_b64 s[0:1], 0x400000
	s_nop 0
	v_lshl_add_u64 v[198:199], v[198:199], 0, s[0:1]
	global_load_dwordx2 v[198:199], v[198:199], off
	s_ashr_i32 s21, s20, 31
	v_readlane_b32 s56, v251, 32
	s_lshl_b64 s[16:17], s[20:21], 2
	v_readlane_b32 s58, v251, 34
	v_readlane_b32 s59, v251, 35
	s_add_u32 s0, s58, s16
	s_addc_u32 s1, s59, s17
	v_readlane_b32 s60, v251, 36
	v_readlane_b32 s61, v251, 37
	v_or_b32_e32 v172, s28, v166
	v_lshlrev_b32_e32 v32, 1, v158
	s_movk_i32 s74, 0x2000
	s_movk_i32 s76, 0x1000
	v_readlane_b32 s62, v251, 38
	v_readlane_b32 s63, v251, 39
	v_readlane_b32 s57, v251, 33
	v_readlane_b32 s64, v251, 40
	v_readlane_b32 s65, v251, 41
	v_readlane_b32 s66, v251, 42
	v_readlane_b32 s67, v251, 43
	v_readlane_b32 s68, v251, 44
	v_readlane_b32 s69, v251, 45
	v_readlane_b32 s70, v251, 46
	v_readlane_b32 s71, v251, 47
	s_waitcnt vmcnt(8)
	ds_write_b128 v212, v[0:3]
	s_waitcnt vmcnt(7)
	ds_write_b128 v212, v[4:7] offset:1280
	s_waitcnt vmcnt(6)
	ds_write_b128 v212, v[8:11] offset:2560
	s_waitcnt vmcnt(5)
	ds_write_b128 v212, v[12:15] offset:3840
	s_waitcnt vmcnt(4)
	ds_write_b128 v212, v[16:19] offset:5120
	s_waitcnt vmcnt(3)
	ds_write_b128 v212, v[20:23] offset:6400
	s_waitcnt vmcnt(2)
	ds_write_b128 v212, v[24:27] offset:7680
	s_waitcnt vmcnt(1)
	ds_write_b128 v212, v[28:31] offset:8960
	s_lshl_b32 s86, s19, 8
	s_ashr_i32 s19, s18, 31
	s_waitcnt vmcnt(0)
	ds_write_b32 v183, v198
	ds_write_b32 v184, v199
	v_mov_b64_e32 v[0:1], s[8:9]
	v_mad_i64_i32 v[0:1], s[0:1], v172, s77, v[0:1]
	v_lshl_add_u64 v[0:1], v[0:1], 0, s[86:87]
	v_lshl_add_u64 v[8:9], v[0:1], 0, v[32:33]
	s_mov_b64 s[0:1], 0x2800
	v_lshl_add_u64 v[74:75], v[8:9], 0, s[0:1]
	v_add_co_u32_e64 v0, s[0:1], s74, v8
	s_movk_i32 s77, 0x3000
	s_nop 0
	v_addc_co_u32_e64 v1, s[0:1], 0, v9, s[0:1]
	s_mov_b32 s0, 0x32000
	s_nop 0
	v_add_co_u32_e64 v30, s[0:1], s0, v8
	global_load_dwordx4 v[4:7], v[0:1], off offset:2048
	s_nop 0
	global_load_dwordx4 v[0:3], v[74:75], off offset:64
	global_load_dwordx4 v[70:73], v[74:75], off offset:128
	global_load_dwordx4 v[66:69], v[74:75], off offset:192
	v_addc_co_u32_e64 v31, s[0:1], 0, v9, s[0:1]
	s_mov_b32 s0, 0x62000
	s_nop 0
	v_add_co_u32_e64 v88, s[0:1], s0, v8
	global_load_dwordx4 v[62:65], v[30:31], off offset:2048
	global_load_dwordx4 v[58:61], v[30:31], off offset:2112
	global_load_dwordx4 v[54:57], v[30:31], off offset:2176
	global_load_dwordx4 v[50:53], v[30:31], off offset:2240
	v_addc_co_u32_e64 v89, s[0:1], 0, v9, s[0:1]
	s_mov_b32 s0, 0x92000
	s_nop 0
	v_add_co_u32_e64 v86, s[0:1], s0, v8
	global_load_dwordx4 v[46:49], v[88:89], off offset:2048
	global_load_dwordx4 v[42:45], v[88:89], off offset:2112
	global_load_dwordx4 v[38:41], v[88:89], off offset:2176
	global_load_dwordx4 v[24:27], v[88:89], off offset:2240
	v_addc_co_u32_e64 v87, s[0:1], 0, v9, s[0:1]
	global_load_dwordx4 v[20:23], v[86:87], off offset:2048
	global_load_dwordx4 v[16:19], v[86:87], off offset:2112
	global_load_dwordx4 v[8:11], v[86:87], off offset:2176
	global_load_dwordx4 v[12:15], v[86:87], off offset:2240
	s_waitcnt lgkmcnt(0)
	ds_read2_b32 v[102:103], v185 offset1:16
	ds_read2_b32 v[28:29], v185 offset0:32 offset1:48
	global_load_dwordx4 v[82:85], v[74:75], off offset:-2048
	global_load_dwordx4 v[92:95], v[74:75], off offset:-1984
	global_load_dwordx4 v[96:99], v[74:75], off offset:-1920
	global_load_dwordx4 v[104:107], v[74:75], off offset:-1856
	s_waitcnt vmcnt(3)
	v_mfma_f32_16x16x32_bf16 v[74:77], v[82:85], v[4:7], 0
	ds_read_b64 v[100:101], v186
	ds_read_b32 v32, v188
	ds_read_b32 v90, v189
	ds_read_b32 v118, v190
	ds_read_b32 v91, v191
	s_mov_b32 s0, 0x5040100
	s_waitcnt vmcnt(2)
	v_mfma_f32_16x16x32_bf16 v[74:77], v[92:95], v[0:3], v[74:77]
	s_waitcnt vmcnt(1)
	v_mfma_f32_16x16x32_bf16 v[74:77], v[96:99], v[70:73], v[74:77]
	v_mfma_f32_16x16x32_bf16 v[108:111], v[82:85], v[62:65], 0
	s_waitcnt vmcnt(0)
	v_mfma_f32_16x16x32_bf16 v[78:81], v[104:107], v[66:69], v[74:77]
	s_waitcnt lgkmcnt(4)
	s_nop 3
	v_sub_f32_e32 v76, v103, v100
	v_min_f32_e32 v76, 0, v76
	v_mfma_f32_16x16x32_bf16 v[108:111], v[92:95], v[58:61], v[108:111]
	v_mul_f32_e32 v76, 0x3fb8aa3b, v76
	v_exp_f32_e32 v114, v76
	v_sub_f32_e32 v76, v103, v101
	v_min_f32_e32 v76, 0, v76
	v_mul_f32_e32 v76, 0x3fb8aa3b, v76
	v_mfma_f32_16x16x32_bf16 v[108:111], v[96:99], v[54:57], v[108:111]
	v_exp_f32_e32 v115, v76
	s_waitcnt lgkmcnt(3)
	v_sub_f32_e32 v76, v103, v32
	s_waitcnt lgkmcnt(1)
	v_sub_f32_e32 v77, v103, v118
	v_min_f32_e32 v76, 0, v76
	v_min_f32_e32 v77, 0, v77
	v_mul_f32_e32 v76, 0x3fb8aa3b, v76
	v_mul_f32_e32 v77, 0x3fb8aa3b, v77
	v_exp_f32_e32 v76, v76
	v_exp_f32_e32 v77, v77
	v_mfma_f32_16x16x32_bf16 v[108:111], v[104:107], v[50:53], v[108:111]
	v_sub_f32_e32 v74, v102, v100
	v_min_f32_e32 v74, 0, v74
	v_mul_f32_e32 v74, 0x3fb8aa3b, v74
	s_waitcnt lgkmcnt(0)
	v_pk_mul_f32 v[76:77], v[90:91], v[76:77]
	v_exp_f32_e32 v119, v74
	v_sub_f32_e32 v74, v102, v101
	s_nop 0
	v_pk_mul_f32 v[76:77], v[76:77], v[110:111]
	v_mfma_f32_16x16x32_bf16 v[110:113], v[82:85], v[46:49], 0
	v_min_f32_e32 v74, 0, v74
	v_mul_f32_e32 v74, 0x3fb8aa3b, v74
	v_exp_f32_e32 v120, v74
	v_mfma_f32_16x16x32_bf16 v[82:85], v[82:85], v[20:23], 0
	v_sub_f32_e32 v74, v102, v32
	v_sub_f32_e32 v75, v102, v118
	v_min_f32_e32 v74, 0, v74
	v_min_f32_e32 v75, 0, v75
	v_mfma_f32_16x16x32_bf16 v[82:85], v[92:95], v[16:19], v[82:85]
	v_mul_f32_e32 v74, 0x3fb8aa3b, v74
	v_mul_f32_e32 v75, 0x3fb8aa3b, v75
	v_exp_f32_e32 v74, v74
	v_exp_f32_e32 v75, v75
	v_mfma_f32_16x16x32_bf16 v[82:85], v[96:99], v[8:11], v[82:85]
	v_mul_f32_e64 v74, v90, v74
	v_mul_f32_e64 v75, v91, v75
	v_mfma_f32_16x16x32_bf16 v[110:113], v[92:95], v[42:45], v[110:113]
	v_mul_f32_e64 v74, v74, v80
	v_mul_f32_e64 v75, v75, v81
	v_sub_f32_e32 v80, v28, v100
	v_min_f32_e32 v80, 0, v80
	v_mfma_f32_16x16x32_bf16 v[92:95], v[104:107], v[12:15], v[82:85]
	v_mul_f32_e32 v80, 0x3fb8aa3b, v80
	v_exp_f32_e32 v116, v80
	v_sub_f32_e32 v80, v28, v101
	v_sub_f32_e32 v82, v29, v100
	v_sub_f32_e32 v83, v29, v101
	v_min_f32_e32 v82, 0, v82
	v_min_f32_e32 v83, 0, v83
	v_mfma_f32_16x16x32_bf16 v[110:113], v[96:99], v[38:41], v[110:113]
	v_mul_f32_e32 v82, 0x3fb8aa3b, v82
	v_mul_f32_e32 v83, 0x3fb8aa3b, v83
	ds_read_b64 v[96:97], v187
	v_min_f32_e32 v80, 0, v80
	v_exp_f32_e32 v82, v82
	v_exp_f32_e32 v83, v83
	v_mul_f32_e32 v80, 0x3fb8aa3b, v80
	v_exp_f32_e32 v117, v80
	v_sub_f32_e32 v80, v28, v32
	v_sub_f32_e32 v32, v29, v32
	v_min_f32_e32 v32, 0, v32
	s_waitcnt lgkmcnt(0)
	v_pk_mul_f32 v[82:83], v[96:97], v[82:83]
	v_mul_f32_e32 v32, 0x3fb8aa3b, v32
	v_sub_f32_e32 v81, v28, v118
	v_pk_mul_f32 v[82:83], v[82:83], v[92:93]
	v_exp_f32_e32 v92, v32
	v_sub_f32_e32 v32, v29, v118
	v_min_f32_e32 v80, 0, v80
	v_min_f32_e32 v81, 0, v81
	v_min_f32_e32 v32, 0, v32
	v_mul_f32_e32 v80, 0x3fb8aa3b, v80
	v_mul_f32_e32 v81, 0x3fb8aa3b, v81
	v_mul_f32_e32 v84, v96, v119
	v_mul_f32_e32 v32, 0x3fb8aa3b, v32
	v_exp_f32_e32 v80, v80
	v_exp_f32_e32 v81, v81
	v_mul_f32_e32 v78, v84, v78
	v_exp_f32_e32 v93, v32
	v_mfma_f32_16x16x32_bf16 v[110:113], v[104:107], v[24:27], v[110:113]
	v_cndmask_b32_e64 v126, v78, 0, s[46:47]
	v_mul_f32_e32 v78, v97, v120
	v_mul_f32_e32 v78, v78, v79
	v_cndmask_b32_e64 v127, 0, v78, s[48:49]
	v_pk_mul_f32 v[78:79], v[96:97], v[114:115]
	v_pk_mul_f32 v[80:81], v[90:91], v[80:81]
	v_pk_mul_f32 v[84:85], v[78:79], v[108:109]
	v_pk_mul_f32 v[78:79], v[96:97], v[116:117]
	v_pk_mul_f32 v[90:91], v[90:91], v[92:93]
	v_pk_mul_f32 v[78:79], v[78:79], v[110:111]
	v_pk_mul_f32 v[90:91], v[90:91], v[94:95]
	global_load_dwordx4 v[92:95], v[30:31], off
	global_load_dwordx4 v[96:99], v[30:31], off offset:64
	global_load_dwordx4 v[104:107], v[30:31], off offset:128
	global_load_dwordx4 v[108:111], v[30:31], off offset:192
	v_pk_mul_f32 v[80:81], v[80:81], v[112:113]
	ds_read_b128 v[112:115], v186 offset:64
	s_waitcnt vmcnt(3)
	v_mfma_f32_16x16x32_bf16 v[116:119], v[92:95], v[62:65], 0
	s_waitcnt lgkmcnt(0)
	v_sub_f32_e32 v30, v103, v112
	v_min_f32_e32 v30, 0, v30
	v_mul_f32_e32 v30, 0x3fb8aa3b, v30
	v_mfma_f32_16x16x32_bf16 v[120:123], v[92:95], v[46:49], 0
	v_exp_f32_e32 v32, v30
	v_sub_f32_e32 v30, v103, v113
	v_min_f32_e32 v30, 0, v30
	v_mfma_f32_16x16x32_bf16 v[92:95], v[92:95], v[20:23], 0
	v_mul_f32_e32 v30, 0x3fb8aa3b, v30
	v_exp_f32_e32 v128, v30
	v_sub_f32_e32 v100, v28, v112
	s_waitcnt vmcnt(2)
	v_mfma_f32_16x16x32_bf16 v[116:119], v[96:99], v[58:61], v[116:119]
	v_sub_f32_e32 v101, v28, v113
	v_min_f32_e32 v100, 0, v100
	v_min_f32_e32 v101, 0, v101
	v_mfma_f32_16x16x32_bf16 v[120:123], v[96:99], v[42:45], v[120:123]
	v_mul_f32_e32 v100, 0x3fb8aa3b, v100
	v_mul_f32_e32 v101, 0x3fb8aa3b, v101
	v_exp_f32_e32 v100, v100
	v_mfma_f32_16x16x32_bf16 v[92:95], v[96:99], v[16:19], v[92:95]
	v_sub_f32_e32 v96, v29, v112
	v_min_f32_e32 v96, 0, v96
	v_mul_f32_e32 v96, 0x3fb8aa3b, v96
	s_waitcnt vmcnt(1)
	v_mfma_f32_16x16x32_bf16 v[116:119], v[104:107], v[54:57], v[116:119]
	v_exp_f32_e32 v101, v101
	v_sub_f32_e32 v30, v103, v114
	v_sub_f32_e32 v31, v103, v115
	v_mfma_f32_16x16x32_bf16 v[120:123], v[104:107], v[38:41], v[120:123]
	v_min_f32_e32 v30, 0, v30
	v_min_f32_e32 v31, 0, v31
	v_sub_f32_e32 v124, v28, v114
	v_mfma_f32_16x16x32_bf16 v[92:95], v[104:107], v[8:11], v[92:95]
	v_exp_f32_e32 v104, v96
	v_sub_f32_e32 v96, v29, v113
	v_min_f32_e32 v96, 0, v96
	v_mul_f32_e32 v96, 0x3fb8aa3b, v96
	v_exp_f32_e32 v105, v96
	ds_read_b128 v[96:99], v187 offset:64
	s_waitcnt vmcnt(0)
	v_mfma_f32_16x16x32_bf16 v[116:119], v[108:111], v[50:53], v[116:119]
	v_sub_f32_e32 v125, v28, v115
	v_mul_f32_e32 v30, 0x3fb8aa3b, v30
	v_mul_f32_e32 v31, 0x3fb8aa3b, v31
	s_waitcnt lgkmcnt(0)
	v_mul_f32_e32 v32, v96, v32
	v_mfma_f32_16x16x32_bf16 v[120:123], v[108:111], v[24:27], v[120:123]
	s_nop 1
	v_mul_f32_e32 v32, v32, v116
	v_pk_mul_f32 v[100:101], v[96:97], v[100:101]
	v_min_f32_e32 v124, 0, v124
	v_mfma_f32_16x16x32_bf16 v[92:95], v[108:111], v[12:15], v[92:95]
	v_cndmask_b32_e64 v108, v32, 0, s[46:47]
	v_mul_f32_e32 v32, v97, v128
	v_mul_f32_e32 v32, v32, v117
	v_cndmask_b32_e64 v109, 0, v32, s[48:49]
	v_sub_f32_e32 v32, v29, v114
	v_min_f32_e32 v32, 0, v32
	v_pk_mul_f32 v[96:97], v[96:97], v[104:105]
	v_mul_f32_e32 v32, 0x3fb8aa3b, v32
	v_min_f32_e32 v125, 0, v125
	v_pk_mul_f32 v[92:93], v[96:97], v[92:93]
	v_exp_f32_e32 v96, v32
	v_sub_f32_e32 v32, v29, v115
	v_exp_f32_e32 v30, v30
	v_exp_f32_e32 v31, v31
	v_mul_f32_e32 v124, 0x3fb8aa3b, v124
	v_mul_f32_e32 v125, 0x3fb8aa3b, v125
	v_min_f32_e32 v32, 0, v32
	v_exp_f32_e32 v124, v124
	v_exp_f32_e32 v125, v125
	v_mul_f32_e32 v32, 0x3fb8aa3b, v32
	v_exp_f32_e32 v97, v32
	v_pk_mul_f32 v[30:31], v[98:99], v[30:31]
	v_pk_mul_f32 v[100:101], v[100:101], v[120:121]
	v_pk_mul_f32 v[104:105], v[30:31], v[118:119]
	v_pk_mul_f32 v[30:31], v[98:99], v[124:125]
	v_cvt_pk_bf16_f32 v78, v78, v79
	v_pk_mul_f32 v[106:107], v[30:31], v[122:123]
	v_pk_mul_f32 v[30:31], v[98:99], v[96:97]
	v_cvt_pk_bf16_f32 v79, v80, v81
	v_pk_mul_f32 v[94:95], v[30:31], v[94:95]
	v_cvt_pk_bf16_f32 v31, v74, v75
	v_cvt_pk_bf16_f32 v75, v76, v77
	v_cvt_pk_bf16_f32 v77, v104, v105
	v_cvt_pk_bf16_f32 v74, v84, v85
	v_cndmask_b32_e64 v84, v77, 0, s[52:53]
	v_lshrrev_b32_e32 v77, 16, v77
	v_cndmask_b32_e64 v77, v77, 0, s[50:51]
	v_perm_b32 v77, v77, v84, s0
	v_cvt_pk_bf16_f32 v80, v100, v101
	v_cvt_pk_bf16_f32 v81, v106, v107
	v_cvt_pk_bf16_f32 v82, v82, v83
	v_cvt_pk_bf16_f32 v83, v90, v91
	v_cvt_pk_bf16_f32 v84, v92, v93
	v_cvt_pk_bf16_f32 v85, v94, v95
	global_load_dwordx4 v[90:93], v[88:89], off
	global_load_dwordx4 v[94:97], v[88:89], off offset:64
	global_load_dwordx4 v[98:101], v[88:89], off offset:128
	global_load_dwordx4 v[104:107], v[88:89], off offset:192
	v_cvt_pk_bf16_f32 v76, v108, v109
	ds_read_b128 v[108:111], v186 offset:128
	s_waitcnt vmcnt(3)
	v_mfma_f32_16x16x32_bf16 v[112:115], v[90:93], v[46:49], 0
	s_waitcnt lgkmcnt(0)
	v_sub_f32_e32 v88, v28, v108
	v_min_f32_e32 v88, 0, v88
	v_mul_f32_e32 v88, 0x3fb8aa3b, v88
	v_exp_f32_e32 v118, v88
	v_sub_f32_e32 v88, v28, v109
	v_min_f32_e32 v88, 0, v88
	v_mul_f32_e32 v88, 0x3fb8aa3b, v88
	v_exp_f32_e32 v119, v88
	v_sub_f32_e32 v88, v28, v110
	v_min_f32_e32 v88, 0, v88
	v_mul_f32_e32 v88, 0x3fb8aa3b, v88
	v_exp_f32_e32 v116, v88
	v_sub_f32_e32 v88, v28, v111
	v_min_f32_e32 v88, 0, v88
	v_mul_f32_e32 v88, 0x3fb8aa3b, v88
	v_exp_f32_e32 v117, v88
	v_mfma_f32_16x16x32_bf16 v[88:91], v[90:93], v[20:23], 0
	v_cndmask_b32_e64 v32, v31, 0, s[52:53]
	v_lshrrev_b32_e32 v31, 16, v31
	v_cndmask_b32_e64 v31, v31, 0, s[50:51]
	s_waitcnt vmcnt(2)
	v_mfma_f32_16x16x32_bf16 v[88:91], v[94:97], v[16:19], v[88:91]
	v_perm_b32 v31, v31, v32, s0
	v_cvt_pk_bf16_f32 v30, v126, v127
	v_mul_f32_e32 v28, 0x3fb8aa3b, v28
	s_waitcnt vmcnt(1)
	v_mfma_f32_16x16x32_bf16 v[88:91], v[98:101], v[8:11], v[88:91]
	v_exp_f32_e32 v176, v28
	v_mul_f32_e32 v28, 0x3fb8aa3b, v29
	v_exp_f32_e32 v28, v28
	s_waitcnt vmcnt(0)
	v_mfma_f32_16x16x32_bf16 v[90:93], v[104:107], v[12:15], v[88:91]
	v_mov_b32_e32 v32, v33
	s_nop 1
	v_sub_f32_e32 v88, v29, v108
	v_sub_f32_e32 v89, v29, v109
	v_mfma_f32_16x16x32_bf16 v[112:115], v[94:97], v[42:45], v[112:115]
	v_min_f32_e32 v88, 0, v88
	v_min_f32_e32 v89, 0, v89
	v_mul_f32_e32 v88, 0x3fb8aa3b, v88
	v_mul_f32_e32 v89, 0x3fb8aa3b, v89
	ds_read_b128 v[94:97], v187 offset:128
	v_exp_f32_e32 v88, v88
	v_exp_f32_e32 v89, v89
	v_mfma_f32_16x16x32_bf16 v[112:115], v[98:101], v[38:41], v[112:115]
	s_waitcnt lgkmcnt(0)
	v_mul_f32_e32 v98, v94, v118
	v_pk_mul_f32 v[88:89], v[94:95], v[88:89]
	v_mfma_f32_16x16x32_bf16 v[112:115], v[104:107], v[24:27], v[112:115]
	v_mul_f32_e64 v90, v88, v90
	v_mul_f32_e64 v91, v89, v91
	v_sub_f32_e32 v88, v29, v110
	v_min_f32_e32 v88, 0, v88
	v_mul_f32_e32 v88, 0x3fb8aa3b, v88
	v_exp_f32_e32 v94, v88
	v_sub_f32_e32 v88, v29, v111
	v_min_f32_e32 v88, 0, v88
	v_mul_f32_e32 v98, v98, v112
	v_mul_f32_e32 v88, 0x3fb8aa3b, v88
	v_cndmask_b32_e64 v120, v98, 0, s[46:47]
	v_mul_f32_e32 v98, v95, v119
	v_exp_f32_e32 v95, v88
	v_mul_f32_e32 v98, v98, v113
	v_cndmask_b32_e64 v121, 0, v98, s[48:49]
	v_pk_mul_f32 v[88:89], v[96:97], v[116:117]
	v_pk_mul_f32 v[94:95], v[96:97], v[94:95]
	v_pk_mul_f32 v[88:89], v[88:89], v[114:115]
	v_pk_mul_f32 v[92:93], v[94:95], v[92:93]
	global_load_dwordx4 v[94:97], v[86:87], off
	global_load_dwordx4 v[98:101], v[86:87], off offset:64
	global_load_dwordx4 v[104:107], v[86:87], off offset:128
	global_load_dwordx4 v[108:111], v[86:87], off offset:192
	s_waitcnt vmcnt(3)
	v_mfma_f32_16x16x32_bf16 v[94:97], v[94:97], v[20:23], 0
	ds_read_b128 v[112:115], v186 offset:192
	ds_read_b128 v[116:119], v187 offset:192
	v_cvt_pk_bf16_f32 v90, v90, v91
	v_cvt_pk_bf16_f32 v91, v92, v93
	s_waitcnt vmcnt(2)
	v_mfma_f32_16x16x32_bf16 v[94:97], v[98:101], v[16:19], v[94:97]
	s_waitcnt lgkmcnt(1)
	v_sub_f32_e32 v86, v29, v112
	v_min_f32_e32 v86, 0, v86
	v_mul_f32_e32 v86, 0x3fb8aa3b, v86
	s_waitcnt vmcnt(1)
	v_mfma_f32_16x16x32_bf16 v[94:97], v[104:107], v[8:11], v[94:97]
	v_exp_f32_e32 v86, v86
	v_sub_f32_e32 v87, v29, v115
	v_min_f32_e32 v87, 0, v87
	s_waitcnt vmcnt(0)
	v_mfma_f32_16x16x32_bf16 v[94:97], v[108:111], v[12:15], v[94:97]
	s_waitcnt lgkmcnt(0)
	v_mul_f32_e32 v86, v116, v86
	v_mul_f32_e32 v87, 0x3fb8aa3b, v87
	v_exp_f32_e32 v87, v87
	s_nop 3
	v_mul_f32_e32 v86, v86, v94
	v_cndmask_b32_e64 v98, v86, 0, s[46:47]
	v_sub_f32_e32 v86, v29, v113
	v_min_f32_e32 v86, 0, v86
	v_mul_f32_e32 v86, 0x3fb8aa3b, v86
	v_exp_f32_e32 v86, v86
	s_nop 0
	v_mul_f32_e32 v86, v117, v86
	v_mul_f32_e32 v86, v86, v95
	v_cndmask_b32_e64 v99, 0, v86, s[48:49]
	v_sub_f32_e32 v86, v29, v114
	v_min_f32_e32 v86, 0, v86
	v_mul_f32_e32 v86, 0x3fb8aa3b, v86
	v_exp_f32_e32 v86, v86
	v_cvt_pk_bf16_f32 v92, v98, v99
	v_mul_f32_e32 v98, 0x3fb8aa3b, v102
	v_mul_f32_e32 v102, 0x3fb8aa3b, v103
	v_pk_mul_f32 v[86:87], v[118:119], v[86:87]
	v_exp_f32_e32 v178, v98
	v_pk_mul_f32 v[94:95], v[86:87], v[96:97]
	v_cvt_pk_bf16_f32 v87, v88, v89
	v_cvt_pk_bf16_f32 v93, v94, v95
	v_cndmask_b32_e64 v88, v87, 0, s[52:53]
	v_lshrrev_b32_e32 v87, 16, v87
	v_cndmask_b32_e64 v94, v93, 0, s[52:53]
	v_lshrrev_b32_e32 v93, 16, v93
	v_cndmask_b32_e64 v87, v87, 0, s[50:51]
	v_cndmask_b32_e64 v93, v93, 0, s[50:51]
	v_perm_b32 v87, v87, v88, s0
	v_perm_b32 v93, v93, v94, s0
	s_lshl_b64 s[0:1], s[18:19], 12
	s_lshl_b64 s[18:19], s[20:21], 6
	s_add_u32 s0, s18, s0
	s_addc_u32 s1, s19, s1
	v_mov_b32_e32 v95, s1
	v_or_b32_e32 v94, s0, v166
	v_lshlrev_b64 v[94:95], 8, v[94:95]
	v_lshl_add_u64 v[142:143], v[162:163], 0, v[94:95]
	v_cvt_pk_bf16_f32 v86, v120, v121
	global_load_dwordx4 v[106:109], v[142:143], off
	global_load_dwordx4 v[110:113], v[142:143], off offset:64
	global_load_dwordx4 v[114:117], v[142:143], off offset:128
	global_load_dwordx4 v[118:121], v[142:143], off offset:192
	s_waitcnt vmcnt(3)
	v_mfma_f32_16x16x32_bf16 v[94:97], v[106:109], v[4:7], 0
	v_exp_f32_e32 v174, v102
	v_mov_b32_e32 v88, v33
	v_mfma_f32_16x16x32_bf16 v[98:101], v[106:109], v[62:65], 0
	v_mov_b32_e32 v89, v33
	v_mfma_f32_16x16x32_bf16 v[102:105], v[106:109], v[46:49], 0
	v_mfma_f32_16x16x32_bf16 v[106:109], v[106:109], v[20:23], 0
	s_waitcnt vmcnt(2)
	v_mfma_f32_16x16x32_bf16 v[94:97], v[110:113], v[0:3], v[94:97]
	v_mfma_f32_16x16x32_bf16 v[98:101], v[110:113], v[58:61], v[98:101]
	v_mfma_f32_16x16x32_bf16 v[102:105], v[110:113], v[42:45], v[102:105]
	v_mfma_f32_16x16x32_bf16 v[106:109], v[110:113], v[16:19], v[106:109]
	v_add_co_u32_e64 v110, s[0:1], s76, v142
	s_nop 1
	v_addc_co_u32_e64 v111, s[0:1], 0, v143, s[0:1]
	v_add_co_u32_e64 v126, s[0:1], s74, v142
	s_waitcnt vmcnt(1)
	v_mfma_f32_16x16x32_bf16 v[94:97], v[114:117], v[70:73], v[94:97]
	v_addc_co_u32_e64 v127, s[0:1], 0, v143, s[0:1]
	global_load_dwordx4 v[122:125], v[126:127], off offset:-4096
	global_load_dwordx4 v[128:131], v[110:111], off offset:64
	global_load_dwordx4 v[132:135], v[110:111], off offset:128
	global_load_dwordx4 v[136:139], v[110:111], off offset:192
	v_mfma_f32_16x16x32_bf16 v[98:101], v[114:117], v[54:57], v[98:101]
	v_mfma_f32_16x16x32_bf16 v[102:105], v[114:117], v[38:41], v[102:105]
	v_mfma_f32_16x16x32_bf16 v[106:109], v[114:117], v[8:11], v[106:109]
	s_waitcnt vmcnt(4)
	v_mfma_f32_16x16x32_bf16 v[94:97], v[118:121], v[66:69], v[94:97]
	v_mfma_f32_16x16x32_bf16 v[98:101], v[118:121], v[50:53], v[98:101]
	v_mfma_f32_16x16x32_bf16 v[102:105], v[118:121], v[24:27], v[102:105]
	s_nop 5
	v_mul_f32_e64 v96, v178, v96
	v_mul_f32_e64 v97, v178, v97
	v_pk_mul_f32 v[94:95], v[178:179], v[94:95] op_sel_hi:[0,1]
	v_mfma_f32_16x16x32_bf16 v[106:109], v[118:121], v[12:15], v[106:109]
	s_waitcnt vmcnt(3)
	v_mfma_f32_16x16x32_bf16 v[110:113], v[122:125], v[4:7], 0
	v_mul_f32_e64 v104, v176, v104
	v_mul_f32_e64 v105, v176, v105
	v_pk_mul_f32 v[102:103], v[176:177], v[102:103] op_sel_hi:[0,1]
	s_nop 2
	v_pk_mul_f32 v[108:109], v[28:29], v[108:109] op_sel_hi:[0,1]
	v_mfma_f32_16x16x32_bf16 v[114:117], v[122:125], v[62:65], 0
	v_mul_f32_e64 v106, v28, v106
	v_mul_f32_e64 v107, v28, v107
	v_mfma_f32_16x16x32_bf16 v[118:121], v[122:125], v[46:49], 0
	v_mfma_f32_16x16x32_bf16 v[122:125], v[122:125], v[20:23], 0
	s_waitcnt vmcnt(2)
	v_mfma_f32_16x16x32_bf16 v[110:113], v[128:131], v[0:3], v[110:113]
	v_mfma_f32_16x16x32_bf16 v[114:117], v[128:131], v[58:61], v[114:117]
	v_mfma_f32_16x16x32_bf16 v[118:121], v[128:131], v[42:45], v[118:121]
	v_mfma_f32_16x16x32_bf16 v[122:125], v[128:131], v[16:19], v[122:125]
	s_waitcnt vmcnt(1)
	v_mfma_f32_16x16x32_bf16 v[110:113], v[132:135], v[70:73], v[110:113]
	v_mfma_f32_16x16x32_bf16 v[114:117], v[132:135], v[54:57], v[114:117]
	v_mfma_f32_16x16x32_bf16 v[118:121], v[132:135], v[38:41], v[118:121]
	v_mfma_f32_16x16x32_bf16 v[122:125], v[132:135], v[8:11], v[122:125]
	s_waitcnt vmcnt(0)
	v_mfma_f32_16x16x32_bf16 v[110:113], v[136:139], v[66:69], v[110:113]
	v_mfma_f32_16x16x32_bf16 v[114:117], v[136:139], v[50:53], v[114:117]
	v_mfma_f32_16x16x32_bf16 v[118:121], v[136:139], v[24:27], v[118:121]
	s_nop 5
	v_mul_f32_e64 v112, v178, v112
	v_mul_f32_e64 v113, v178, v113
	v_pk_mul_f32 v[110:111], v[178:179], v[110:111] op_sel_hi:[0,1]
	v_pk_mul_f32 v[116:117], v[174:175], v[116:117] op_sel_hi:[0,1]
	v_mfma_f32_16x16x32_bf16 v[122:125], v[136:139], v[12:15], v[122:125]
	global_load_dwordx4 v[138:141], v[126:127], off
	global_load_dwordx4 v[144:147], v[126:127], off offset:64
	global_load_dwordx4 v[148:151], v[126:127], off offset:128
	global_load_dwordx4 v[152:155], v[126:127], off offset:192
	v_pk_mul_f32 v[114:115], v[174:175], v[114:115] op_sel_hi:[0,1]
	s_waitcnt vmcnt(3)
	v_mfma_f32_16x16x32_bf16 v[126:129], v[138:141], v[4:7], 0
	v_mul_f32_e64 v120, v176, v120
	v_mul_f32_e64 v121, v176, v121
	v_pk_mul_f32 v[118:119], v[176:177], v[118:119] op_sel_hi:[0,1]
	v_pk_mul_f32 v[124:125], v[28:29], v[124:125] op_sel_hi:[0,1]
	v_mfma_f32_16x16x32_bf16 v[130:133], v[138:141], v[62:65], 0
	v_mul_f32_e64 v122, v28, v122
	v_mul_f32_e64 v123, v28, v123
	v_mfma_f32_16x16x32_bf16 v[134:137], v[138:141], v[46:49], 0
	v_mfma_f32_16x16x32_bf16 v[138:141], v[138:141], v[20:23], 0
	s_waitcnt vmcnt(2)
	v_mfma_f32_16x16x32_bf16 v[126:129], v[144:147], v[0:3], v[126:129]
	v_mfma_f32_16x16x32_bf16 v[130:133], v[144:147], v[58:61], v[130:133]
	v_mfma_f32_16x16x32_bf16 v[134:137], v[144:147], v[42:45], v[134:137]
	v_mfma_f32_16x16x32_bf16 v[138:141], v[144:147], v[16:19], v[138:141]
	s_waitcnt vmcnt(1)
	v_mfma_f32_16x16x32_bf16 v[126:129], v[148:151], v[70:73], v[126:129]
	v_mfma_f32_16x16x32_bf16 v[130:133], v[148:151], v[54:57], v[130:133]
	v_mfma_f32_16x16x32_bf16 v[134:137], v[148:151], v[38:41], v[134:137]
	v_mfma_f32_16x16x32_bf16 v[138:141], v[148:151], v[8:11], v[138:141]
	s_waitcnt vmcnt(0)
	v_mfma_f32_16x16x32_bf16 v[126:129], v[152:155], v[66:69], v[126:129]
	v_mfma_f32_16x16x32_bf16 v[130:133], v[152:155], v[50:53], v[130:133]
	v_mfma_f32_16x16x32_bf16 v[134:137], v[152:155], v[24:27], v[134:137]
	s_nop 5
	v_mul_f32_e64 v128, v178, v128
	v_mul_f32_e64 v129, v178, v129
	v_pk_mul_f32 v[126:127], v[178:179], v[126:127] op_sel_hi:[0,1]
	v_pk_mul_f32 v[132:133], v[174:175], v[132:133] op_sel_hi:[0,1]
	v_mfma_f32_16x16x32_bf16 v[138:141], v[152:155], v[12:15], v[138:141]
	v_add_co_u32_e64 v154, s[0:1], s77, v142
	v_pk_mul_f32 v[130:131], v[174:175], v[130:131] op_sel_hi:[0,1]
	s_nop 0
	v_addc_co_u32_e64 v155, s[0:1], 0, v143, s[0:1]
	global_load_dwordx4 v[142:145], v[154:155], off
	global_load_dwordx4 v[146:149], v[154:155], off offset:64
	global_load_dwordx4 v[150:153], v[154:155], off offset:128
	s_nop 0
	global_load_dwordx4 v[154:157], v[154:155], off offset:192
	s_waitcnt vmcnt(3)
	v_mfma_f32_16x16x32_bf16 v[4:7], v[142:145], v[4:7], 0
	v_mul_f32_e64 v136, v176, v136
	v_mul_f32_e64 v137, v176, v137
	v_pk_mul_f32 v[134:135], v[176:177], v[134:135] op_sel_hi:[0,1]
	s_waitcnt vmcnt(2)
	v_mfma_f32_16x16x32_bf16 v[0:3], v[146:149], v[0:3], v[4:7]
	v_mul_f32_e64 v140, v28, v140
	v_mul_f32_e64 v141, v28, v141
	v_pk_mul_f32 v[138:139], v[28:29], v[138:139] op_sel_hi:[0,1]
	s_add_u32 s0, s62, s16
	s_waitcnt vmcnt(1)
	v_mfma_f32_16x16x32_bf16 v[0:3], v[150:153], v[70:73], v[0:3]
	s_addc_u32 s1, s63, s17
	s_waitcnt vmcnt(0)
	v_mfma_f32_16x16x32_bf16 v[0:3], v[154:157], v[66:69], v[0:3]
	s_nop 7
	v_pk_mul_f32 v[68:69], v[178:179], v[2:3] op_sel_hi:[0,1]
	v_pk_mul_f32 v[66:67], v[178:179], v[0:1] op_sel_hi:[0,1]
	v_mfma_f32_16x16x32_bf16 v[0:3], v[142:145], v[62:65], 0
	v_mfma_f32_16x16x32_bf16 v[0:3], v[146:149], v[58:61], v[0:3]
	v_mfma_f32_16x16x32_bf16 v[0:3], v[150:153], v[54:57], v[0:3]
	v_mfma_f32_16x16x32_bf16 v[0:3], v[154:157], v[50:53], v[0:3]
	s_nop 7
	v_pk_mul_f32 v[72:73], v[174:175], v[2:3] op_sel_hi:[0,1]
	v_pk_mul_f32 v[70:71], v[174:175], v[0:1] op_sel_hi:[0,1]
	v_mfma_f32_16x16x32_bf16 v[0:3], v[142:145], v[46:49], 0
	v_mfma_f32_16x16x32_bf16 v[0:3], v[146:149], v[42:45], v[0:3]
	v_mfma_f32_16x16x32_bf16 v[0:3], v[150:153], v[38:41], v[0:3]
	v_mfma_f32_16x16x32_bf16 v[0:3], v[154:157], v[24:27], v[0:3]
	s_nop 7
	v_pk_mul_f32 v[26:27], v[176:177], v[2:3] op_sel_hi:[0,1]
	v_pk_mul_f32 v[24:25], v[176:177], v[0:1] op_sel_hi:[0,1]
	v_mfma_f32_16x16x32_bf16 v[0:3], v[142:145], v[20:23], 0
	v_mfma_f32_16x16x32_bf16 v[0:3], v[146:149], v[16:19], v[0:3]
	v_mul_f32_e64 v18, v174, v100
	v_mul_f32_e64 v19, v174, v101
	v_pk_mul_f32 v[16:17], v[174:175], v[98:99] op_sel_hi:[0,1]
	v_mfma_f32_16x16x32_bf16 v[0:3], v[150:153], v[8:11], v[0:3]
	v_mfma_f32_16x16x32_bf16 v[0:3], v[154:157], v[12:15], v[0:3]
	s_nop 7
	v_pk_mul_f32 v[10:11], v[28:29], v[2:3] op_sel_hi:[0,1]
	v_pk_mul_f32 v[8:9], v[28:29], v[0:1] op_sel_hi:[0,1]
	ds_read_b64_tr_b16 v[2:3], v213 offset:2560
	ds_read_b64_tr_b16 v[0:1], v213
	ds_read_b64_tr_b16 v[4:5], v213 offset:32
	ds_read_b64_tr_b16 v[12:13], v213 offset:5120
	ds_read_b64_tr_b16 v[14:15], v213 offset:7680
	s_waitcnt lgkmcnt(3)
	v_mfma_f32_16x16x32_bf16 v[94:97], v[0:3], v[30:33], v[94:97]
	v_mfma_f32_16x16x32_bf16 v[50:53], v[0:3], v[74:77], v[16:19]
	v_mfma_f32_16x16x32_bf16 v[16:19], v[0:3], v[78:81], v[102:105]
	v_mfma_f32_16x16x32_bf16 v[0:3], v[0:3], v[82:85], v[106:109]
	s_waitcnt lgkmcnt(0)
	v_mfma_f32_16x16x32_bf16 v[38:41], v[12:15], v[86:89], v[16:19]
	v_mfma_f32_16x16x32_bf16 v[12:15], v[12:15], v[90:93], v[0:3]
	ds_read_b64_tr_b16 v[6:7], v213 offset:2592
	s_nop 3
	ds_read_b64_tr_b16 v[0:1], v213 offset:5152
	ds_read_b64_tr_b16 v[2:3], v213 offset:7712
	s_waitcnt lgkmcnt(2)
	v_mfma_f32_16x16x32_bf16 v[62:65], v[4:7], v[30:33], v[110:113]
	v_mfma_f32_16x16x32_bf16 v[46:49], v[4:7], v[74:77], v[114:117]
	v_mfma_f32_16x16x32_bf16 v[16:19], v[4:7], v[78:81], v[118:121]
	v_mfma_f32_16x16x32_bf16 v[4:7], v[4:7], v[82:85], v[122:125]
	s_waitcnt lgkmcnt(0)
	v_mfma_f32_16x16x32_bf16 v[20:23], v[0:3], v[86:89], v[16:19]
	v_mfma_f32_16x16x32_bf16 v[4:7], v[0:3], v[90:93], v[4:7]
	ds_read_b64_tr_b16 v[0:1], v213 offset:64
	ds_read_b64_tr_b16 v[2:3], v213 offset:2624
	ds_read_b64_tr_b16 v[54:55], v213 offset:5184
	ds_read_b64_tr_b16 v[56:57], v213 offset:7744
	ds_read_b64_tr_b16 v[98:99], v213 offset:96
	ds_read_b64_tr_b16 v[100:101], v213 offset:2656
	ds_read_b64_tr_b16 v[102:103], v213 offset:5216
	ds_read_b64_tr_b16 v[104:105], v213 offset:7776
	s_waitcnt lgkmcnt(6)
	v_mfma_f32_16x16x32_bf16 v[58:61], v[0:3], v[30:33], v[126:129]
	v_mfma_f32_16x16x32_bf16 v[42:45], v[0:3], v[74:77], v[130:133]
	v_mfma_f32_16x16x32_bf16 v[16:19], v[0:3], v[78:81], v[134:137]
	v_mfma_f32_16x16x32_bf16 v[0:3], v[0:3], v[82:85], v[138:141]
	s_waitcnt lgkmcnt(4)
	v_mfma_f32_16x16x32_bf16 v[16:19], v[54:57], v[86:89], v[16:19]
	v_mfma_f32_16x16x32_bf16 v[0:3], v[54:57], v[90:93], v[0:3]
	s_waitcnt lgkmcnt(2)
	v_mfma_f32_16x16x32_bf16 v[54:57], v[98:101], v[30:33], v[66:69]
	v_add_u32_e32 v32, v192, v158
	v_mfma_f32_16x16x32_bf16 v[28:31], v[98:101], v[74:77], v[70:73]
	s_nop 0
	ds_read_b64 v[68:69], v32
	v_lshlrev_b32_e32 v32, 1, v170
	global_load_dword v70, v33, s[0:1] offset:768
	s_add_u32 s0, s2, s14
	s_addc_u32 s1, s3, s15
	v_mfma_f32_16x16x32_bf16 v[24:27], v[98:101], v[78:81], v[24:27]
	v_mov_b64_e32 v[78:79], s[0:1]
	v_mad_i64_i32 v[66:67], s[0:1], v172, s96, v[78:79]
	v_lshl_add_u64 v[72:73], v[66:67], 0, v[32:33]
	global_load_dwordx2 v[74:75], v[72:73], off
	s_waitcnt lgkmcnt(0)
	v_lshlrev_b32_e32 v66, 16, v68
	v_and_b32_e32 v67, 0xffff0000, v68
	v_mfma_f32_16x16x32_bf16 v[8:11], v[98:101], v[82:85], v[8:11]
	s_waitcnt vmcnt(1)
	v_pk_fma_f32 v[66:67], v[70:71], v[66:67], v[94:95] op_sel_hi:[0,1,1]
	v_mfma_f32_16x16x32_bf16 v[24:27], v[102:105], v[86:89], v[24:27]
	s_waitcnt vmcnt(0)
	v_lshlrev_b32_e32 v76, 16, v74
	v_mul_f32_e32 v68, 0xbfb8aa3b, v76
	v_exp_f32_e32 v68, v68
	v_and_b32_e32 v77, 0xffff0000, v74
	v_lshlrev_b32_e32 v74, 16, v75
	v_mul_f32_e32 v71, 0xbfb8aa3b, v74
	v_add_f32_e32 v68, 1.0, v68
	v_rcp_f32_e32 v80, v68
	v_mul_f32_e32 v68, 0xbfb8aa3b, v77
	v_exp_f32_e32 v68, v68
	v_exp_f32_e32 v71, v71
	v_pk_mul_f32 v[66:67], v[66:67], v[76:77]
	v_and_b32_e32 v75, 0xffff0000, v75
	v_add_f32_e32 v68, 1.0, v68
	v_rcp_f32_e32 v81, v68
	v_add_f32_e32 v71, 1.0, v71
	v_mfma_f32_16x16x32_bf16 v[8:11], v[102:105], v[90:93], v[8:11]
	v_mul_f32_e64 v66, v66, v80
	v_mul_f32_e64 v67, v67, v81
	v_mul_f32_e32 v68, v67, v67
	v_pk_fma_f32 v[76:77], v[66:67], v[66:67], v[68:69] op_sel_hi:[1,1,0]
	v_lshlrev_b32_e32 v68, 16, v69
	v_and_b32_e32 v69, 0xffff0000, v69
	v_rcp_f32_e32 v80, v71
	v_pk_fma_f32 v[68:69], v[70:71], v[68:69], v[96:97] op_sel_hi:[0,1,1]
	v_mul_f32_e32 v71, 0xbfb8aa3b, v75
	v_exp_f32_e32 v71, v71
	v_pk_mul_f32 v[68:69], v[68:69], v[74:75]
	v_add_f32_e32 v71, 1.0, v71
	v_rcp_f32_e32 v81, v71
	v_add_u32_e32 v71, v192, v193
	v_pk_mul_f32 v[68:69], v[68:69], v[80:81]
	global_load_dwordx2 v[80:81], v[72:73], off offset:32
	v_pk_fma_f32 v[74:75], v[68:69], v[68:69], v[76:77]
	v_mul_f32_e32 v76, v69, v69
	v_pk_add_f32 v[74:75], v[76:77], v[74:75] op_sel_hi:[0,1]
	ds_read_b64 v[76:77], v71
	s_waitcnt lgkmcnt(0)
	v_lshlrev_b32_e32 v82, 16, v76
	v_and_b32_e32 v83, 0xffff0000, v76
	s_waitcnt vmcnt(0)
	v_lshlrev_b32_e32 v84, 16, v80
	v_mul_f32_e32 v71, 0xbfb8aa3b, v84
	v_exp_f32_e32 v71, v71
	v_and_b32_e32 v85, 0xffff0000, v80
	v_lshlrev_b32_e32 v80, 16, v81
	v_and_b32_e32 v81, 0xffff0000, v81
	v_add_f32_e32 v71, 1.0, v71
	v_rcp_f32_e32 v86, v71
	v_pk_fma_f32 v[62:63], v[70:71], v[82:83], v[62:63] op_sel_hi:[0,1,1]
	v_mul_f32_e32 v71, 0xbfb8aa3b, v85
	v_exp_f32_e32 v71, v71
	v_pk_mul_f32 v[62:63], v[62:63], v[84:85]
	v_add_f32_e32 v71, 1.0, v71
	v_rcp_f32_e32 v87, v71
	v_mul_f32_e32 v71, 0xbfb8aa3b, v80
	v_exp_f32_e32 v71, v71
	v_pk_mul_f32 v[62:63], v[62:63], v[86:87]
	s_nop 0
	v_pk_fma_f32 v[74:75], v[62:63], v[62:63], v[74:75]
	v_mul_f32_e32 v76, v63, v63
	v_pk_add_f32 v[74:75], v[76:77], v[74:75] op_sel_hi:[0,1]
	v_lshlrev_b32_e32 v76, 16, v77
	v_and_b32_e32 v77, 0xffff0000, v77
	v_add_f32_e32 v71, 1.0, v71
	v_pk_fma_f32 v[64:65], v[70:71], v[76:77], v[64:65] op_sel_hi:[0,1,1]
	v_rcp_f32_e32 v82, v71
	v_pk_mul_f32 v[64:65], v[64:65], v[80:81]
	v_mul_f32_e32 v71, 0xbfb8aa3b, v81
	global_load_dwordx2 v[80:81], v[72:73], off offset:64
	v_exp_f32_e32 v71, v71
	s_waitcnt vmcnt(0)
	v_lshlrev_b32_e32 v84, 16, v80
	v_add_f32_e32 v71, 1.0, v71
	v_rcp_f32_e32 v83, v71
	v_add_u32_e32 v71, v192, v194
	v_and_b32_e32 v85, 0xffff0000, v80
	v_lshlrev_b32_e32 v80, 16, v81
	v_pk_mul_f32 v[64:65], v[64:65], v[82:83]
	v_and_b32_e32 v81, 0xffff0000, v81
	v_pk_fma_f32 v[74:75], v[64:65], v[64:65], v[74:75]
	v_mul_f32_e32 v76, v65, v65
	v_pk_add_f32 v[74:75], v[76:77], v[74:75] op_sel_hi:[0,1]
	ds_read_b64 v[76:77], v71
	v_mul_f32_e32 v71, 0xbfb8aa3b, v84
	v_exp_f32_e32 v71, v71
	s_waitcnt lgkmcnt(0)
	v_lshlrev_b32_e32 v82, 16, v76
	v_and_b32_e32 v83, 0xffff0000, v76
	v_add_f32_e32 v71, 1.0, v71
	v_rcp_f32_e32 v86, v71
	v_pk_fma_f32 v[58:59], v[70:71], v[82:83], v[58:59] op_sel_hi:[0,1,1]
	v_mul_f32_e32 v71, 0xbfb8aa3b, v85
	v_exp_f32_e32 v71, v71
	v_pk_mul_f32 v[58:59], v[58:59], v[84:85]
	v_add_f32_e32 v71, 1.0, v71
	v_rcp_f32_e32 v87, v71
	v_mul_f32_e32 v71, 0xbfb8aa3b, v80
	v_exp_f32_e32 v71, v71
	v_pk_mul_f32 v[58:59], v[58:59], v[86:87]
	s_nop 0
	v_pk_fma_f32 v[74:75], v[58:59], v[58:59], v[74:75]
	v_mul_f32_e32 v76, v59, v59
	v_pk_add_f32 v[74:75], v[76:77], v[74:75] op_sel_hi:[0,1]
	v_lshlrev_b32_e32 v76, 16, v77
	v_and_b32_e32 v77, 0xffff0000, v77
	v_add_f32_e32 v71, 1.0, v71
	v_pk_fma_f32 v[60:61], v[70:71], v[76:77], v[60:61] op_sel_hi:[0,1,1]
	v_rcp_f32_e32 v82, v71
	v_pk_mul_f32 v[60:61], v[60:61], v[80:81]
	v_mul_f32_e32 v71, 0xbfb8aa3b, v81
	global_load_dwordx2 v[80:81], v[72:73], off offset:96
	v_exp_f32_e32 v71, v71
	s_nop 0
	v_add_f32_e32 v71, 1.0, v71
	v_rcp_f32_e32 v83, v71
	v_add_u32_e32 v71, v192, v195
	v_pk_mul_f32 v[60:61], v[60:61], v[82:83]
	s_nop 0
	v_pk_fma_f32 v[74:75], v[60:61], v[60:61], v[74:75]
	v_mul_f32_e32 v76, v61, v61
	v_pk_add_f32 v[74:75], v[76:77], v[74:75] op_sel_hi:[0,1]
	ds_read_b64 v[76:77], v71
	s_waitcnt lgkmcnt(0)
	v_lshlrev_b32_e32 v72, 16, v76
	v_and_b32_e32 v73, 0xffff0000, v76
	s_waitcnt vmcnt(0)
	v_lshlrev_b32_e32 v82, 16, v80
	v_mul_f32_e32 v71, 0xbfb8aa3b, v82
	v_exp_f32_e32 v71, v71
	v_and_b32_e32 v83, 0xffff0000, v80
	v_lshlrev_b32_e32 v76, 16, v81
	v_add_f32_e32 v71, 1.0, v71
	v_rcp_f32_e32 v84, v71
	v_pk_fma_f32 v[54:55], v[70:71], v[72:73], v[54:55] op_sel_hi:[0,1,1]
	v_mul_f32_e32 v71, 0xbfb8aa3b, v83
	v_exp_f32_e32 v71, v71
	v_pk_mul_f32 v[54:55], v[54:55], v[82:83]
	v_add_f32_e32 v71, 1.0, v71
	v_rcp_f32_e32 v85, v71
	v_mul_f32_e32 v71, 0xbfb8aa3b, v76
	v_exp_f32_e32 v71, v71
	v_pk_mul_f32 v[72:73], v[54:55], v[84:85]
	s_nop 0
	v_pk_fma_f32 v[54:55], v[72:73], v[72:73], v[74:75]
	v_mul_f32_e32 v74, v73, v73
	v_pk_add_f32 v[54:55], v[74:75], v[54:55] op_sel_hi:[0,1]
	v_lshlrev_b32_e32 v74, 16, v77
	v_and_b32_e32 v75, 0xffff0000, v77
	v_and_b32_e32 v77, 0xffff0000, v81
	v_add_f32_e32 v71, 1.0, v71
	v_rcp_f32_e32 v80, v71
	v_pk_fma_f32 v[56:57], v[70:71], v[74:75], v[56:57] op_sel_hi:[0,1,1]
	v_mul_f32_e32 v71, 0xbfb8aa3b, v77
	v_exp_f32_e32 v71, v71
	v_pk_mul_f32 v[56:57], v[56:57], v[76:77]
	v_or_b32_e32 v76, s28, v208
	v_add_f32_e32 v71, 1.0, v71
	v_rcp_f32_e32 v81, v71
	s_nop 0
	v_pk_mul_f32 v[56:57], v[56:57], v[80:81]
	s_nop 0
	v_pk_fma_f32 v[54:55], v[56:57], v[56:57], v[54:55]
	v_mul_f32_e32 v74, v57, v57
	v_pk_add_f32 v[110:111], v[74:75], v[54:55] op_sel_hi:[0,1]
	v_or_b32_e32 v54, s28, v196
	v_mad_i64_i32 v[74:75], s[0:1], v54, s96, v[78:79]
	v_lshl_add_u64 v[74:75], v[74:75], 0, v[32:33]
	global_load_dwordx2 v[126:127], v[74:75], off
	global_load_dwordx2 v[122:123], v[74:75], off offset:32
	global_load_dwordx2 v[116:117], v[74:75], off offset:64
	global_load_dwordx2 v[112:113], v[74:75], off offset:96
	v_mad_i64_i32 v[74:75], s[0:1], v76, s96, v[78:79]
	v_lshl_add_u64 v[74:75], v[74:75], 0, v[32:33]
	global_load_dwordx2 v[106:107], v[74:75], off
	global_load_dwordx2 v[102:103], v[74:75], off offset:32
	global_load_dwordx2 v[98:99], v[74:75], off offset:64
	global_load_dwordx2 v[94:95], v[74:75], off offset:96
	v_or_b32_e32 v74, s28, v210
	v_mad_i64_i32 v[78:79], s[0:1], v74, s96, v[78:79]
	v_lshl_add_u64 v[78:79], v[78:79], 0, v[32:33]
	global_load_dwordx2 v[90:91], v[78:79], off
	global_load_dwordx2 v[86:87], v[78:79], off offset:32
	global_load_dwordx2 v[82:83], v[78:79], off offset:64
	v_add_u32_e32 v55, v197, v158
	global_load_dwordx2 v[78:79], v[78:79], off offset:96
	v_add_u32_e32 v32, v211, v193
	ds_read_b64 v[120:121], v55
	ds_read_b64 v[88:89], v32
	v_add_u32_e32 v55, v197, v193
	v_add_u32_e32 v32, v211, v194
	ds_read_b64 v[124:125], v55
	ds_read_b64 v[84:85], v32
	v_add_u32_e32 v55, v197, v194
	v_add_u32_e32 v32, v211, v195
	ds_read_b64 v[118:119], v55
	ds_read_b64 v[80:81], v32
	v_add_u32_e32 v55, v197, v195
	ds_read_b64 v[114:115], v55
	v_add_u32_e32 v55, v209, v158
	ds_read_b64 v[108:109], v55
	v_add_u32_e32 v55, v209, v193
	ds_read_b64 v[104:105], v55
	v_add_u32_e32 v55, v209, v194
	ds_read_b64 v[100:101], v55
	v_add_u32_e32 v55, v209, v195
	ds_read_b64 v[96:97], v55
	v_add_u32_e32 v55, v211, v158
	ds_read_b64 v[92:93], v55
	s_lshl_b32 s0, s26, 11
	v_mov_b32_e32 v55, v110
	s_add_i32 s14, s0, 0
	s_nop 0
	v_permlane16_swap_b32_e32 v110, v55
	s_add_i32 s14, s14, 0x15000
	v_add_f32_e32 v55, v110, v55
	s_add_i32 s0, s14, s23
	v_mov_b32_e32 v71, v55
	v_lshl_add_u32 v32, v166, 2, s0
	s_nop 0
	v_permlane32_swap_b32_e32 v55, v71
	s_and_saveexec_b64 s[0:1], s[42:43]
	v_add_f32_e32 v55, v55, v71
	ds_write_b32 v32, v55
	s_or_b64 exec, exec, s[0:1]
	s_waitcnt vmcnt(11)
	v_lshlrev_b32_e32 v128, 16, v126
	v_mul_f32_e32 v55, 0xbfb8aa3b, v128
	v_exp_f32_e32 v55, v55
	v_and_b32_e32 v129, 0xffff0000, v126
	v_lshlrev_b32_e32 v126, 16, v127
	v_mov_b32_e32 v71, v70
	v_add_f32_e32 v55, 1.0, v55
	v_rcp_f32_e32 v130, v55
	v_mul_f32_e32 v55, 0xbfb8aa3b, v129
	v_exp_f32_e32 v55, v55
	s_waitcnt lgkmcnt(11)
	v_lshlrev_b32_e32 v110, 16, v120
	v_and_b32_e32 v111, 0xffff0000, v120
	v_pk_fma_f32 v[50:51], v[70:71], v[110:111], v[50:51]
	v_add_f32_e32 v55, 1.0, v55
	v_rcp_f32_e32 v131, v55
	v_mul_f32_e32 v55, 0xbfb8aa3b, v126
	v_exp_f32_e32 v55, v55
	v_and_b32_e32 v127, 0xffff0000, v127
	v_pk_mul_f32 v[50:51], v[50:51], v[128:129]
	v_lshlrev_b32_e32 v120, 16, v121
	v_add_f32_e32 v55, 1.0, v55
	v_rcp_f32_e32 v128, v55
	v_mul_f32_e32 v55, 0xbfb8aa3b, v127
	v_exp_f32_e32 v55, v55
	v_and_b32_e32 v121, 0xffff0000, v121
	v_pk_fma_f32 v[52:53], v[70:71], v[120:121], v[52:53]
	v_pk_mul_f32 v[50:51], v[50:51], v[130:131]
	v_pk_mul_f32 v[52:53], v[52:53], v[126:127]
	v_add_f32_e32 v55, 1.0, v55
	s_waitcnt vmcnt(10)
	v_lshlrev_b32_e32 v126, 16, v122
	v_rcp_f32_e32 v129, v55
	v_mul_f32_e32 v55, 0xbfb8aa3b, v126
	v_exp_f32_e32 v55, v55
	v_and_b32_e32 v127, 0xffff0000, v122
	v_pk_mul_f32 v[52:53], v[52:53], v[128:129]
	v_lshlrev_b32_e32 v122, 16, v123
	v_add_f32_e32 v55, 1.0, v55
	v_rcp_f32_e32 v128, v55
	v_mul_f32_e32 v55, 0xbfb8aa3b, v127
	v_exp_f32_e32 v55, v55
	v_mul_f32_e32 v110, v51, v51
	v_pk_fma_f32 v[110:111], v[50:51], v[50:51], v[110:111] op_sel_hi:[1,1,0]
	v_mul_f32_e32 v120, v53, v53
	v_add_f32_e32 v55, 1.0, v55
	v_rcp_f32_e32 v129, v55
	v_mul_f32_e32 v55, 0xbfb8aa3b, v122
	v_exp_f32_e32 v55, v55
	v_pk_fma_f32 v[110:111], v[52:53], v[52:53], v[110:111]
	v_and_b32_e32 v123, 0xffff0000, v123
	v_pk_add_f32 v[110:111], v[120:121], v[110:111] op_sel_hi:[0,1]
	s_waitcnt lgkmcnt(9)
	v_lshlrev_b32_e32 v120, 16, v124
	v_and_b32_e32 v121, 0xffff0000, v124
	v_pk_fma_f32 v[46:47], v[70:71], v[120:121], v[46:47]
	v_add_f32_e32 v55, 1.0, v55
	v_pk_mul_f32 v[46:47], v[46:47], v[126:127]
	v_rcp_f32_e32 v124, v55
	v_mul_f32_e32 v55, 0xbfb8aa3b, v123
	v_pk_mul_f32 v[46:47], v[46:47], v[128:129]
	v_exp_f32_e32 v55, v55
	v_pk_fma_f32 v[110:111], v[46:47], v[46:47], v[110:111]
	v_mul_f32_e32 v120, v47, v47
	v_pk_add_f32 v[110:111], v[120:121], v[110:111] op_sel_hi:[0,1]
	v_lshlrev_b32_e32 v120, 16, v125
	v_and_b32_e32 v121, 0xffff0000, v125
	v_pk_fma_f32 v[48:49], v[70:71], v[120:121], v[48:49]
	v_add_f32_e32 v55, 1.0, v55
	v_pk_mul_f32 v[48:49], v[48:49], v[122:123]
	s_waitcnt vmcnt(9)
	v_lshlrev_b32_e32 v122, 16, v116
	v_rcp_f32_e32 v125, v55
	v_mul_f32_e32 v55, 0xbfb8aa3b, v122
	v_exp_f32_e32 v55, v55
	v_and_b32_e32 v123, 0xffff0000, v116
	v_pk_mul_f32 v[48:49], v[48:49], v[124:125]
	v_add_f32_e32 v55, 1.0, v55
	v_rcp_f32_e32 v124, v55
	v_mul_f32_e32 v55, 0xbfb8aa3b, v123
	v_exp_f32_e32 v55, v55
	v_pk_fma_f32 v[110:111], v[48:49], v[48:49], v[110:111]
	v_mul_f32_e32 v120, v49, v49
	v_pk_add_f32 v[110:111], v[120:121], v[110:111] op_sel_hi:[0,1]
	v_add_f32_e32 v55, 1.0, v55
	v_rcp_f32_e32 v125, v55
	s_waitcnt lgkmcnt(7)
	v_lshlrev_b32_e32 v120, 16, v118
	v_and_b32_e32 v121, 0xffff0000, v118
	v_pk_fma_f32 v[42:43], v[70:71], v[120:121], v[42:43]
	v_lshlrev_b32_e32 v118, 16, v119
	v_pk_mul_f32 v[42:43], v[42:43], v[122:123]
	v_and_b32_e32 v119, 0xffff0000, v119
	v_pk_mul_f32 v[42:43], v[42:43], v[124:125]
	v_pk_fma_f32 v[44:45], v[70:71], v[118:119], v[44:45]
	v_pk_fma_f32 v[110:111], v[42:43], v[42:43], v[110:111]
	v_mul_f32_e32 v116, v43, v43
	v_pk_add_f32 v[110:111], v[116:117], v[110:111] op_sel_hi:[0,1]
	v_lshlrev_b32_e32 v116, 16, v117
	v_mul_f32_e32 v55, 0xbfb8aa3b, v116
	v_exp_f32_e32 v55, v55
	v_and_b32_e32 v117, 0xffff0000, v117
	s_waitcnt vmcnt(8)
	v_lshlrev_b32_e32 v118, 16, v112
	v_pk_mul_f32 v[44:45], v[44:45], v[116:117]
	v_add_f32_e32 v55, 1.0, v55
	v_rcp_f32_e32 v120, v55
	v_mul_f32_e32 v55, 0xbfb8aa3b, v117
	v_exp_f32_e32 v55, v55
	v_and_b32_e32 v119, 0xffff0000, v112
	v_add_f32_e32 v55, 1.0, v55
	v_rcp_f32_e32 v121, v55
	v_mul_f32_e32 v55, 0xbfb8aa3b, v118
	v_exp_f32_e32 v55, v55
	v_pk_mul_f32 v[44:45], v[44:45], v[120:121]
	s_nop 0
	v_pk_fma_f32 v[110:111], v[44:45], v[44:45], v[110:111]
	v_add_f32_e32 v55, 1.0, v55
	v_rcp_f32_e32 v120, v55
	v_mul_f32_e32 v55, 0xbfb8aa3b, v119
	v_exp_f32_e32 v55, v55
	v_mul_f32_e32 v116, v45, v45
	v_pk_add_f32 v[110:111], v[116:117], v[110:111] op_sel_hi:[0,1]
	s_waitcnt lgkmcnt(5)
	v_lshlrev_b32_e32 v116, 16, v114
	v_add_f32_e32 v55, 1.0, v55
	v_rcp_f32_e32 v121, v55
	v_and_b32_e32 v117, 0xffff0000, v114
	v_pk_fma_f32 v[28:29], v[70:71], v[116:117], v[28:29]
	v_lshlrev_b32_e32 v114, 16, v115
	v_pk_mul_f32 v[28:29], v[28:29], v[118:119]
	v_and_b32_e32 v115, 0xffff0000, v115
	v_pk_mul_f32 v[28:29], v[28:29], v[120:121]
	v_pk_fma_f32 v[30:31], v[70:71], v[114:115], v[30:31]
	v_pk_fma_f32 v[110:111], v[28:29], v[28:29], v[110:111]
	v_mul_f32_e32 v112, v29, v29
	v_pk_add_f32 v[110:111], v[112:113], v[110:111] op_sel_hi:[0,1]
	v_lshlrev_b32_e32 v112, 16, v113
	v_mul_f32_e32 v55, 0xbfb8aa3b, v112
	v_exp_f32_e32 v55, v55
	v_and_b32_e32 v113, 0xffff0000, v113
	v_pk_mul_f32 v[30:31], v[30:31], v[112:113]
	v_add_f32_e32 v55, 1.0, v55
	v_rcp_f32_e32 v116, v55
	v_mul_f32_e32 v55, 0xbfb8aa3b, v113
	v_exp_f32_e32 v55, v55
	s_nop 0
	v_add_f32_e32 v55, 1.0, v55
	v_rcp_f32_e32 v117, v55
	s_nop 0
	v_pk_mul_f32 v[30:31], v[30:31], v[116:117]
	s_nop 0
	v_pk_fma_f32 v[110:111], v[30:31], v[30:31], v[110:111]
	v_mul_f32_e32 v112, v31, v31
	v_pk_add_f32 v[110:111], v[112:113], v[110:111] op_sel_hi:[0,1]
	v_mov_b32_e32 v55, v110
	s_nop 1
	v_permlane16_swap_b32_e32 v110, v55
	v_add_f32_e32 v55, v110, v55
	v_mov_b32_e32 v75, v55
	s_nop 1
	v_permlane32_swap_b32_e32 v55, v75
	s_and_saveexec_b64 s[0:1], s[42:43]
	v_add_f32_e32 v55, v55, v75
	ds_write_b32 v32, v55 offset:64
	s_or_b64 exec, exec, s[0:1]
	s_waitcnt vmcnt(7)
	v_lshlrev_b32_e32 v112, 16, v106
	v_mul_f32_e32 v55, 0xbfb8aa3b, v112
	v_exp_f32_e32 v55, v55
	v_and_b32_e32 v113, 0xffff0000, v106
	s_waitcnt lgkmcnt(4)
	v_lshlrev_b32_e32 v110, 16, v108
	v_and_b32_e32 v111, 0xffff0000, v108
	v_add_f32_e32 v55, 1.0, v55
	v_rcp_f32_e32 v114, v55
	v_mul_f32_e32 v55, 0xbfb8aa3b, v113
	v_exp_f32_e32 v55, v55
	v_pk_fma_f32 v[38:39], v[70:71], v[110:111], v[38:39]
	v_lshlrev_b32_e32 v108, 16, v109
	v_pk_mul_f32 v[38:39], v[38:39], v[112:113]
	v_add_f32_e32 v55, 1.0, v55
	v_rcp_f32_e32 v115, v55
	v_and_b32_e32 v109, 0xffff0000, v109
	v_pk_fma_f32 v[40:41], v[70:71], v[108:109], v[40:41]
	v_pk_mul_f32 v[38:39], v[38:39], v[114:115]
	s_nop 0
	v_mul_f32_e32 v106, v39, v39
	v_pk_fma_f32 v[110:111], v[38:39], v[38:39], v[106:107] op_sel_hi:[1,1,0]
	v_lshlrev_b32_e32 v106, 16, v107
	v_mul_f32_e32 v55, 0xbfb8aa3b, v106
	v_exp_f32_e32 v55, v55
	v_and_b32_e32 v107, 0xffff0000, v107
	v_pk_mul_f32 v[40:41], v[40:41], v[106:107]
	v_add_f32_e32 v55, 1.0, v55
	v_rcp_f32_e32 v112, v55
	v_mul_f32_e32 v55, 0xbfb8aa3b, v107
	v_exp_f32_e32 v55, v55
	s_nop 0
	v_add_f32_e32 v55, 1.0, v55
	v_rcp_f32_e32 v113, v55
	s_nop 0
	v_pk_mul_f32 v[40:41], v[40:41], v[112:113]
	s_nop 0
	v_pk_fma_f32 v[106:107], v[40:41], v[40:41], v[110:111]
	s_waitcnt vmcnt(6)
	v_lshlrev_b32_e32 v110, 16, v102
	v_mul_f32_e32 v55, 0xbfb8aa3b, v110
	v_exp_f32_e32 v55, v55
	v_and_b32_e32 v111, 0xffff0000, v102
	v_mul_f32_e32 v108, v41, v41
	v_pk_add_f32 v[106:107], v[108:109], v[106:107] op_sel_hi:[0,1]
	v_add_f32_e32 v55, 1.0, v55
	v_rcp_f32_e32 v112, v55
	v_mul_f32_e32 v55, 0xbfb8aa3b, v111
	v_exp_f32_e32 v55, v55
	s_waitcnt lgkmcnt(3)
	v_lshlrev_b32_e32 v108, 16, v104
	v_and_b32_e32 v109, 0xffff0000, v104
	v_pk_fma_f32 v[20:21], v[70:71], v[108:109], v[20:21]
	v_add_f32_e32 v55, 1.0, v55
	v_rcp_f32_e32 v113, v55
	v_pk_mul_f32 v[20:21], v[20:21], v[110:111]
	v_lshlrev_b32_e32 v104, 16, v105
	v_and_b32_e32 v105, 0xffff0000, v105
	v_pk_mul_f32 v[20:21], v[20:21], v[112:113]
	v_pk_fma_f32 v[22:23], v[70:71], v[104:105], v[22:23]
	v_pk_fma_f32 v[106:107], v[20:21], v[20:21], v[106:107]
	v_mul_f32_e32 v102, v21, v21
	v_pk_add_f32 v[106:107], v[102:103], v[106:107] op_sel_hi:[0,1]
	v_lshlrev_b32_e32 v102, 16, v103
	v_mul_f32_e32 v55, 0xbfb8aa3b, v102
	v_exp_f32_e32 v55, v55
	v_and_b32_e32 v103, 0xffff0000, v103
	v_pk_mul_f32 v[22:23], v[22:23], v[102:103]
	v_add_f32_e32 v55, 1.0, v55
	v_rcp_f32_e32 v108, v55
	v_mul_f32_e32 v55, 0xbfb8aa3b, v103
	v_exp_f32_e32 v55, v55
	s_nop 0
	v_add_f32_e32 v55, 1.0, v55
	v_rcp_f32_e32 v109, v55
	s_nop 0
	v_pk_mul_f32 v[22:23], v[22:23], v[108:109]
	s_nop 0
	v_pk_fma_f32 v[102:103], v[22:23], v[22:23], v[106:107]
	s_waitcnt vmcnt(5)
	v_lshlrev_b32_e32 v106, 16, v98
	v_mul_f32_e32 v55, 0xbfb8aa3b, v106
	v_exp_f32_e32 v55, v55
	v_and_b32_e32 v107, 0xffff0000, v98
	v_mul_f32_e32 v104, v23, v23
	v_pk_add_f32 v[102:103], v[104:105], v[102:103] op_sel_hi:[0,1]
	v_add_f32_e32 v55, 1.0, v55
	v_rcp_f32_e32 v108, v55
	v_mul_f32_e32 v55, 0xbfb8aa3b, v107
	v_exp_f32_e32 v55, v55
	s_waitcnt lgkmcnt(2)
	v_lshlrev_b32_e32 v104, 16, v100
	v_and_b32_e32 v105, 0xffff0000, v100
	v_pk_fma_f32 v[16:17], v[70:71], v[104:105], v[16:17]
	v_add_f32_e32 v55, 1.0, v55
	v_rcp_f32_e32 v109, v55
	v_pk_mul_f32 v[16:17], v[16:17], v[106:107]
	v_lshlrev_b32_e32 v100, 16, v101
	v_and_b32_e32 v101, 0xffff0000, v101
	v_pk_mul_f32 v[16:17], v[16:17], v[108:109]
	v_pk_fma_f32 v[18:19], v[70:71], v[100:101], v[18:19]
	v_pk_fma_f32 v[102:103], v[16:17], v[16:17], v[102:103]
	v_mul_f32_e32 v98, v17, v17
	v_pk_add_f32 v[102:103], v[98:99], v[102:103] op_sel_hi:[0,1]
	v_lshlrev_b32_e32 v98, 16, v99
	v_mul_f32_e32 v55, 0xbfb8aa3b, v98
	v_exp_f32_e32 v55, v55
	v_and_b32_e32 v99, 0xffff0000, v99
	v_pk_mul_f32 v[18:19], v[18:19], v[98:99]
	v_add_f32_e32 v55, 1.0, v55
	v_rcp_f32_e32 v104, v55
	v_mul_f32_e32 v55, 0xbfb8aa3b, v99
	v_exp_f32_e32 v55, v55
	s_nop 0
	v_add_f32_e32 v55, 1.0, v55
	v_rcp_f32_e32 v105, v55
	s_nop 0
	v_pk_mul_f32 v[18:19], v[18:19], v[104:105]
	s_nop 0
	v_pk_fma_f32 v[98:99], v[18:19], v[18:19], v[102:103]
	s_waitcnt vmcnt(4)
	v_lshlrev_b32_e32 v102, 16, v94
	v_mul_f32_e32 v55, 0xbfb8aa3b, v102
	v_exp_f32_e32 v55, v55
	v_and_b32_e32 v103, 0xffff0000, v94
	v_mul_f32_e32 v100, v19, v19
	v_pk_add_f32 v[98:99], v[100:101], v[98:99] op_sel_hi:[0,1]
	v_add_f32_e32 v55, 1.0, v55
	v_rcp_f32_e32 v104, v55
	v_mul_f32_e32 v55, 0xbfb8aa3b, v103
	v_exp_f32_e32 v55, v55
	s_waitcnt lgkmcnt(1)
	v_lshlrev_b32_e32 v100, 16, v96
	v_and_b32_e32 v101, 0xffff0000, v96
	v_pk_fma_f32 v[24:25], v[70:71], v[100:101], v[24:25]
	v_add_f32_e32 v55, 1.0, v55
	v_rcp_f32_e32 v105, v55
	v_pk_mul_f32 v[24:25], v[24:25], v[102:103]
	v_lshlrev_b32_e32 v96, 16, v97
	v_and_b32_e32 v97, 0xffff0000, v97
	v_pk_mul_f32 v[24:25], v[24:25], v[104:105]
	v_pk_fma_f32 v[26:27], v[70:71], v[96:97], v[26:27]
	v_pk_fma_f32 v[98:99], v[24:25], v[24:25], v[98:99]
	v_mul_f32_e32 v94, v25, v25
	v_pk_add_f32 v[98:99], v[94:95], v[98:99] op_sel_hi:[0,1]
	v_lshlrev_b32_e32 v94, 16, v95
	v_mul_f32_e32 v55, 0xbfb8aa3b, v94
	v_exp_f32_e32 v55, v55
	v_and_b32_e32 v95, 0xffff0000, v95
	v_pk_mul_f32 v[26:27], v[26:27], v[94:95]
	v_add_f32_e32 v55, 1.0, v55
	v_rcp_f32_e32 v100, v55
	v_mul_f32_e32 v55, 0xbfb8aa3b, v95
	v_exp_f32_e32 v55, v55
	s_nop 0
	v_add_f32_e32 v55, 1.0, v55
	v_rcp_f32_e32 v101, v55
	s_nop 0
	v_pk_mul_f32 v[26:27], v[26:27], v[100:101]
	s_nop 0
	v_pk_fma_f32 v[94:95], v[26:27], v[26:27], v[98:99]
	v_mul_f32_e32 v96, v27, v27
	v_pk_add_f32 v[94:95], v[96:97], v[94:95] op_sel_hi:[0,1]
	v_mov_b32_e32 v55, v94
	s_nop 1
	v_permlane16_swap_b32_e32 v94, v55
	v_add_f32_e32 v55, v94, v55
	v_mov_b32_e32 v75, v55
	s_nop 1
	v_permlane32_swap_b32_e32 v55, v75
	s_and_saveexec_b64 s[0:1], s[42:43]
	v_readlane_b32 s72, v254, 1
	v_readlane_b32 s70, v254, 2
	v_readlane_b32 s71, v254, 3
	v_readlane_b32 s73, v254, 4
	s_mov_b32 s75, 0x8000
	s_mov_b32 s78, 0x200000
	s_mov_b32 s79, 0x7ffff
	v_add_f32_e32 v55, v55, v75
	ds_write_b32 v32, v55 offset:128
	s_or_b64 exec, exec, s[0:1]
	s_waitcnt vmcnt(3)
	v_lshlrev_b32_e32 v96, 16, v90
	v_mul_f32_e32 v55, 0xbfb8aa3b, v96
	v_exp_f32_e32 v55, v55
	v_and_b32_e32 v97, 0xffff0000, v90
	v_lshlrev_b32_e32 v90, 16, v91
	s_waitcnt lgkmcnt(0)
	v_lshlrev_b32_e32 v94, 16, v92
	v_add_f32_e32 v55, 1.0, v55
	v_rcp_f32_e32 v98, v55
	v_mul_f32_e32 v55, 0xbfb8aa3b, v97
	v_exp_f32_e32 v55, v55
	v_and_b32_e32 v95, 0xffff0000, v92
	v_pk_fma_f32 v[12:13], v[70:71], v[94:95], v[12:13]
	v_and_b32_e32 v91, 0xffff0000, v91
	v_add_f32_e32 v55, 1.0, v55
	v_rcp_f32_e32 v99, v55
	v_mul_f32_e32 v55, 0xbfb8aa3b, v90
	v_exp_f32_e32 v55, v55
	v_pk_mul_f32 v[12:13], v[12:13], v[96:97]
	v_lshlrev_b32_e32 v92, 16, v93
	v_and_b32_e32 v93, 0xffff0000, v93
	v_add_f32_e32 v55, 1.0, v55
	v_rcp_f32_e32 v96, v55
	v_mul_f32_e32 v55, 0xbfb8aa3b, v91
	v_exp_f32_e32 v55, v55
	v_pk_mul_f32 v[94:95], v[12:13], v[98:99]
	v_pk_fma_f32 v[14:15], v[70:71], v[92:93], v[14:15]
	v_mul_f32_e32 v12, v95, v95
	v_add_f32_e32 v55, 1.0, v55
	v_rcp_f32_e32 v97, v55
	v_pk_mul_f32 v[14:15], v[14:15], v[90:91]
	v_pk_fma_f32 v[12:13], v[94:95], v[94:95], v[12:13] op_sel_hi:[1,1,0]
	s_waitcnt vmcnt(2)
	v_lshlrev_b32_e32 v92, 16, v86
	v_pk_mul_f32 v[90:91], v[14:15], v[96:97]
	v_and_b32_e32 v93, 0xffff0000, v86
	v_pk_fma_f32 v[12:13], v[90:91], v[90:91], v[12:13]
	v_mul_f32_e32 v14, v91, v91
	v_pk_add_f32 v[12:13], v[14:15], v[12:13] op_sel_hi:[0,1]
	v_lshlrev_b32_e32 v14, 16, v88
	v_and_b32_e32 v15, 0xffff0000, v88
	v_mul_f32_e32 v55, 0xbfb8aa3b, v92
	v_pk_fma_f32 v[4:5], v[70:71], v[14:15], v[4:5]
	v_mul_f32_e32 v14, 0xbfb8aa3b, v93
	v_exp_f32_e32 v55, v55
	v_exp_f32_e32 v14, v14
	v_pk_mul_f32 v[4:5], v[4:5], v[92:93]
	v_and_b32_e32 v15, 0xffff0000, v87
	v_add_f32_e32 v55, 1.0, v55
	v_add_f32_e32 v14, 1.0, v14
	v_rcp_f32_e32 v96, v55
	v_rcp_f32_e32 v97, v14
	v_lshlrev_b32_e32 v14, 16, v87
	v_mul_f32_e32 v55, 0xbfb8aa3b, v14
	v_exp_f32_e32 v55, v55
	v_pk_mul_f32 v[92:93], v[4:5], v[96:97]
	v_add_f32_e32 v55, 1.0, v55
	v_pk_fma_f32 v[4:5], v[92:93], v[92:93], v[12:13]
	v_mul_f32_e32 v12, v93, v93
	v_pk_add_f32 v[4:5], v[12:13], v[4:5] op_sel_hi:[0,1]
	v_lshlrev_b32_e32 v12, 16, v89
	v_and_b32_e32 v13, 0xffff0000, v89
	v_pk_fma_f32 v[6:7], v[70:71], v[12:13], v[6:7]
	v_mul_f32_e32 v12, 0xbfb8aa3b, v15
	v_exp_f32_e32 v12, v12
	v_rcp_f32_e32 v86, v55
	v_pk_mul_f32 v[6:7], v[6:7], v[14:15]
	s_waitcnt vmcnt(1)
	v_and_b32_e32 v13, 0xffff0000, v82
	v_add_f32_e32 v12, 1.0, v12
	v_rcp_f32_e32 v87, v12
	v_lshlrev_b32_e32 v12, 16, v82
	v_mul_f32_e32 v14, 0xbfb8aa3b, v12
	v_exp_f32_e32 v14, v14
	v_pk_mul_f32 v[86:87], v[6:7], v[86:87]
	v_add_f32_e32 v14, 1.0, v14
	v_pk_fma_f32 v[4:5], v[86:87], v[86:87], v[4:5]
	v_mul_f32_e32 v6, v87, v87
	v_pk_add_f32 v[4:5], v[6:7], v[4:5] op_sel_hi:[0,1]
	v_lshlrev_b32_e32 v6, 16, v84
	v_and_b32_e32 v7, 0xffff0000, v84
	v_pk_fma_f32 v[0:1], v[70:71], v[6:7], v[0:1]
	v_mul_f32_e32 v6, 0xbfb8aa3b, v13
	v_exp_f32_e32 v6, v6
	v_rcp_f32_e32 v14, v14
	v_pk_mul_f32 v[0:1], v[0:1], v[12:13]
	v_and_b32_e32 v7, 0xffff0000, v83
	v_add_f32_e32 v6, 1.0, v6
	v_rcp_f32_e32 v15, v6
	v_lshlrev_b32_e32 v6, 16, v83
	v_mul_f32_e32 v12, 0xbfb8aa3b, v6
	v_exp_f32_e32 v12, v12
	v_pk_mul_f32 v[88:89], v[0:1], v[14:15]
	v_add_f32_e32 v12, 1.0, v12
	v_pk_fma_f32 v[0:1], v[88:89], v[88:89], v[4:5]
	v_mul_f32_e32 v4, v89, v89
	v_pk_add_f32 v[0:1], v[4:5], v[0:1] op_sel_hi:[0,1]
	v_lshlrev_b32_e32 v4, 16, v85
	v_and_b32_e32 v5, 0xffff0000, v85
	v_pk_fma_f32 v[2:3], v[70:71], v[4:5], v[2:3]
	v_mul_f32_e32 v4, 0xbfb8aa3b, v7
	v_exp_f32_e32 v4, v4
	v_rcp_f32_e32 v12, v12
	v_pk_mul_f32 v[2:3], v[2:3], v[6:7]
	s_waitcnt vmcnt(0)
	v_and_b32_e32 v5, 0xffff0000, v78
	v_add_f32_e32 v4, 1.0, v4
	v_rcp_f32_e32 v13, v4
	v_lshlrev_b32_e32 v4, 16, v78
	v_mul_f32_e32 v6, 0xbfb8aa3b, v4
	v_exp_f32_e32 v6, v6
	v_pk_mul_f32 v[82:83], v[2:3], v[12:13]
	v_add_f32_e32 v6, 1.0, v6
	v_pk_fma_f32 v[0:1], v[82:83], v[82:83], v[0:1]
	v_mul_f32_e32 v2, v83, v83
	v_pk_add_f32 v[0:1], v[2:3], v[0:1] op_sel_hi:[0,1]
	v_lshlrev_b32_e32 v2, 16, v80
	v_and_b32_e32 v3, 0xffff0000, v80
	v_pk_fma_f32 v[2:3], v[70:71], v[2:3], v[8:9]
	v_rcp_f32_e32 v6, v6
	v_pk_mul_f32 v[2:3], v[2:3], v[4:5]
	v_mul_f32_e32 v4, 0xbfb8aa3b, v5
	v_exp_f32_e32 v4, v4
	v_and_b32_e32 v5, 0xffff0000, v79
	v_add_f32_e32 v4, 1.0, v4
	v_rcp_f32_e32 v7, v4
	v_lshlrev_b32_e32 v4, 16, v79
	v_pk_mul_f32 v[84:85], v[2:3], v[6:7]
	s_nop 0
	v_pk_fma_f32 v[0:1], v[84:85], v[84:85], v[0:1]
	v_mul_f32_e32 v2, v85, v85
	v_pk_add_f32 v[0:1], v[2:3], v[0:1] op_sel_hi:[0,1]
	v_lshlrev_b32_e32 v2, 16, v81
	v_and_b32_e32 v3, 0xffff0000, v81
	v_pk_fma_f32 v[2:3], v[70:71], v[2:3], v[10:11]
	v_mul_f32_e32 v6, 0xbfb8aa3b, v4
	v_pk_mul_f32 v[2:3], v[2:3], v[4:5]
	v_mul_f32_e32 v4, 0xbfb8aa3b, v5
	v_exp_f32_e32 v6, v6
	v_exp_f32_e32 v4, v4
	v_add_f32_e32 v6, 1.0, v6
	v_add_f32_e32 v4, 1.0, v4
	v_rcp_f32_e32 v6, v6
	v_rcp_f32_e32 v7, v4
	s_nop 0
	v_pk_mul_f32 v[70:71], v[2:3], v[6:7]
	s_nop 0
	v_pk_fma_f32 v[0:1], v[70:71], v[70:71], v[0:1]
	v_mul_f32_e32 v2, v71, v71
	v_pk_add_f32 v[0:1], v[2:3], v[0:1] op_sel_hi:[0,1]
	v_mov_b32_e32 v1, v0
	s_nop 1
	v_permlane16_swap_b32_e32 v0, v1
	v_add_f32_e32 v0, v0, v1
	v_mov_b32_e32 v1, v0
	s_nop 1
	v_permlane32_swap_b32_e32 v0, v1
	s_and_saveexec_b64 s[0:1], s[42:43]
	s_cbranch_execz .LBB0_1267
	v_add_f32_e32 v0, v0, v1
	ds_write_b32 v32, v0 offset:192
	s_branch .LBB0_1267
